# attention unit epilogue: row sum-of-squares butterflies on the VALU (DPP quad_perm/row_half_mirror/row_ror:8 + v_permlane16_swap) instead of five ds_swizzle round trips per row
# baseline (speedup 1.0000x reference)
.LBB0_549:
	s_andn2_b64 vcc, exec, s[28:29]
	s_waitcnt lgkmcnt(0)
	s_barrier
	s_cbranch_vccnz .LBB0_528
	ds_read2_b32 v[80:81], v185 offset1:1
	ds_read2_b32 v[82:83], v185 offset0:8 offset1:9
	ds_read2_b32 v[86:87], v185 offset0:10 offset1:11
	ds_read2_b32 v[84:85], v185 offset0:16 offset1:17
	ds_read2_b32 v[94:95], v186 offset1:1
	s_waitcnt lgkmcnt(4)
	v_div_scale_f32 v88, s[16:17], v80, v80, 1.0
	v_rcp_f32_e32 v90, v88
	v_div_scale_f32 v89, vcc, 1.0, v80, 1.0
	ds_read2st64_b32 v[122:123], v187 offset1:1
	v_fma_f32 v91, -v88, v90, 1.0
	v_fmac_f32_e32 v90, v91, v90
	v_mul_f32_e32 v91, v89, v90
	v_fma_f32 v92, -v88, v91, v89
	v_fmac_f32_e32 v91, v92, v90
	v_fma_f32 v92, -v88, v91, v89
	ds_read2_b32 v[88:89], v185 offset0:26 offset1:27
	s_waitcnt lgkmcnt(2)
	v_div_scale_f32 v93, s[16:17], v94, v94, v129
	v_rcp_f32_e32 v96, v93
	v_div_fmas_f32 v90, v92, v90, v91
	v_div_fixup_f32 v80, v90, v80, 1.0
	v_lshl_add_u64 v[196:197], s[36:37], 0, v[134:135]
	v_fma_f32 v90, -v93, v96, 1.0
	v_fmac_f32_e32 v96, v90, v96
	v_div_scale_f32 v90, vcc, v129, v94, v129
	v_mul_f32_e32 v91, v90, v96
	v_fma_f32 v92, -v93, v91, v90
	v_fmac_f32_e32 v91, v92, v96
	v_fma_f32 v90, -v93, v91, v90
	v_div_fmas_f32 v90, v90, v96, v91
	ds_read2st64_b32 v[112:113], v187 offset0:2 offset1:3
	ds_read2st64_b32 v[104:105], v187 offset0:4 offset1:5
	ds_read2st64_b32 v[96:97], v187 offset0:6 offset1:7
	ds_read2st64_b32 v[124:125], v187 offset0:16 offset1:17
	ds_read2st64_b32 v[114:115], v187 offset0:18 offset1:19
	ds_read2st64_b32 v[106:107], v187 offset0:20 offset1:21
	ds_read2st64_b32 v[98:99], v187 offset0:22 offset1:23
	ds_read2st64_b32 v[126:127], v187 offset0:32 offset1:33
	v_div_fixup_f32 v90, v90, v94, v129
	ds_read2st64_b32 v[116:117], v187 offset0:34 offset1:35
	ds_read2st64_b32 v[108:109], v187 offset0:36 offset1:37
	ds_read2st64_b32 v[100:101], v187 offset0:38 offset1:39
	ds_read2st64_b32 v[194:195], v187 offset0:48 offset1:49
	s_waitcnt lgkmcnt(13)
	v_mul_f32_e32 v91, v90, v122
	v_fma_f32 v64, v64, v80, -v91
	s_waitcnt lgkmcnt(8)
	v_mul_f32_e32 v91, v90, v124
	v_fma_f32 v48, v48, v80, -v91
	v_mul_f32_e32 v91, v48, v48
	s_waitcnt lgkmcnt(4)
	v_mul_f32_e32 v92, v90, v126
	v_fmac_f32_e32 v91, v64, v64
	v_fma_f32 v122, v32, v80, -v92
	s_waitcnt lgkmcnt(0)
	v_mul_f32_e32 v32, v90, v194
	v_fmac_f32_e32 v91, v122, v122
	v_fma_f32 v124, v16, v80, -v32
	v_fmac_f32_e32 v91, v124, v124
	s_nop 1
	v_mov_b32_dpp v16, v91 quad_perm:[1,0,3,2] row_mask:0xf bank_mask:0xf
	ds_read2st64_b32 v[118:119], v187 offset0:50 offset1:51
	ds_read2st64_b32 v[110:111], v187 offset0:52 offset1:53
	ds_read2st64_b32 v[102:103], v187 offset0:54 offset1:55
	global_load_dword v80, v[136:137], off
	global_load_dword v94, v[136:137], off offset:128
	v_lshlrev_b64 v[196:197], 12, v[196:197]
	s_waitcnt lgkmcnt(3)
	v_add_f32_e32 v16, v91, v16
	s_nop 1
	v_mov_b32_dpp v32, v16 quad_perm:[2,3,0,1] row_mask:0xf bank_mask:0xf
	v_lshl_add_u64 v[196:197], s[18:19], 0, v[196:197]
	s_waitcnt lgkmcnt(0)
	v_add_f32_e32 v16, v16, v32
	s_nop 1
	v_mov_b32_dpp v32, v16 row_half_mirror row_mask:0xf bank_mask:0xf
	s_waitcnt lgkmcnt(0)
	v_add_f32_e32 v16, v16, v32
	s_nop 1
	v_mov_b32_dpp v32, v16 row_ror:8 row_mask:0xf bank_mask:0xf
	s_waitcnt lgkmcnt(0)
	v_add_f32_e32 v16, v16, v32
	v_mov_b32_e32 v32, v16
	s_nop 1
	v_permlane16_swap_b32_e32 v16, v32
	s_waitcnt lgkmcnt(0)
	v_add_f32_e32 v16, v16, v32
	v_fmamk_f32 v16, v16, 0x3c000000, v190
	v_mul_f32_e32 v32, 0x4f800000, v16
	v_cmp_gt_f32_e32 vcc, s71, v16
	s_nop 1
	v_cndmask_b32_e32 v16, v16, v32, vcc
	v_sqrt_f32_e32 v32, v16
	s_nop 0
	v_add_u32_e32 v90, -1, v32
	v_fma_f32 v91, -v90, v32, v16
	v_cmp_ge_f32_e64 s[16:17], 0, v91
	v_add_u32_e32 v91, 1, v32
	s_nop 0
	v_cndmask_b32_e64 v90, v32, v90, s[16:17]
	v_fma_f32 v32, -v91, v32, v16
	v_cmp_lt_f32_e64 s[16:17], 0, v32
	s_nop 1
	v_cndmask_b32_e64 v32, v90, v91, s[16:17]
	v_mul_f32_e32 v90, 0x37800000, v32
	v_cndmask_b32_e32 v32, v32, v90, vcc
	v_cmp_class_f32_e32 vcc, v16, v191
	ds_read2_b32 v[92:93], v185 offset0:18 offset1:19
	ds_read2_b32 v[90:91], v185 offset0:24 offset1:25
	v_cndmask_b32_e32 v16, v32, v16, vcc
	v_div_scale_f32 v32, s[16:17], v16, v16, s72
	v_rcp_f32_e32 v121, v32
	v_div_scale_f32 v126, vcc, s72, v16, s72
	v_fma_f32 v120, -v32, v121, 1.0
	v_fmac_f32_e32 v121, v120, v121
	global_load_dword v120, v[136:137], off offset:256
	v_mul_f32_e32 v130, v126, v121
	v_fma_f32 v193, -v32, v130, v126
	v_fmac_f32_e32 v130, v193, v121
	v_fma_f32 v32, -v32, v130, v126
	v_div_fmas_f32 v32, v32, v121, v130
	global_load_dword v121, v[136:137], off offset:384
	v_div_fixup_f32 v126, v32, v16, s72
	v_div_scale_f32 v16, s[16:17], v81, v81, 1.0
	v_rcp_f32_e32 v32, v16
	v_mul_f32_e32 v64, v64, v126
	v_fma_f32 v130, -v16, v32, 1.0
	v_fmac_f32_e32 v32, v130, v32
	v_div_scale_f32 v130, vcc, 1.0, v81, 1.0
	v_mul_f32_e32 v193, v130, v32
	v_fma_f32 v194, -v16, v193, v130
	v_fmac_f32_e32 v193, v194, v32
	v_fma_f32 v16, -v16, v193, v130
	v_div_scale_f32 v130, s[16:17], v95, v95, v129
	v_rcp_f32_e32 v194, v130
	v_div_fmas_f32 v16, v16, v32, v193
	v_div_fixup_f32 v16, v16, v81, 1.0
	s_waitcnt vmcnt(3)
	v_mul_f32_e32 v64, v80, v64
	v_fma_f32 v32, -v130, v194, 1.0
	v_fmac_f32_e32 v194, v32, v194
	v_div_scale_f32 v32, vcc, v129, v95, v129
	v_mul_f32_e32 v81, v32, v194
	v_fma_f32 v193, -v130, v81, v32
	v_fmac_f32_e32 v81, v193, v194
	v_fma_f32 v32, -v130, v81, v32
	v_div_fmas_f32 v32, v32, v194, v81
	v_div_fixup_f32 v32, v32, v95, v129
	v_mul_f32_e32 v81, v32, v123
	v_fma_f32 v81, v65, v16, -v81
	v_mul_f32_e32 v65, v32, v125
	v_fma_f32 v95, v49, v16, -v65
	v_mul_f32_e32 v49, v95, v95
	v_mul_f32_e32 v65, v32, v127
	v_fmac_f32_e32 v49, v81, v81
	v_fma_f32 v123, v33, v16, -v65
	v_mul_f32_e32 v32, v32, v195
	v_fmac_f32_e32 v49, v123, v123
	v_fma_f32 v125, v17, v16, -v32
	v_fmac_f32_e32 v49, v125, v125
	s_nop 1
	v_mov_b32_dpp v65, v49 quad_perm:[1,0,3,2] row_mask:0xf bank_mask:0xf
	v_lshl_add_u64 v[16:17], v[196:197], 0, s[38:39]
	v_lshlrev_b32_e32 v130, 1, v128
	v_lshl_add_u64 v[16:17], v[16:17], 0, v[130:131]
	v_lshl_add_u64 v[32:33], v[16:17], 0, s[30:31]
	s_waitcnt lgkmcnt(0)
	v_add_f32_e32 v49, v49, v65
	s_nop 1
	v_mov_b32_dpp v65, v49 quad_perm:[2,3,0,1] row_mask:0xf bank_mask:0xf
	v_bfe_u32 v127, v64, 16, 1
	v_add_co_u32_e32 v16, vcc, s74, v16
	v_add3_u32 v64, v64, v127, s73
	s_waitcnt lgkmcnt(0)
	v_add_f32_e32 v49, v49, v65
	s_nop 1
	v_mov_b32_dpp v65, v49 row_half_mirror row_mask:0xf bank_mask:0xf
	v_addc_co_u32_e32 v17, vcc, 0, v17, vcc
	global_store_short_d16_hi v[16:17], v64, off offset:1024
	v_mul_f32_e32 v16, v48, v126
	s_waitcnt lgkmcnt(0)
	v_add_f32_e32 v17, v49, v65
	s_nop 1
	v_mov_b32_dpp v48, v17 row_ror:8 row_mask:0xf bank_mask:0xf
	s_waitcnt vmcnt(3)
	v_mul_f32_e32 v16, v94, v16
	v_bfe_u32 v49, v16, 16, 1
	v_add3_u32 v16, v16, v49, s73
	global_store_short_d16_hi v[32:33], v16, off offset:64
	s_waitcnt lgkmcnt(0)
	v_add_f32_e32 v16, v17, v48
	v_mov_b32_e32 v17, v16
	s_nop 1
	v_permlane16_swap_b32_e32 v16, v17
	v_mul_f32_e32 v48, v122, v126
	s_waitcnt lgkmcnt(0)
	v_add_f32_e32 v16, v16, v17
	v_fmamk_f32 v16, v16, 0x3c000000, v190
	v_mul_f32_e32 v17, 0x4f800000, v16
	v_cmp_gt_f32_e32 vcc, s71, v16
	s_waitcnt vmcnt(3)
	v_mul_f32_e32 v48, v120, v48
	v_bfe_u32 v49, v48, 16, 1
	v_cndmask_b32_e32 v16, v16, v17, vcc
	v_sqrt_f32_e32 v17, v16
	v_add3_u32 v48, v48, v49, s73
	global_store_short_d16_hi v[32:33], v48, off offset:128
	v_mul_f32_e32 v48, v124, v126
	v_add_u32_e32 v49, -1, v17
	v_fma_f32 v64, -v49, v17, v16
	v_cmp_ge_f32_e64 s[16:17], 0, v64
	v_add_u32_e32 v64, 1, v17
	s_waitcnt vmcnt(3)
	v_mul_f32_e32 v48, v121, v48
	v_cndmask_b32_e64 v49, v17, v49, s[16:17]
	v_fma_f32 v17, -v64, v17, v16
	v_cmp_lt_f32_e64 s[16:17], 0, v17
	s_nop 1
	v_cndmask_b32_e64 v17, v49, v64, s[16:17]
	v_mul_f32_e32 v49, 0x37800000, v17
	v_cndmask_b32_e32 v17, v17, v49, vcc
	v_cmp_class_f32_e32 vcc, v16, v191
	s_nop 1
	v_cndmask_b32_e32 v49, v17, v16, vcc
	v_div_scale_f32 v16, s[16:17], v49, v49, s72
	v_rcp_f32_e32 v64, v16
	v_bfe_u32 v17, v48, 16, 1
	v_add3_u32 v17, v48, v17, s73
	global_store_short_d16_hi v[32:33], v17, off offset:192
	v_fma_f32 v17, -v16, v64, 1.0
	v_fmac_f32_e32 v64, v17, v64
	v_div_scale_f32 v17, vcc, s72, v49, s72
	v_mul_f32_e32 v32, v17, v64
	v_fma_f32 v33, -v16, v32, v17
	v_fmac_f32_e32 v32, v33, v64
	v_fma_f32 v33, -v16, v32, v17
	ds_read2_b32 v[16:17], v188 offset1:1
	v_div_fmas_f32 v48, v33, v64, v32
	ds_read2_b32 v[32:33], v189 offset1:1
	v_div_fixup_f32 v122, v48, v49, s72
	v_lshl_add_u64 v[48:49], s[36:37], 0, v[138:139]
	s_waitcnt lgkmcnt(1)
	v_div_scale_f32 v64, s[16:17], v16, v16, 1.0
	v_rcp_f32_e32 v65, v64
	v_lshlrev_b64 v[48:49], 12, v[48:49]
	v_lshl_add_u64 v[48:49], s[18:19], 0, v[48:49]
	v_lshl_add_u64 v[48:49], v[48:49], 0, s[38:39]
	v_fma_f32 v124, -v64, v65, 1.0
	v_fmac_f32_e32 v65, v124, v65
	v_div_scale_f32 v124, vcc, 1.0, v16, 1.0
	v_mul_f32_e32 v126, v124, v65
	v_fma_f32 v127, -v64, v126, v124
	v_fmac_f32_e32 v126, v127, v65
	v_fma_f32 v64, -v64, v126, v124
	s_waitcnt lgkmcnt(0)
	v_div_scale_f32 v124, s[16:17], v32, v32, v129
	v_rcp_f32_e32 v127, v124
	v_div_fmas_f32 v64, v64, v65, v126
	v_div_fixup_f32 v16, v64, v16, 1.0
	v_mul_f32_e32 v81, v81, v122
	v_fma_f32 v64, -v124, v127, 1.0
	v_fmac_f32_e32 v127, v64, v127
	v_div_scale_f32 v64, vcc, v129, v32, v129
	v_mul_f32_e32 v65, v64, v127
	v_fma_f32 v126, -v124, v65, v64
	v_fmac_f32_e32 v65, v126, v127
	v_fma_f32 v64, -v124, v65, v64
	v_div_fmas_f32 v64, v64, v127, v65
	v_div_fixup_f32 v32, v64, v32, v129
	v_mul_f32_e32 v64, v32, v112
	v_fma_f32 v66, v66, v16, -v64
	v_mul_f32_e32 v64, v32, v114
	v_fma_f32 v50, v50, v16, -v64
	v_mul_f32_e32 v112, v50, v50
	v_mul_f32_e32 v64, v32, v116
	v_fmac_f32_e32 v112, v66, v66
	v_fma_f32 v34, v34, v16, -v64
	v_mul_f32_e32 v32, v32, v118
	v_fmac_f32_e32 v112, v34, v34
	v_fma_f32 v32, v18, v16, -v32
	v_fmac_f32_e32 v112, v32, v32
	s_nop 1
	v_mov_b32_dpp v16, v112 quad_perm:[1,0,3,2] row_mask:0xf bank_mask:0xf
	v_lshl_add_u64 v[48:49], v[48:49], 0, v[130:131]
	v_mul_f32_e32 v81, v80, v81
	v_lshl_add_u64 v[64:65], v[48:49], 0, s[30:31]
	v_add_co_u32_e32 v48, vcc, s74, v48
	s_waitcnt lgkmcnt(0)
	v_add_f32_e32 v16, v112, v16
	s_nop 1
	v_mov_b32_dpp v18, v16 quad_perm:[2,3,0,1] row_mask:0xf bank_mask:0xf
	v_bfe_u32 v112, v81, 16, 1
	v_add3_u32 v81, v81, v112, s73
	v_addc_co_u32_e32 v49, vcc, 0, v49, vcc
	s_waitcnt lgkmcnt(0)
	v_add_f32_e32 v16, v16, v18
	s_nop 1
	v_mov_b32_dpp v18, v16 row_half_mirror row_mask:0xf bank_mask:0xf
	global_store_short_d16_hi v[48:49], v81, off offset:1024
	v_mul_f32_e32 v48, v95, v122
	v_mul_f32_e32 v48, v94, v48
	v_bfe_u32 v49, v48, 16, 1
	s_waitcnt lgkmcnt(0)
	v_add_f32_e32 v16, v16, v18
	s_nop 1
	v_mov_b32_dpp v18, v16 row_ror:8 row_mask:0xf bank_mask:0xf
	v_add3_u32 v48, v48, v49, s73
	global_store_short_d16_hi v[64:65], v48, off offset:64
	v_mul_f32_e32 v48, v123, v122
	v_mul_f32_e32 v48, v120, v48
	s_waitcnt lgkmcnt(0)
	v_add_f32_e32 v16, v16, v18
	v_mov_b32_e32 v18, v16
	s_nop 1
	v_permlane16_swap_b32_e32 v16, v18
	v_bfe_u32 v49, v48, 16, 1
	v_add3_u32 v48, v48, v49, s73
	global_store_short_d16_hi v[64:65], v48, off offset:128
	v_mul_f32_e32 v48, v125, v122
	s_waitcnt lgkmcnt(0)
	v_add_f32_e32 v16, v16, v18
	v_fmamk_f32 v16, v16, 0x3c000000, v190
	v_mul_f32_e32 v18, 0x4f800000, v16
	v_cmp_gt_f32_e32 vcc, s71, v16
	v_mul_f32_e32 v48, v121, v48
	s_nop 0
	v_cndmask_b32_e32 v16, v16, v18, vcc
	v_sqrt_f32_e32 v18, v16
	s_nop 0
	v_add_u32_e32 v49, -1, v18
	v_fma_f32 v81, -v49, v18, v16
	v_cmp_ge_f32_e64 s[16:17], 0, v81
	v_add_u32_e32 v81, 1, v18
	s_nop 0
	v_cndmask_b32_e64 v49, v18, v49, s[16:17]
	v_fma_f32 v18, -v81, v18, v16
	v_cmp_lt_f32_e64 s[16:17], 0, v18
	s_nop 1
	v_cndmask_b32_e64 v18, v49, v81, s[16:17]
	v_mul_f32_e32 v49, 0x37800000, v18
	v_cndmask_b32_e32 v18, v18, v49, vcc
	v_cmp_class_f32_e32 vcc, v16, v191
	v_bfe_u32 v81, v48, 16, 1
	v_add3_u32 v48, v48, v81, s73
	v_cndmask_b32_e32 v16, v18, v16, vcc
	v_div_scale_f32 v18, s[16:17], v16, v16, s72
	v_rcp_f32_e32 v49, v18
	global_store_short_d16_hi v[64:65], v48, off offset:192
	v_fma_f32 v48, -v18, v49, 1.0
	v_fmac_f32_e32 v49, v48, v49
	v_div_scale_f32 v48, vcc, s72, v16, s72
	v_mul_f32_e32 v64, v48, v49
	v_fma_f32 v65, -v18, v64, v48
	v_fmac_f32_e32 v64, v65, v49
	v_fma_f32 v18, -v18, v64, v48
	v_div_fmas_f32 v18, v18, v49, v64
	v_div_scale_f32 v64, s[16:17], v17, v17, 1.0
	v_rcp_f32_e32 v65, v64
	v_div_fixup_f32 v81, v18, v16, s72
	v_lshl_add_u64 v[48:49], s[36:37], 0, v[140:141]
	v_lshlrev_b64 v[48:49], 12, v[48:49]
	v_fma_f32 v16, -v64, v65, 1.0
	v_fmac_f32_e32 v65, v16, v65
	v_div_scale_f32 v16, vcc, 1.0, v17, 1.0
	v_mul_f32_e32 v18, v16, v65
	v_fma_f32 v95, -v64, v18, v16
	v_fmac_f32_e32 v18, v95, v65
	v_fma_f32 v16, -v64, v18, v16
	v_div_scale_f32 v64, s[16:17], v33, v33, v129
	v_rcp_f32_e32 v95, v64
	v_div_fmas_f32 v16, v16, v65, v18
	v_div_fixup_f32 v16, v16, v17, 1.0
	v_mul_f32_e32 v32, v32, v81
	v_fma_f32 v17, -v64, v95, 1.0
	v_fmac_f32_e32 v95, v17, v95
	v_div_scale_f32 v17, vcc, v129, v33, v129
	v_mul_f32_e32 v18, v17, v95
	v_fma_f32 v65, -v64, v18, v17
	v_fmac_f32_e32 v18, v65, v95
	v_fma_f32 v17, -v64, v18, v17
	v_div_fmas_f32 v17, v17, v95, v18
	v_div_fixup_f32 v17, v17, v33, v129
	v_mul_f32_e32 v18, v17, v113
	v_fma_f32 v64, v67, v16, -v18
	v_mul_f32_e32 v18, v17, v115
	v_fma_f32 v65, v51, v16, -v18
	v_mul_f32_e32 v33, v65, v65
	v_mul_f32_e32 v18, v17, v117
	v_fmac_f32_e32 v33, v64, v64
	v_fma_f32 v67, v35, v16, -v18
	v_mul_f32_e32 v17, v17, v119
	v_fmac_f32_e32 v33, v67, v67
	v_fma_f32 v95, v19, v16, -v17
	v_fmac_f32_e32 v33, v95, v95
	s_nop 1
	v_mov_b32_dpp v35, v33 quad_perm:[1,0,3,2] row_mask:0xf bank_mask:0xf
	v_lshl_add_u64 v[16:17], s[18:19], 0, v[48:49]
	v_lshl_add_u64 v[16:17], v[16:17], 0, s[38:39]
	v_mul_f32_e32 v48, v66, v81
	v_lshl_add_u64 v[16:17], v[16:17], 0, v[130:131]
	s_waitcnt lgkmcnt(0)
	v_add_f32_e32 v33, v33, v35
	s_nop 1
	v_mov_b32_dpp v35, v33 quad_perm:[2,3,0,1] row_mask:0xf bank_mask:0xf
	v_mul_f32_e32 v48, v80, v48
	v_lshl_add_u64 v[18:19], v[16:17], 0, s[30:31]
	v_bfe_u32 v49, v48, 16, 1
	v_add_co_u32_e32 v16, vcc, s74, v16
	s_waitcnt lgkmcnt(0)
	v_add_f32_e32 v33, v33, v35
	s_nop 1
	v_mov_b32_dpp v35, v33 row_half_mirror row_mask:0xf bank_mask:0xf
	v_add3_u32 v48, v48, v49, s73
	v_addc_co_u32_e32 v17, vcc, 0, v17, vcc
	global_store_short_d16_hi v[16:17], v48, off offset:1024
	s_waitcnt lgkmcnt(0)
	v_add_f32_e32 v17, v33, v35
	s_nop 1
	v_mov_b32_dpp v33, v17 row_ror:8 row_mask:0xf bank_mask:0xf
	v_mul_f32_e32 v16, v50, v81
	v_mul_f32_e32 v16, v94, v16
	v_bfe_u32 v35, v16, 16, 1
	v_add3_u32 v16, v16, v35, s73
	global_store_short_d16_hi v[18:19], v16, off offset:64
	s_waitcnt lgkmcnt(0)
	v_add_f32_e32 v16, v17, v33
	v_mov_b32_e32 v17, v16
	s_nop 1
	v_permlane16_swap_b32_e32 v16, v17
	v_mul_f32_e32 v33, v34, v81
	v_mul_f32_e32 v33, v120, v33
	v_bfe_u32 v34, v33, 16, 1
	v_add3_u32 v33, v33, v34, s73
	s_waitcnt lgkmcnt(0)
	v_add_f32_e32 v16, v16, v17
	v_fmamk_f32 v16, v16, 0x3c000000, v190
	v_mul_f32_e32 v17, 0x4f800000, v16
	v_cmp_gt_f32_e32 vcc, s71, v16
	global_store_short_d16_hi v[18:19], v33, off offset:128
	v_mul_f32_e32 v32, v121, v32
	v_cndmask_b32_e32 v16, v16, v17, vcc
	v_sqrt_f32_e32 v17, v16
	s_nop 0
	v_add_u32_e32 v33, -1, v17
	v_fma_f32 v34, -v33, v17, v16
	v_cmp_ge_f32_e64 s[16:17], 0, v34
	v_add_u32_e32 v34, 1, v17
	s_nop 0
	v_cndmask_b32_e64 v33, v17, v33, s[16:17]
	v_fma_f32 v17, -v34, v17, v16
	v_cmp_lt_f32_e64 s[16:17], 0, v17
	s_nop 1
	v_cndmask_b32_e64 v17, v33, v34, s[16:17]
	v_mul_f32_e32 v33, 0x37800000, v17
	v_cndmask_b32_e32 v17, v17, v33, vcc
	v_cmp_class_f32_e32 vcc, v16, v191
	v_bfe_u32 v34, v32, 16, 1
	v_add3_u32 v32, v32, v34, s73
	v_cndmask_b32_e32 v16, v17, v16, vcc
	v_div_scale_f32 v17, s[16:17], v16, v16, s72
	v_rcp_f32_e32 v33, v17
	global_store_short_d16_hi v[18:19], v32, off offset:192
	v_fma_f32 v18, -v17, v33, 1.0
	v_fmac_f32_e32 v33, v18, v33
	v_div_scale_f32 v18, vcc, s72, v16, s72
	v_mul_f32_e32 v19, v18, v33
	v_fma_f32 v32, -v17, v19, v18
	v_fmac_f32_e32 v19, v32, v33
	v_fma_f32 v17, -v17, v19, v18
	v_div_scale_f32 v18, s[16:17], v82, v82, 1.0
	v_rcp_f32_e32 v50, v18
	v_div_fmas_f32 v17, v17, v33, v19
	v_div_fixup_f32 v66, v17, v16, s72
	v_lshl_add_u64 v[16:17], s[36:37], 0, v[142:143]
	v_lshlrev_b64 v[32:33], 12, v[16:17]
	v_fma_f32 v16, -v18, v50, 1.0
	v_fmac_f32_e32 v50, v16, v50
	v_div_scale_f32 v16, vcc, 1.0, v82, 1.0
	v_mul_f32_e32 v51, v16, v50
	v_fma_f32 v17, -v18, v51, v16
	v_fmac_f32_e32 v51, v17, v50
	v_fma_f32 v81, -v18, v51, v16
	ds_read2_b32 v[48:49], v186 offset0:8 offset1:9
	ds_read2_b32 v[18:19], v186 offset0:10 offset1:11
	ds_read2_b32 v[34:35], v186 offset0:16 offset1:17
	ds_read2_b32 v[16:17], v186 offset0:18 offset1:19
	v_div_fmas_f32 v50, v81, v50, v51
	s_waitcnt lgkmcnt(3)
	v_div_scale_f32 v112, s[16:17], v48, v48, v129
	v_rcp_f32_e32 v113, v112
	v_div_fixup_f32 v50, v50, v82, 1.0
	v_lshl_add_u64 v[32:33], s[18:19], 0, v[32:33]
	v_lshl_add_u64 v[32:33], v[32:33], 0, s[38:39]
	v_fma_f32 v51, -v112, v113, 1.0
	v_fmac_f32_e32 v113, v51, v113
	v_div_scale_f32 v51, vcc, v129, v48, v129
	v_mul_f32_e32 v81, v51, v113
	v_fma_f32 v82, -v112, v81, v51
	v_fmac_f32_e32 v81, v82, v113
	v_fma_f32 v51, -v112, v81, v51
	v_div_fmas_f32 v51, v51, v113, v81
	v_div_fixup_f32 v48, v51, v48, v129
	v_mul_f32_e32 v51, v48, v104
	v_fma_f32 v68, v68, v50, -v51
	v_mul_f32_e32 v51, v48, v106
	v_fma_f32 v52, v52, v50, -v51
	v_mul_f32_e32 v81, v52, v52
	v_mul_f32_e32 v51, v48, v108
	v_fmac_f32_e32 v81, v68, v68
	v_fma_f32 v36, v36, v50, -v51
	v_mul_f32_e32 v48, v48, v110
	v_fmac_f32_e32 v81, v36, v36
	v_fma_f32 v48, v20, v50, -v48
	v_fmac_f32_e32 v81, v48, v48
	s_nop 1
	v_mov_b32_dpp v20, v81 quad_perm:[1,0,3,2] row_mask:0xf bank_mask:0xf
	v_mul_f32_e32 v64, v64, v66
	v_lshl_add_u64 v[32:33], v[32:33], 0, v[130:131]
	v_mul_f32_e32 v64, v80, v64
	v_lshl_add_u64 v[50:51], v[32:33], 0, s[30:31]
	s_waitcnt lgkmcnt(0)
	v_add_f32_e32 v20, v81, v20
	s_nop 1
	v_mov_b32_dpp v81, v20 quad_perm:[2,3,0,1] row_mask:0xf bank_mask:0xf
	v_bfe_u32 v82, v64, 16, 1
	v_add_co_u32_e32 v32, vcc, s74, v32
	v_add3_u32 v64, v64, v82, s73
	s_waitcnt lgkmcnt(0)
	v_add_f32_e32 v20, v20, v81
	s_nop 1
	v_mov_b32_dpp v81, v20 row_half_mirror row_mask:0xf bank_mask:0xf
	v_addc_co_u32_e32 v33, vcc, 0, v33, vcc
	global_store_short_d16_hi v[32:33], v64, off offset:1024
	v_mul_f32_e32 v32, v65, v66
	s_waitcnt lgkmcnt(0)
	v_add_f32_e32 v20, v20, v81
	s_nop 1
	v_mov_b32_dpp v33, v20 row_ror:8 row_mask:0xf bank_mask:0xf
	v_mul_f32_e32 v32, v94, v32
	v_bfe_u32 v64, v32, 16, 1
	v_add3_u32 v32, v32, v64, s73
	global_store_short_d16_hi v[50:51], v32, off offset:64
	s_waitcnt lgkmcnt(0)
	v_add_f32_e32 v20, v20, v33
	v_mov_b32_e32 v32, v20
	s_nop 1
	v_permlane16_swap_b32_e32 v20, v32
	v_mul_f32_e32 v33, v67, v66
	v_mul_f32_e32 v33, v120, v33
	v_bfe_u32 v64, v33, 16, 1
	v_add3_u32 v33, v33, v64, s73
	s_waitcnt lgkmcnt(0)
	v_add_f32_e32 v20, v20, v32
	v_fmamk_f32 v20, v20, 0x3c000000, v190
	v_mul_f32_e32 v32, 0x4f800000, v20
	v_cmp_gt_f32_e32 vcc, s71, v20
	global_store_short_d16_hi v[50:51], v33, off offset:128
	v_mul_f32_e32 v33, v95, v66
	v_cndmask_b32_e32 v20, v20, v32, vcc
	v_sqrt_f32_e32 v32, v20
	v_mul_f32_e32 v33, v121, v33
	v_add_u32_e32 v64, -1, v32
	v_fma_f32 v65, -v64, v32, v20
	v_cmp_ge_f32_e64 s[16:17], 0, v65
	v_add_u32_e32 v65, 1, v32
	s_nop 0
	v_cndmask_b32_e64 v64, v32, v64, s[16:17]
	v_fma_f32 v32, -v65, v32, v20
	v_cmp_lt_f32_e64 s[16:17], 0, v32
	s_nop 1
	v_cndmask_b32_e64 v32, v64, v65, s[16:17]
	v_mul_f32_e32 v64, 0x37800000, v32
	v_cndmask_b32_e32 v32, v32, v64, vcc
	v_cmp_class_f32_e32 vcc, v20, v191
	v_bfe_u32 v65, v33, 16, 1
	v_add3_u32 v33, v33, v65, s73
	v_cndmask_b32_e32 v20, v32, v20, vcc
	v_div_scale_f32 v32, s[16:17], v20, v20, s72
	v_rcp_f32_e32 v64, v32
	global_store_short_d16_hi v[50:51], v33, off offset:192
	v_fma_f32 v33, -v32, v64, 1.0
	v_fmac_f32_e32 v64, v33, v64
	v_div_scale_f32 v33, vcc, s72, v20, s72
	v_mul_f32_e32 v50, v33, v64
	v_fma_f32 v51, -v32, v50, v33
	v_fmac_f32_e32 v50, v51, v64
	v_fma_f32 v32, -v32, v50, v33
	v_div_fmas_f32 v32, v32, v64, v50
	v_div_scale_f32 v50, s[16:17], v83, v83, 1.0
	v_rcp_f32_e32 v51, v50
	v_div_fixup_f32 v64, v32, v20, s72
	v_lshl_add_u64 v[32:33], s[36:37], 0, v[144:145]
	v_lshlrev_b64 v[32:33], 12, v[32:33]
	v_fma_f32 v20, -v50, v51, 1.0
	v_fmac_f32_e32 v51, v20, v51
	v_div_scale_f32 v20, vcc, 1.0, v83, 1.0
	v_mul_f32_e32 v65, v20, v51
	v_fma_f32 v66, -v50, v65, v20
	v_fmac_f32_e32 v65, v66, v51
	v_fma_f32 v20, -v50, v65, v20
	v_div_scale_f32 v50, s[16:17], v49, v49, v129
	v_rcp_f32_e32 v66, v50
	v_div_fmas_f32 v20, v20, v51, v65
	v_div_fixup_f32 v20, v20, v83, 1.0
	v_mul_f32_e32 v36, v36, v64
	v_fma_f32 v51, -v50, v66, 1.0
	v_fmac_f32_e32 v66, v51, v66
	v_div_scale_f32 v51, vcc, v129, v49, v129
	v_mul_f32_e32 v65, v51, v66
	v_fma_f32 v67, -v50, v65, v51
	v_fmac_f32_e32 v65, v67, v66
	v_fma_f32 v50, -v50, v65, v51
	v_div_fmas_f32 v50, v50, v66, v65
	v_div_fixup_f32 v49, v50, v49, v129
	v_mul_f32_e32 v51, v49, v107
	v_mul_f32_e32 v50, v49, v105
	v_fma_f32 v51, v53, v20, -v51
	v_fma_f32 v50, v69, v20, -v50
	v_mul_f32_e32 v53, v51, v51
	v_mul_f32_e32 v65, v49, v109
	v_fmac_f32_e32 v53, v50, v50
	v_fma_f32 v37, v37, v20, -v65
	v_mul_f32_e32 v49, v49, v111
	v_fmac_f32_e32 v53, v37, v37
	v_fma_f32 v49, v21, v20, -v49
	v_fmac_f32_e32 v53, v49, v49
	s_nop 1
	v_mov_b32_dpp v65, v53 quad_perm:[1,0,3,2] row_mask:0xf bank_mask:0xf
	v_lshl_add_u64 v[20:21], s[18:19], 0, v[32:33]
	v_lshl_add_u64 v[20:21], v[20:21], 0, s[38:39]
	v_mul_f32_e32 v66, v68, v64
	v_lshl_add_u64 v[20:21], v[20:21], 0, v[130:131]
	s_waitcnt lgkmcnt(0)
	v_add_f32_e32 v53, v53, v65
	s_nop 1
	v_mov_b32_dpp v65, v53 quad_perm:[2,3,0,1] row_mask:0xf bank_mask:0xf
	v_mul_f32_e32 v66, v80, v66
	v_lshl_add_u64 v[32:33], v[20:21], 0, s[30:31]
	v_bfe_u32 v67, v66, 16, 1
	v_add_co_u32_e32 v20, vcc, s74, v20
	s_waitcnt lgkmcnt(0)
	v_add_f32_e32 v53, v53, v65
	s_nop 1
	v_mov_b32_dpp v65, v53 row_half_mirror row_mask:0xf bank_mask:0xf
	v_add3_u32 v66, v66, v67, s73
	v_addc_co_u32_e32 v21, vcc, 0, v21, vcc
	global_store_short_d16_hi v[20:21], v66, off offset:1024
	s_waitcnt lgkmcnt(0)
	v_add_f32_e32 v21, v53, v65
	v_mul_f32_e32 v20, v52, v64
	s_nop 1
	v_mov_b32_dpp v52, v21 row_ror:8 row_mask:0xf bank_mask:0xf
	v_mul_f32_e32 v20, v94, v20
	v_bfe_u32 v53, v20, 16, 1
	v_add3_u32 v20, v20, v53, s73
	global_store_short_d16_hi v[32:33], v20, off offset:64
	s_waitcnt lgkmcnt(0)
	v_add_f32_e32 v20, v21, v52
	v_mov_b32_e32 v21, v20
	s_nop 1
	v_permlane16_swap_b32_e32 v20, v21
	v_mul_f32_e32 v36, v120, v36
	v_bfe_u32 v52, v36, 16, 1
	v_add3_u32 v36, v36, v52, s73
	global_store_short_d16_hi v[32:33], v36, off offset:128
	s_waitcnt lgkmcnt(0)
	v_add_f32_e32 v20, v20, v21
	v_fmamk_f32 v20, v20, 0x3c000000, v190
	v_mul_f32_e32 v21, 0x4f800000, v20
	v_cmp_gt_f32_e32 vcc, s71, v20
	v_mul_f32_e32 v36, v48, v64
	v_mul_f32_e32 v36, v121, v36
	v_cndmask_b32_e32 v20, v20, v21, vcc
	v_sqrt_f32_e32 v21, v20
	s_nop 0
	v_add_u32_e32 v48, -1, v21
	v_fma_f32 v52, -v48, v21, v20
	v_cmp_ge_f32_e64 s[16:17], 0, v52
	v_add_u32_e32 v52, 1, v21
	s_nop 0
	v_cndmask_b32_e64 v48, v21, v48, s[16:17]
	v_fma_f32 v21, -v52, v21, v20
	v_cmp_lt_f32_e64 s[16:17], 0, v21
	s_nop 1
	v_cndmask_b32_e64 v21, v48, v52, s[16:17]
	v_mul_f32_e32 v48, 0x37800000, v21
	v_cndmask_b32_e32 v21, v21, v48, vcc
	v_cmp_class_f32_e32 vcc, v20, v191
	v_bfe_u32 v52, v36, 16, 1
	v_add3_u32 v36, v36, v52, s73
	v_cndmask_b32_e32 v20, v21, v20, vcc
	v_div_scale_f32 v21, s[16:17], v20, v20, s72
	v_rcp_f32_e32 v48, v21
	global_store_short_d16_hi v[32:33], v36, off offset:192
	v_fma_f32 v32, -v21, v48, 1.0
	v_fmac_f32_e32 v48, v32, v48
	v_div_scale_f32 v32, vcc, s72, v20, s72
	v_mul_f32_e32 v33, v32, v48
	v_fma_f32 v36, -v21, v33, v32
	v_fmac_f32_e32 v33, v36, v48
	v_fma_f32 v21, -v21, v33, v32
	v_div_scale_f32 v32, s[16:17], v86, v86, 1.0
	v_div_fmas_f32 v21, v21, v48, v33
	v_rcp_f32_e32 v33, v32
	v_div_fixup_f32 v36, v21, v20, s72
	v_lshl_add_u64 v[20:21], s[36:37], 0, v[146:147]
	v_lshlrev_b64 v[20:21], 12, v[20:21]
	v_fma_f32 v48, -v32, v33, 1.0
	v_fmac_f32_e32 v33, v48, v33
	v_div_scale_f32 v48, vcc, 1.0, v86, 1.0
	v_mul_f32_e32 v52, v48, v33
	v_fma_f32 v53, -v32, v52, v48
	v_fmac_f32_e32 v52, v53, v33
	v_fma_f32 v32, -v32, v52, v48
	v_div_scale_f32 v48, s[16:17], v18, v18, v129
	v_rcp_f32_e32 v53, v48
	v_div_fmas_f32 v32, v32, v33, v52
	v_div_fixup_f32 v32, v32, v86, 1.0
	v_lshl_add_u64 v[20:21], s[18:19], 0, v[20:21]
	v_fma_f32 v33, -v48, v53, 1.0
	v_fmac_f32_e32 v53, v33, v53
	v_div_scale_f32 v33, vcc, v129, v18, v129
	v_mul_f32_e32 v52, v33, v53
	v_fma_f32 v64, -v48, v52, v33
	v_fmac_f32_e32 v52, v64, v53
	v_fma_f32 v33, -v48, v52, v33
	v_div_fmas_f32 v33, v33, v53, v52
	v_div_fixup_f32 v18, v33, v18, v129
	v_mul_f32_e32 v33, v18, v96
	v_fma_f32 v48, v70, v32, -v33
	v_mul_f32_e32 v33, v18, v98
	v_fma_f32 v52, v54, v32, -v33
	v_mul_f32_e32 v53, v52, v52
	v_mul_f32_e32 v33, v18, v100
	v_fmac_f32_e32 v53, v48, v48
	v_fma_f32 v38, v38, v32, -v33
	v_mul_f32_e32 v18, v18, v102
	v_fmac_f32_e32 v53, v38, v38
	v_fma_f32 v22, v22, v32, -v18
	v_fmac_f32_e32 v53, v22, v22
	s_nop 1
	v_mov_b32_dpp v18, v53 quad_perm:[1,0,3,2] row_mask:0xf bank_mask:0xf
	v_lshl_add_u64 v[20:21], v[20:21], 0, s[38:39]
	v_mul_f32_e32 v50, v50, v36
	v_lshl_add_u64 v[20:21], v[20:21], 0, v[130:131]
	v_mul_f32_e32 v50, v80, v50
	s_waitcnt lgkmcnt(0)
	v_add_f32_e32 v18, v53, v18
	s_nop 1
	v_mov_b32_dpp v53, v18 quad_perm:[2,3,0,1] row_mask:0xf bank_mask:0xf
	v_lshl_add_u64 v[32:33], v[20:21], 0, s[30:31]
	v_bfe_u32 v54, v50, 16, 1
	v_add_co_u32_e32 v20, vcc, s74, v20
	s_waitcnt lgkmcnt(0)
	v_add_f32_e32 v18, v18, v53
	s_nop 1
	v_mov_b32_dpp v53, v18 row_half_mirror row_mask:0xf bank_mask:0xf
	v_add3_u32 v50, v50, v54, s73
	v_addc_co_u32_e32 v21, vcc, 0, v21, vcc
	global_store_short_d16_hi v[20:21], v50, off offset:1024
	s_waitcnt lgkmcnt(0)
	v_add_f32_e32 v18, v18, v53
	s_nop 1
	v_mov_b32_dpp v21, v18 row_ror:8 row_mask:0xf bank_mask:0xf
	v_mul_f32_e32 v20, v51, v36
	v_mul_f32_e32 v20, v94, v20
	v_bfe_u32 v50, v20, 16, 1
	v_add3_u32 v20, v20, v50, s73
	s_waitcnt lgkmcnt(0)
	v_add_f32_e32 v18, v18, v21
	global_store_short_d16_hi v[32:33], v20, off offset:64
	v_mov_b32_e32 v20, v18
	s_nop 1
	v_permlane16_swap_b32_e32 v18, v20
	v_mul_f32_e32 v21, v37, v36
	v_mul_f32_e32 v21, v120, v21
	v_bfe_u32 v37, v21, 16, 1
	v_add3_u32 v21, v21, v37, s73
	s_waitcnt lgkmcnt(0)
	v_add_f32_e32 v18, v18, v20
	v_fmamk_f32 v18, v18, 0x3c000000, v190
	v_mul_f32_e32 v20, 0x4f800000, v18
	v_cmp_gt_f32_e32 vcc, s71, v18
	global_store_short_d16_hi v[32:33], v21, off offset:128
	v_mul_f32_e32 v21, v49, v36
	v_cndmask_b32_e32 v18, v18, v20, vcc
	v_sqrt_f32_e32 v20, v18
	v_mul_f32_e32 v21, v121, v21
	v_add_u32_e32 v36, -1, v20
	v_fma_f32 v37, -v36, v20, v18
	v_cmp_ge_f32_e64 s[16:17], 0, v37
	v_add_u32_e32 v37, 1, v20
	s_nop 0
	v_cndmask_b32_e64 v36, v20, v36, s[16:17]
	v_fma_f32 v20, -v37, v20, v18
	v_cmp_lt_f32_e64 s[16:17], 0, v20
	s_nop 1
	v_cndmask_b32_e64 v20, v36, v37, s[16:17]
	v_mul_f32_e32 v36, 0x37800000, v20
	v_cndmask_b32_e32 v20, v20, v36, vcc
	v_cmp_class_f32_e32 vcc, v18, v191
	v_bfe_u32 v37, v21, 16, 1
	v_add3_u32 v21, v21, v37, s73
	v_cndmask_b32_e32 v18, v20, v18, vcc
	v_div_scale_f32 v20, s[16:17], v18, v18, s72
	v_rcp_f32_e32 v36, v20
	global_store_short_d16_hi v[32:33], v21, off offset:192
	v_fma_f32 v21, -v20, v36, 1.0
	v_fmac_f32_e32 v36, v21, v36
	v_div_scale_f32 v21, vcc, s72, v18, s72
	v_mul_f32_e32 v32, v21, v36
	v_fma_f32 v33, -v20, v32, v21
	v_fmac_f32_e32 v32, v33, v36
	v_fma_f32 v20, -v20, v32, v21
	v_div_fmas_f32 v20, v20, v36, v32
	v_div_scale_f32 v32, s[16:17], v87, v87, 1.0
	v_rcp_f32_e32 v33, v32
	v_div_fixup_f32 v36, v20, v18, s72
	v_lshl_add_u64 v[20:21], s[36:37], 0, v[148:149]
	v_lshlrev_b64 v[20:21], 12, v[20:21]
	v_fma_f32 v18, -v32, v33, 1.0
	v_fmac_f32_e32 v33, v18, v33
	v_div_scale_f32 v18, vcc, 1.0, v87, 1.0
	v_mul_f32_e32 v37, v18, v33
	v_fma_f32 v49, -v32, v37, v18
	v_fmac_f32_e32 v37, v49, v33
	v_fma_f32 v18, -v32, v37, v18
	v_div_scale_f32 v32, s[16:17], v19, v19, v129
	v_rcp_f32_e32 v49, v32
	v_div_fmas_f32 v18, v18, v33, v37
	v_div_fixup_f32 v18, v18, v87, 1.0
	v_mul_f32_e32 v22, v22, v36
	v_fma_f32 v33, -v32, v49, 1.0
	v_fmac_f32_e32 v49, v33, v49
	v_div_scale_f32 v33, vcc, v129, v19, v129
	v_mul_f32_e32 v37, v33, v49
	v_fma_f32 v50, -v32, v37, v33
	v_fmac_f32_e32 v37, v50, v49
	v_fma_f32 v32, -v32, v37, v33
	v_div_fmas_f32 v32, v32, v49, v37
	v_div_fixup_f32 v19, v32, v19, v129
	v_mul_f32_e32 v32, v19, v97
	v_fma_f32 v81, v71, v18, -v32
	v_mul_f32_e32 v32, v19, v99
	v_fma_f32 v95, v55, v18, -v32
	v_mul_f32_e32 v32, v95, v95
	v_mul_f32_e32 v33, v19, v101
	v_fmac_f32_e32 v32, v81, v81
	v_fma_f32 v100, v39, v18, -v33
	v_mul_f32_e32 v19, v19, v103
	v_fmac_f32_e32 v32, v100, v100
	v_fma_f32 v101, v23, v18, -v19
	v_fmac_f32_e32 v32, v101, v101
	s_nop 1
	v_mov_b32_dpp v23, v32 quad_perm:[1,0,3,2] row_mask:0xf bank_mask:0xf
	v_lshl_add_u64 v[18:19], s[18:19], 0, v[20:21]
	v_lshl_add_u64 v[18:19], v[18:19], 0, s[38:39]
	v_mul_f32_e32 v33, v48, v36
	v_lshl_add_u64 v[18:19], v[18:19], 0, v[130:131]
	s_waitcnt lgkmcnt(0)
	v_add_f32_e32 v23, v32, v23
	s_nop 1
	v_mov_b32_dpp v32, v23 quad_perm:[2,3,0,1] row_mask:0xf bank_mask:0xf
	v_mul_f32_e32 v33, v80, v33
	v_lshl_add_u64 v[20:21], v[18:19], 0, s[30:31]
	v_bfe_u32 v37, v33, 16, 1
	v_add_co_u32_e32 v18, vcc, s74, v18
	s_waitcnt lgkmcnt(0)
	v_add_f32_e32 v23, v23, v32
	s_nop 1
	v_mov_b32_dpp v32, v23 row_half_mirror row_mask:0xf bank_mask:0xf
	v_add3_u32 v33, v33, v37, s73
	v_addc_co_u32_e32 v19, vcc, 0, v19, vcc
	global_store_short_d16_hi v[18:19], v33, off offset:1024
	s_waitcnt lgkmcnt(0)
	v_add_f32_e32 v19, v23, v32
	s_nop 1
	v_mov_b32_dpp v23, v19 row_ror:8 row_mask:0xf bank_mask:0xf
	v_mul_f32_e32 v18, v52, v36
	v_mul_f32_e32 v18, v94, v18
	v_bfe_u32 v32, v18, 16, 1
	v_add3_u32 v18, v18, v32, s73
	global_store_short_d16_hi v[20:21], v18, off offset:64
	s_waitcnt lgkmcnt(0)
	v_add_f32_e32 v18, v19, v23
	v_mov_b32_e32 v19, v18
	s_nop 1
	v_permlane16_swap_b32_e32 v18, v19
	v_mul_f32_e32 v23, v38, v36
	v_mul_f32_e32 v23, v120, v23
	v_bfe_u32 v32, v23, 16, 1
	v_add3_u32 v23, v23, v32, s73
	s_waitcnt lgkmcnt(0)
	v_add_f32_e32 v18, v18, v19
	v_fmamk_f32 v18, v18, 0x3c000000, v190
	v_mul_f32_e32 v19, 0x4f800000, v18
	v_cmp_gt_f32_e32 vcc, s71, v18
	global_store_short_d16_hi v[20:21], v23, off offset:128
	v_mul_f32_e32 v22, v121, v22
	v_cndmask_b32_e32 v18, v18, v19, vcc
	v_sqrt_f32_e32 v19, v18
	ds_read2st64_b32 v[70:71], v187 offset0:8 offset1:9
	v_add_u32_e32 v23, -1, v19
	v_fma_f32 v32, -v23, v19, v18
	v_cmp_ge_f32_e64 s[16:17], 0, v32
	v_add_u32_e32 v32, 1, v19
	s_nop 0
	v_cndmask_b32_e64 v23, v19, v23, s[16:17]
	v_fma_f32 v19, -v32, v19, v18
	v_cmp_lt_f32_e64 s[16:17], 0, v19
	s_nop 1
	v_cndmask_b32_e64 v19, v23, v32, s[16:17]
	v_mul_f32_e32 v23, 0x37800000, v19
	v_cndmask_b32_e32 v19, v19, v23, vcc
	v_cmp_class_f32_e32 vcc, v18, v191
	v_bfe_u32 v32, v22, 16, 1
	v_add3_u32 v22, v22, v32, s73
	v_cndmask_b32_e32 v18, v19, v18, vcc
	v_div_scale_f32 v19, s[16:17], v18, v18, s72
	v_rcp_f32_e32 v23, v19
	global_store_short_d16_hi v[20:21], v22, off offset:192
	v_fma_f32 v20, -v19, v23, 1.0
	v_fmac_f32_e32 v23, v20, v23
	v_div_scale_f32 v20, vcc, s72, v18, s72
	v_mul_f32_e32 v21, v20, v23
	v_fma_f32 v22, -v19, v21, v20
	v_fmac_f32_e32 v21, v22, v23
	v_fma_f32 v19, -v19, v21, v20
	v_div_scale_f32 v20, s[16:17], v84, v84, 1.0
	v_div_fmas_f32 v19, v19, v23, v21
	v_rcp_f32_e32 v21, v20
	v_div_fixup_f32 v102, v19, v18, s72
	v_lshl_add_u64 v[18:19], s[36:37], 0, v[150:151]
	v_lshlrev_b64 v[68:69], 12, v[18:19]
	v_fma_f32 v18, -v20, v21, 1.0
	v_fmac_f32_e32 v21, v18, v21
	v_div_scale_f32 v18, vcc, 1.0, v84, 1.0
	v_mul_f32_e32 v19, v18, v21
	v_fma_f32 v22, -v20, v19, v18
	v_fmac_f32_e32 v19, v22, v21
	v_fma_f32 v18, -v20, v19, v18
	v_div_scale_f32 v20, s[16:17], v34, v34, v129
	v_rcp_f32_e32 v22, v20
	v_div_fmas_f32 v18, v18, v21, v19
	v_div_fixup_f32 v84, v18, v84, 1.0
	v_lshl_add_u64 v[68:69], s[18:19], 0, v[68:69]
	v_fma_f32 v18, -v20, v22, 1.0
	v_fmac_f32_e32 v22, v18, v22
	v_div_scale_f32 v18, vcc, v129, v34, v129
	v_mul_f32_e32 v19, v18, v22
	v_fma_f32 v21, -v20, v19, v18
	v_fmac_f32_e32 v19, v21, v22
	v_fma_f32 v18, -v20, v19, v18
	v_div_fmas_f32 v18, v18, v22, v19
	v_div_fixup_f32 v34, v18, v34, v129
	ds_read2st64_b32 v[52:53], v187 offset0:10 offset1:11
	ds_read2st64_b32 v[36:37], v187 offset0:12 offset1:13
	ds_read2st64_b32 v[18:19], v187 offset0:14 offset1:15
	ds_read2st64_b32 v[82:83], v187 offset0:24 offset1:25
	s_waitcnt lgkmcnt(4)
	v_mul_f32_e32 v20, v34, v70
	v_fma_f32 v70, v72, v84, -v20
	ds_read2st64_b32 v[54:55], v187 offset0:26 offset1:27
	ds_read2st64_b32 v[38:39], v187 offset0:28 offset1:29
	ds_read2st64_b32 v[20:21], v187 offset0:30 offset1:31
	ds_read2st64_b32 v[86:87], v187 offset0:40 offset1:41
	s_waitcnt lgkmcnt(4)
	v_mul_f32_e32 v22, v34, v82
	v_fma_f32 v56, v56, v84, -v22
	ds_read2st64_b32 v[64:65], v187 offset0:42 offset1:43
	ds_read2st64_b32 v[48:49], v187 offset0:44 offset1:45
	ds_read2st64_b32 v[22:23], v187 offset0:46 offset1:47
	ds_read2st64_b32 v[96:97], v187 offset0:56 offset1:57
	v_mul_f32_e32 v72, v56, v56
	s_waitcnt lgkmcnt(4)
	v_mul_f32_e32 v32, v34, v86
	v_fmac_f32_e32 v72, v70, v70
	v_fma_f32 v40, v40, v84, -v32
	s_waitcnt lgkmcnt(0)
	v_mul_f32_e32 v34, v34, v96
	v_fmac_f32_e32 v72, v40, v40
	v_fma_f32 v82, v24, v84, -v34
	v_fmac_f32_e32 v72, v82, v82
	s_nop 1
	v_mov_b32_dpp v24, v72 quad_perm:[1,0,3,2] row_mask:0xf bank_mask:0xf
	v_lshl_add_u64 v[68:69], v[68:69], 0, s[38:39]
	v_lshl_add_u64 v[68:69], v[68:69], 0, v[130:131]
	v_lshl_add_u64 v[98:99], v[68:69], 0, s[30:31]
	v_add_co_u32_e32 v68, vcc, s74, v68
	s_waitcnt lgkmcnt(0)
	v_add_f32_e32 v24, v72, v24
	s_nop 1
	v_mov_b32_dpp v34, v24 quad_perm:[2,3,0,1] row_mask:0xf bank_mask:0xf
	v_mul_f32_e32 v72, v81, v102
	v_mul_f32_e32 v72, v80, v72
	v_bfe_u32 v81, v72, 16, 1
	v_add3_u32 v72, v72, v81, s73
	s_waitcnt lgkmcnt(0)
	v_add_f32_e32 v24, v24, v34
	s_nop 1
	v_mov_b32_dpp v34, v24 row_half_mirror row_mask:0xf bank_mask:0xf
	v_addc_co_u32_e32 v69, vcc, 0, v69, vcc
	ds_read2st64_b32 v[66:67], v187 offset0:58 offset1:59
	ds_read2st64_b32 v[50:51], v187 offset0:60 offset1:61
	ds_read2st64_b32 v[32:33], v187 offset0:62 offset1:63
	global_store_short_d16_hi v[68:69], v72, off offset:1024
	s_waitcnt lgkmcnt(3)
	v_add_f32_e32 v24, v24, v34
	s_nop 1
	v_mov_b32_dpp v34, v24 row_ror:8 row_mask:0xf bank_mask:0xf
	v_mul_f32_e32 v68, v95, v102
	v_mul_f32_e32 v68, v94, v68
	v_bfe_u32 v69, v68, 16, 1
	v_add3_u32 v68, v68, v69, s73
	s_waitcnt lgkmcnt(0)
	v_add_f32_e32 v24, v24, v34
	v_mov_b32_e32 v34, v24
	s_nop 1
	v_permlane16_swap_b32_e32 v24, v34
	global_store_short_d16_hi v[98:99], v68, off offset:64
	v_mul_f32_e32 v68, v100, v102
	v_mul_f32_e32 v68, v120, v68
	v_bfe_u32 v69, v68, 16, 1
	s_waitcnt lgkmcnt(0)
	v_add_f32_e32 v24, v24, v34
	v_fmamk_f32 v24, v24, 0x3c000000, v190
	v_mul_f32_e32 v34, 0x4f800000, v24
	v_cmp_gt_f32_e32 vcc, s71, v24
	v_add3_u32 v68, v68, v69, s73
	global_store_short_d16_hi v[98:99], v68, off offset:128
	v_cndmask_b32_e32 v24, v24, v34, vcc
	v_sqrt_f32_e32 v34, v24
	v_mul_f32_e32 v68, v101, v102
	v_mul_f32_e32 v68, v121, v68
	v_add_u32_e32 v69, -1, v34
	v_fma_f32 v72, -v69, v34, v24
	v_cmp_ge_f32_e64 s[16:17], 0, v72
	v_add_u32_e32 v72, 1, v34
	s_nop 0
	v_cndmask_b32_e64 v69, v34, v69, s[16:17]
	v_fma_f32 v34, -v72, v34, v24
	v_cmp_lt_f32_e64 s[16:17], 0, v34
	s_nop 1
	v_cndmask_b32_e64 v34, v69, v72, s[16:17]
	v_mul_f32_e32 v69, 0x37800000, v34
	v_cndmask_b32_e32 v34, v34, v69, vcc
	v_cmp_class_f32_e32 vcc, v24, v191
	v_bfe_u32 v72, v68, 16, 1
	v_add3_u32 v68, v68, v72, s73
	v_cndmask_b32_e32 v24, v34, v24, vcc
	v_div_scale_f32 v34, s[16:17], v24, v24, s72
	v_rcp_f32_e32 v69, v34
	global_store_short_d16_hi v[98:99], v68, off offset:192
	v_fma_f32 v68, -v34, v69, 1.0
	v_fmac_f32_e32 v69, v68, v69
	v_div_scale_f32 v68, vcc, s72, v24, s72
	v_mul_f32_e32 v72, v68, v69
	v_fma_f32 v81, -v34, v72, v68
	v_fmac_f32_e32 v72, v81, v69
	v_fma_f32 v34, -v34, v72, v68
	v_div_fmas_f32 v34, v34, v69, v72
	v_div_scale_f32 v72, s[16:17], v85, v85, 1.0
	v_rcp_f32_e32 v81, v72
	v_div_fixup_f32 v84, v34, v24, s72
	v_lshl_add_u64 v[68:69], s[36:37], 0, v[152:153]
	v_lshlrev_b64 v[68:69], 12, v[68:69]
	v_fma_f32 v24, -v72, v81, 1.0
	v_fmac_f32_e32 v81, v24, v81
	v_div_scale_f32 v24, vcc, 1.0, v85, 1.0
	v_mul_f32_e32 v34, v24, v81
	v_fma_f32 v86, -v72, v34, v24
	v_fmac_f32_e32 v34, v86, v81
	v_fma_f32 v24, -v72, v34, v24
	v_div_scale_f32 v72, s[16:17], v35, v35, v129
	v_rcp_f32_e32 v86, v72
	v_div_fmas_f32 v24, v24, v81, v34
	v_div_fixup_f32 v24, v24, v85, 1.0
	v_mul_f32_e32 v70, v70, v84
	v_fma_f32 v34, -v72, v86, 1.0
	v_fmac_f32_e32 v86, v34, v86
	v_div_scale_f32 v34, vcc, v129, v35, v129
	v_mul_f32_e32 v81, v34, v86
	v_fma_f32 v85, -v72, v81, v34
	v_fmac_f32_e32 v81, v85, v86
	v_fma_f32 v34, -v72, v81, v34
	v_div_fmas_f32 v34, v34, v86, v81
	v_div_fixup_f32 v34, v34, v35, v129
	v_mul_f32_e32 v35, v34, v71
	v_fma_f32 v71, v73, v24, -v35
	v_mul_f32_e32 v35, v34, v83
	v_fma_f32 v57, v57, v24, -v35
	v_mul_f32_e32 v72, v57, v57
	v_mul_f32_e32 v35, v34, v87
	v_fmac_f32_e32 v72, v71, v71
	v_fma_f32 v41, v41, v24, -v35
	v_mul_f32_e32 v34, v34, v97
	v_fmac_f32_e32 v72, v41, v41
	v_fma_f32 v73, v25, v24, -v34
	v_fmac_f32_e32 v72, v73, v73
	s_nop 1
	v_mov_b32_dpp v81, v72 quad_perm:[1,0,3,2] row_mask:0xf bank_mask:0xf
	v_lshl_add_u64 v[24:25], s[18:19], 0, v[68:69]
	v_lshl_add_u64 v[24:25], v[24:25], 0, s[38:39]
	v_lshl_add_u64 v[24:25], v[24:25], 0, v[130:131]
	v_mul_f32_e32 v70, v80, v70
	s_waitcnt lgkmcnt(0)
	v_add_f32_e32 v68, v72, v81
	s_nop 1
	v_mov_b32_dpp v69, v68 quad_perm:[2,3,0,1] row_mask:0xf bank_mask:0xf
	v_lshl_add_u64 v[34:35], v[24:25], 0, s[30:31]
	v_bfe_u32 v72, v70, 16, 1
	v_add_co_u32_e32 v24, vcc, s74, v24
	s_waitcnt lgkmcnt(0)
	v_add_f32_e32 v68, v68, v69
	s_nop 1
	v_mov_b32_dpp v69, v68 row_half_mirror row_mask:0xf bank_mask:0xf
	v_add3_u32 v70, v70, v72, s73
	v_addc_co_u32_e32 v25, vcc, 0, v25, vcc
	global_store_short_d16_hi v[24:25], v70, off offset:1024
	s_waitcnt lgkmcnt(0)
	v_add_f32_e32 v25, v68, v69
	v_mul_f32_e32 v24, v56, v84
	s_nop 1
	v_mov_b32_dpp v56, v25 row_ror:8 row_mask:0xf bank_mask:0xf
	v_mul_f32_e32 v24, v94, v24
	v_bfe_u32 v68, v24, 16, 1
	v_add3_u32 v24, v24, v68, s73
	global_store_short_d16_hi v[34:35], v24, off offset:64
	s_waitcnt lgkmcnt(0)
	v_add_f32_e32 v24, v25, v56
	v_mov_b32_e32 v25, v24
	s_nop 1
	v_permlane16_swap_b32_e32 v24, v25
	v_mul_f32_e32 v40, v40, v84
	v_mul_f32_e32 v40, v120, v40
	v_bfe_u32 v56, v40, 16, 1
	v_add3_u32 v40, v40, v56, s73
	s_waitcnt lgkmcnt(0)
	v_add_f32_e32 v24, v24, v25
	v_fmamk_f32 v24, v24, 0x3c000000, v190
	v_mul_f32_e32 v25, 0x4f800000, v24
	v_cmp_gt_f32_e32 vcc, s71, v24
	global_store_short_d16_hi v[34:35], v40, off offset:128
	v_mul_f32_e32 v40, v82, v84
	v_cndmask_b32_e32 v24, v24, v25, vcc
	v_sqrt_f32_e32 v25, v24
	v_mul_f32_e32 v40, v121, v40
	v_add_u32_e32 v56, -1, v25
	v_fma_f32 v68, -v56, v25, v24
	v_cmp_ge_f32_e64 s[16:17], 0, v68
	v_add_u32_e32 v68, 1, v25
	s_nop 0
	v_cndmask_b32_e64 v56, v25, v56, s[16:17]
	v_fma_f32 v25, -v68, v25, v24
	v_cmp_lt_f32_e64 s[16:17], 0, v25
	s_nop 1
	v_cndmask_b32_e64 v25, v56, v68, s[16:17]
	v_mul_f32_e32 v56, 0x37800000, v25
	v_cndmask_b32_e32 v25, v25, v56, vcc
	v_cmp_class_f32_e32 vcc, v24, v191
	v_bfe_u32 v68, v40, 16, 1
	v_add3_u32 v40, v40, v68, s73
	v_cndmask_b32_e32 v24, v25, v24, vcc
	v_div_scale_f32 v25, s[16:17], v24, v24, s72
	v_rcp_f32_e32 v56, v25
	global_store_short_d16_hi v[34:35], v40, off offset:192
	v_fma_f32 v34, -v25, v56, 1.0
	v_fmac_f32_e32 v56, v34, v56
	v_div_scale_f32 v34, vcc, s72, v24, s72
	v_mul_f32_e32 v35, v34, v56
	v_fma_f32 v40, -v25, v35, v34
	v_fmac_f32_e32 v35, v40, v56
	v_fma_f32 v25, -v25, v35, v34
	v_div_scale_f32 v34, s[16:17], v92, v92, 1.0
	v_div_fmas_f32 v25, v25, v56, v35
	v_rcp_f32_e32 v35, v34
	v_div_fixup_f32 v40, v25, v24, s72
	v_lshl_add_u64 v[24:25], s[36:37], 0, v[154:155]
	v_lshlrev_b64 v[24:25], 12, v[24:25]
	v_fma_f32 v56, -v34, v35, 1.0
	v_fmac_f32_e32 v35, v56, v35
	v_div_scale_f32 v56, vcc, 1.0, v92, 1.0
	v_mul_f32_e32 v68, v56, v35
	v_fma_f32 v69, -v34, v68, v56
	v_fmac_f32_e32 v68, v69, v35
	v_fma_f32 v34, -v34, v68, v56
	v_div_scale_f32 v56, s[16:17], v16, v16, v129
	v_rcp_f32_e32 v69, v56
	v_div_fmas_f32 v34, v34, v35, v68
	v_div_fixup_f32 v34, v34, v92, 1.0
	v_lshl_add_u64 v[24:25], s[18:19], 0, v[24:25]
	v_fma_f32 v35, -v56, v69, 1.0
	v_fmac_f32_e32 v69, v35, v69
	v_div_scale_f32 v35, vcc, v129, v16, v129
	v_mul_f32_e32 v68, v35, v69
	v_fma_f32 v70, -v56, v68, v35
	v_fmac_f32_e32 v68, v70, v69
	v_fma_f32 v35, -v56, v68, v35
	v_div_fmas_f32 v35, v35, v69, v68
	v_div_fixup_f32 v16, v35, v16, v129
	v_mul_f32_e32 v35, v16, v52
	v_fma_f32 v52, v74, v34, -v35
	v_mul_f32_e32 v35, v16, v54
	v_fma_f32 v54, v58, v34, -v35
	v_mul_f32_e32 v56, v54, v54
	v_mul_f32_e32 v35, v16, v64
	v_fmac_f32_e32 v56, v52, v52
	v_fma_f32 v42, v42, v34, -v35
	v_mul_f32_e32 v16, v16, v66
	v_fmac_f32_e32 v56, v42, v42
	v_fma_f32 v26, v26, v34, -v16
	v_fmac_f32_e32 v56, v26, v26
	s_nop 1
	v_mov_b32_dpp v16, v56 quad_perm:[1,0,3,2] row_mask:0xf bank_mask:0xf
	v_lshl_add_u64 v[24:25], v[24:25], 0, s[38:39]
	v_mul_f32_e32 v58, v71, v40
	v_lshl_add_u64 v[24:25], v[24:25], 0, v[130:131]
	v_mul_f32_e32 v58, v80, v58
	s_waitcnt lgkmcnt(0)
	v_add_f32_e32 v16, v56, v16
	s_nop 1
	v_mov_b32_dpp v56, v16 quad_perm:[2,3,0,1] row_mask:0xf bank_mask:0xf
	v_lshl_add_u64 v[34:35], v[24:25], 0, s[30:31]
	v_bfe_u32 v64, v58, 16, 1
	v_add_co_u32_e32 v24, vcc, s74, v24
	s_waitcnt lgkmcnt(0)
	v_add_f32_e32 v16, v16, v56
	s_nop 1
	v_mov_b32_dpp v56, v16 row_half_mirror row_mask:0xf bank_mask:0xf
	v_add3_u32 v58, v58, v64, s73
	v_addc_co_u32_e32 v25, vcc, 0, v25, vcc
	global_store_short_d16_hi v[24:25], v58, off offset:1024
	s_waitcnt lgkmcnt(0)
	v_add_f32_e32 v16, v16, v56
	s_nop 1
	v_mov_b32_dpp v25, v16 row_ror:8 row_mask:0xf bank_mask:0xf
	v_mul_f32_e32 v24, v57, v40
	v_mul_f32_e32 v24, v94, v24
	v_bfe_u32 v56, v24, 16, 1
	v_add3_u32 v24, v24, v56, s73
	s_waitcnt lgkmcnt(0)
	v_add_f32_e32 v16, v16, v25
	global_store_short_d16_hi v[34:35], v24, off offset:64
	v_mov_b32_e32 v24, v16
	s_nop 1
	v_permlane16_swap_b32_e32 v16, v24
	v_mul_f32_e32 v25, v41, v40
	v_mul_f32_e32 v25, v120, v25
	v_bfe_u32 v41, v25, 16, 1
	v_add3_u32 v25, v25, v41, s73
	s_waitcnt lgkmcnt(0)
	v_add_f32_e32 v16, v16, v24
	v_fmamk_f32 v16, v16, 0x3c000000, v190
	v_mul_f32_e32 v24, 0x4f800000, v16
	v_cmp_gt_f32_e32 vcc, s71, v16
	global_store_short_d16_hi v[34:35], v25, off offset:128
	v_mul_f32_e32 v25, v73, v40
	v_cndmask_b32_e32 v16, v16, v24, vcc
	v_sqrt_f32_e32 v24, v16
	v_mul_f32_e32 v25, v121, v25
	v_add_u32_e32 v40, -1, v24
	v_fma_f32 v41, -v40, v24, v16
	v_cmp_ge_f32_e64 s[16:17], 0, v41
	v_add_u32_e32 v41, 1, v24
	s_nop 0
	v_cndmask_b32_e64 v40, v24, v40, s[16:17]
	v_fma_f32 v24, -v41, v24, v16
	v_cmp_lt_f32_e64 s[16:17], 0, v24
	s_nop 1
	v_cndmask_b32_e64 v24, v40, v41, s[16:17]
	v_mul_f32_e32 v40, 0x37800000, v24
	v_cndmask_b32_e32 v24, v24, v40, vcc
	v_cmp_class_f32_e32 vcc, v16, v191
	v_bfe_u32 v41, v25, 16, 1
	v_add3_u32 v25, v25, v41, s73
	v_cndmask_b32_e32 v16, v24, v16, vcc
	v_div_scale_f32 v24, s[16:17], v16, v16, s72
	v_rcp_f32_e32 v40, v24
	global_store_short_d16_hi v[34:35], v25, off offset:192
	v_fma_f32 v25, -v24, v40, 1.0
	v_fmac_f32_e32 v40, v25, v40
	v_div_scale_f32 v25, vcc, s72, v16, s72
	v_mul_f32_e32 v34, v25, v40
	v_fma_f32 v35, -v24, v34, v25
	v_fmac_f32_e32 v34, v35, v40
	v_fma_f32 v24, -v24, v34, v25
	v_div_fmas_f32 v24, v24, v40, v34
	v_div_scale_f32 v34, s[16:17], v93, v93, 1.0
	v_rcp_f32_e32 v35, v34
	v_div_fixup_f32 v40, v24, v16, s72
	v_lshl_add_u64 v[24:25], s[36:37], 0, v[156:157]
	v_lshlrev_b64 v[24:25], 12, v[24:25]
	v_fma_f32 v16, -v34, v35, 1.0
	v_fmac_f32_e32 v35, v16, v35
	v_div_scale_f32 v16, vcc, 1.0, v93, 1.0
	v_mul_f32_e32 v41, v16, v35
	v_fma_f32 v56, -v34, v41, v16
	v_fmac_f32_e32 v41, v56, v35
	v_fma_f32 v16, -v34, v41, v16
	v_div_scale_f32 v34, s[16:17], v17, v17, v129
	v_rcp_f32_e32 v56, v34
	v_div_fmas_f32 v16, v16, v35, v41
	v_div_fixup_f32 v16, v16, v93, 1.0
	v_mul_f32_e32 v26, v26, v40
	v_fma_f32 v35, -v34, v56, 1.0
	v_fmac_f32_e32 v56, v35, v56
	v_div_scale_f32 v35, vcc, v129, v17, v129
	v_mul_f32_e32 v41, v35, v56
	v_fma_f32 v57, -v34, v41, v35
	v_fmac_f32_e32 v41, v57, v56
	v_fma_f32 v34, -v34, v41, v35
	v_div_fmas_f32 v34, v34, v56, v41
	v_div_fixup_f32 v17, v34, v17, v129
	v_mul_f32_e32 v34, v17, v53
	v_fma_f32 v41, v75, v16, -v34
	v_mul_f32_e32 v34, v17, v55
	v_fma_f32 v53, v59, v16, -v34
	v_mul_f32_e32 v34, v53, v53
	v_mul_f32_e32 v35, v17, v65
	v_fmac_f32_e32 v34, v41, v41
	v_fma_f32 v43, v43, v16, -v35
	v_mul_f32_e32 v17, v17, v67
	v_fmac_f32_e32 v34, v43, v43
	v_fma_f32 v55, v27, v16, -v17
	v_fmac_f32_e32 v34, v55, v55
	s_nop 1
	v_mov_b32_dpp v27, v34 quad_perm:[1,0,3,2] row_mask:0xf bank_mask:0xf
	v_lshl_add_u64 v[16:17], s[18:19], 0, v[24:25]
	v_lshl_add_u64 v[16:17], v[16:17], 0, s[38:39]
	v_mul_f32_e32 v35, v52, v40
	v_lshl_add_u64 v[16:17], v[16:17], 0, v[130:131]
	s_waitcnt lgkmcnt(0)
	v_add_f32_e32 v27, v34, v27
	s_nop 1
	v_mov_b32_dpp v34, v27 quad_perm:[2,3,0,1] row_mask:0xf bank_mask:0xf
	v_mul_f32_e32 v35, v80, v35
	v_lshl_add_u64 v[24:25], v[16:17], 0, s[30:31]
	v_bfe_u32 v52, v35, 16, 1
	v_add_co_u32_e32 v16, vcc, s74, v16
	s_waitcnt lgkmcnt(0)
	v_add_f32_e32 v27, v27, v34
	s_nop 1
	v_mov_b32_dpp v34, v27 row_half_mirror row_mask:0xf bank_mask:0xf
	v_add3_u32 v35, v35, v52, s73
	v_addc_co_u32_e32 v17, vcc, 0, v17, vcc
	global_store_short_d16_hi v[16:17], v35, off offset:1024
	s_waitcnt lgkmcnt(0)
	v_add_f32_e32 v17, v27, v34
	s_nop 1
	v_mov_b32_dpp v27, v17 row_ror:8 row_mask:0xf bank_mask:0xf
	v_mul_f32_e32 v16, v54, v40
	v_mul_f32_e32 v16, v94, v16
	v_bfe_u32 v34, v16, 16, 1
	v_add3_u32 v16, v16, v34, s73
	global_store_short_d16_hi v[24:25], v16, off offset:64
	s_waitcnt lgkmcnt(0)
	v_add_f32_e32 v16, v17, v27
	v_mov_b32_e32 v17, v16
	s_nop 1
	v_permlane16_swap_b32_e32 v16, v17
	v_mul_f32_e32 v27, v42, v40
	v_mul_f32_e32 v27, v120, v27
	v_bfe_u32 v34, v27, 16, 1
	v_add3_u32 v27, v27, v34, s73
	s_waitcnt lgkmcnt(0)
	v_add_f32_e32 v16, v16, v17
	v_fmamk_f32 v16, v16, 0x3c000000, v190
	v_mul_f32_e32 v17, 0x4f800000, v16
	v_cmp_gt_f32_e32 vcc, s71, v16
	global_store_short_d16_hi v[24:25], v27, off offset:128
	v_mul_f32_e32 v26, v121, v26
	v_cndmask_b32_e32 v16, v16, v17, vcc
	v_sqrt_f32_e32 v17, v16
	s_nop 0
	v_add_u32_e32 v27, -1, v17
	v_fma_f32 v34, -v27, v17, v16
	v_cmp_ge_f32_e64 s[16:17], 0, v34
	v_add_u32_e32 v34, 1, v17
	s_nop 0
	v_cndmask_b32_e64 v27, v17, v27, s[16:17]
	v_fma_f32 v17, -v34, v17, v16
	v_cmp_lt_f32_e64 s[16:17], 0, v17
	s_nop 1
	v_cndmask_b32_e64 v17, v27, v34, s[16:17]
	v_mul_f32_e32 v27, 0x37800000, v17
	v_cndmask_b32_e32 v17, v17, v27, vcc
	v_cmp_class_f32_e32 vcc, v16, v191
	v_bfe_u32 v34, v26, 16, 1
	v_add3_u32 v26, v26, v34, s73
	v_cndmask_b32_e32 v16, v17, v16, vcc
	v_div_scale_f32 v17, s[16:17], v16, v16, s72
	v_rcp_f32_e32 v27, v17
	global_store_short_d16_hi v[24:25], v26, off offset:192
	v_div_scale_f32 v34, s[16:17], v90, v90, 1.0
	v_fma_f32 v24, -v17, v27, 1.0
	v_fmac_f32_e32 v27, v24, v27
	v_div_scale_f32 v24, vcc, s72, v16, s72
	v_mul_f32_e32 v25, v24, v27
	v_fma_f32 v26, -v17, v25, v24
	v_fmac_f32_e32 v25, v26, v27
	v_rcp_f32_e32 v35, v34
	v_fma_f32 v17, -v17, v25, v24
	v_div_fmas_f32 v17, v17, v27, v25
	v_div_fixup_f32 v40, v17, v16, s72
	v_lshl_add_u64 v[16:17], s[36:37], 0, v[158:159]
	v_lshlrev_b64 v[24:25], 12, v[16:17]
	v_fma_f32 v16, -v34, v35, 1.0
	ds_read2_b32 v[26:27], v186 offset0:24 offset1:25
	v_fmac_f32_e32 v35, v16, v35
	v_div_scale_f32 v16, vcc, 1.0, v90, 1.0
	v_mul_f32_e32 v42, v16, v35
	v_fma_f32 v17, -v34, v42, v16
	v_fmac_f32_e32 v42, v17, v35
	v_fma_f32 v34, -v34, v42, v16
	ds_read2_b32 v[16:17], v186 offset0:26 offset1:27
	s_waitcnt lgkmcnt(1)
	v_div_scale_f32 v52, s[16:17], v26, v26, v129
	v_rcp_f32_e32 v54, v52
	v_div_fmas_f32 v34, v34, v35, v42
	v_div_fixup_f32 v34, v34, v90, 1.0
	v_lshl_add_u64 v[24:25], s[18:19], 0, v[24:25]
	v_fma_f32 v35, -v52, v54, 1.0
	v_fmac_f32_e32 v54, v35, v54
	v_div_scale_f32 v35, vcc, v129, v26, v129
	v_mul_f32_e32 v42, v35, v54
	v_fma_f32 v56, -v52, v42, v35
	v_fmac_f32_e32 v42, v56, v54
	v_fma_f32 v35, -v52, v42, v35
	v_div_fmas_f32 v35, v35, v54, v42
	v_div_fixup_f32 v26, v35, v26, v129
	v_mul_f32_e32 v35, v26, v36
	v_fma_f32 v36, v76, v34, -v35
	v_mul_f32_e32 v35, v26, v38
	v_fma_f32 v38, v60, v34, -v35
	v_mul_f32_e32 v42, v38, v38
	v_mul_f32_e32 v35, v26, v48
	v_fmac_f32_e32 v42, v36, v36
	v_fma_f32 v44, v44, v34, -v35
	v_mul_f32_e32 v26, v26, v50
	v_fmac_f32_e32 v42, v44, v44
	v_fma_f32 v28, v28, v34, -v26
	v_fmac_f32_e32 v42, v28, v28
	s_nop 1
	v_mov_b32_dpp v26, v42 quad_perm:[1,0,3,2] row_mask:0xf bank_mask:0xf
	v_lshl_add_u64 v[24:25], v[24:25], 0, s[38:39]
	v_mul_f32_e32 v41, v41, v40
	v_lshl_add_u64 v[24:25], v[24:25], 0, v[130:131]
	v_mul_f32_e32 v41, v80, v41
	s_waitcnt lgkmcnt(0)
	v_add_f32_e32 v26, v42, v26
	s_nop 1
	v_mov_b32_dpp v42, v26 quad_perm:[2,3,0,1] row_mask:0xf bank_mask:0xf
	v_lshl_add_u64 v[34:35], v[24:25], 0, s[30:31]
	v_bfe_u32 v48, v41, 16, 1
	v_add_co_u32_e32 v24, vcc, s74, v24
	s_waitcnt lgkmcnt(0)
	v_add_f32_e32 v26, v26, v42
	s_nop 1
	v_mov_b32_dpp v42, v26 row_half_mirror row_mask:0xf bank_mask:0xf
	v_add3_u32 v41, v41, v48, s73
	v_addc_co_u32_e32 v25, vcc, 0, v25, vcc
	global_store_short_d16_hi v[24:25], v41, off offset:1024
	s_waitcnt lgkmcnt(0)
	v_add_f32_e32 v25, v26, v42
	s_nop 1
	v_mov_b32_dpp v26, v25 row_ror:8 row_mask:0xf bank_mask:0xf
	v_mul_f32_e32 v24, v53, v40
	v_mul_f32_e32 v24, v94, v24
	v_bfe_u32 v41, v24, 16, 1
	v_add3_u32 v24, v24, v41, s73
	global_store_short_d16_hi v[34:35], v24, off offset:64
	s_waitcnt lgkmcnt(0)
	v_add_f32_e32 v24, v25, v26
	v_mov_b32_e32 v25, v24
	s_nop 1
	v_permlane16_swap_b32_e32 v24, v25
	v_mul_f32_e32 v26, v43, v40
	v_mul_f32_e32 v26, v120, v26
	v_bfe_u32 v41, v26, 16, 1
	v_add3_u32 v26, v26, v41, s73
	s_waitcnt lgkmcnt(0)
	v_add_f32_e32 v24, v24, v25
	v_fmamk_f32 v24, v24, 0x3c000000, v190
	v_mul_f32_e32 v25, 0x4f800000, v24
	v_cmp_gt_f32_e32 vcc, s71, v24
	global_store_short_d16_hi v[34:35], v26, off offset:128
	v_mul_f32_e32 v26, v55, v40
	v_cndmask_b32_e32 v24, v24, v25, vcc
	v_sqrt_f32_e32 v25, v24
	v_mul_f32_e32 v26, v121, v26
	v_add_u32_e32 v40, -1, v25
	v_fma_f32 v41, -v40, v25, v24
	v_cmp_ge_f32_e64 s[16:17], 0, v41
	v_add_u32_e32 v41, 1, v25
	s_nop 0
	v_cndmask_b32_e64 v40, v25, v40, s[16:17]
	v_fma_f32 v25, -v41, v25, v24
	v_cmp_lt_f32_e64 s[16:17], 0, v25
	s_nop 1
	v_cndmask_b32_e64 v25, v40, v41, s[16:17]
	v_mul_f32_e32 v40, 0x37800000, v25
	v_cndmask_b32_e32 v25, v25, v40, vcc
	v_cmp_class_f32_e32 vcc, v24, v191
	v_bfe_u32 v41, v26, 16, 1
	v_add3_u32 v26, v26, v41, s73
	v_cndmask_b32_e32 v24, v25, v24, vcc
	v_div_scale_f32 v25, s[16:17], v24, v24, s72
	v_rcp_f32_e32 v40, v25
	global_store_short_d16_hi v[34:35], v26, off offset:192
	v_fma_f32 v26, -v25, v40, 1.0
	v_fmac_f32_e32 v40, v26, v40
	v_div_scale_f32 v26, vcc, s72, v24, s72
	v_mul_f32_e32 v34, v26, v40
	v_fma_f32 v35, -v25, v34, v26
	v_fmac_f32_e32 v34, v35, v40
	v_fma_f32 v25, -v25, v34, v26
	v_div_scale_f32 v26, s[16:17], v91, v91, 1.0
	v_div_fmas_f32 v25, v25, v40, v34
	v_rcp_f32_e32 v34, v26
	v_div_fixup_f32 v35, v25, v24, s72
	v_lshl_add_u64 v[24:25], s[36:37], 0, v[160:161]
	v_lshlrev_b64 v[24:25], 12, v[24:25]
	v_fma_f32 v40, -v26, v34, 1.0
	v_fmac_f32_e32 v34, v40, v34
	v_div_scale_f32 v40, vcc, 1.0, v91, 1.0
	v_mul_f32_e32 v41, v40, v34
	v_fma_f32 v42, -v26, v41, v40
	v_fmac_f32_e32 v41, v42, v34
	v_fma_f32 v26, -v26, v41, v40
	v_div_scale_f32 v40, s[16:17], v27, v27, v129
	v_rcp_f32_e32 v42, v40
	v_div_fmas_f32 v26, v26, v34, v41
	v_div_fixup_f32 v26, v26, v91, 1.0
	v_lshl_add_u64 v[24:25], s[18:19], 0, v[24:25]
	v_fma_f32 v34, -v40, v42, 1.0
	v_fmac_f32_e32 v42, v34, v42
	v_div_scale_f32 v34, vcc, v129, v27, v129
	v_mul_f32_e32 v41, v34, v42
	v_fma_f32 v43, -v40, v41, v34
	v_fmac_f32_e32 v41, v43, v42
	v_fma_f32 v34, -v40, v41, v34
	v_div_fmas_f32 v34, v34, v42, v41
	v_div_fixup_f32 v27, v34, v27, v129
	v_mul_f32_e32 v34, v27, v37
	v_mul_f32_e32 v37, v27, v39
	v_fma_f32 v37, v61, v26, -v37
	v_fma_f32 v34, v77, v26, -v34
	v_mul_f32_e32 v39, v37, v37
	v_mul_f32_e32 v40, v27, v49
	v_fmac_f32_e32 v39, v34, v34
	v_fma_f32 v40, v45, v26, -v40
	v_mul_f32_e32 v27, v27, v51
	v_fmac_f32_e32 v39, v40, v40
	v_fma_f32 v29, v29, v26, -v27
	v_fmac_f32_e32 v39, v29, v29
	s_nop 1
	v_mov_b32_dpp v41, v39 quad_perm:[1,0,3,2] row_mask:0xf bank_mask:0xf
	v_lshl_add_u64 v[24:25], v[24:25], 0, s[38:39]
	v_mul_f32_e32 v36, v36, v35
	v_lshl_add_u64 v[24:25], v[24:25], 0, v[130:131]
	v_mul_f32_e32 v36, v80, v36
	s_waitcnt lgkmcnt(0)
	v_add_f32_e32 v39, v39, v41
	s_nop 1
	v_mov_b32_dpp v41, v39 quad_perm:[2,3,0,1] row_mask:0xf bank_mask:0xf
	v_lshl_add_u64 v[26:27], v[24:25], 0, s[30:31]
	v_bfe_u32 v42, v36, 16, 1
	v_add_co_u32_e32 v24, vcc, s74, v24
	s_waitcnt lgkmcnt(0)
	v_add_f32_e32 v39, v39, v41
	s_nop 1
	v_mov_b32_dpp v41, v39 row_half_mirror row_mask:0xf bank_mask:0xf
	v_add3_u32 v36, v36, v42, s73
	v_addc_co_u32_e32 v25, vcc, 0, v25, vcc
	global_store_short_d16_hi v[24:25], v36, off offset:1024
	s_waitcnt lgkmcnt(0)
	v_add_f32_e32 v25, v39, v41
	s_nop 1
	v_mov_b32_dpp v36, v25 row_ror:8 row_mask:0xf bank_mask:0xf
	v_mul_f32_e32 v24, v38, v35
	v_mul_f32_e32 v24, v94, v24
	v_bfe_u32 v38, v24, 16, 1
	v_add3_u32 v24, v24, v38, s73
	global_store_short_d16_hi v[26:27], v24, off offset:64
	s_waitcnt lgkmcnt(0)
	v_add_f32_e32 v24, v25, v36
	v_mov_b32_e32 v25, v24
	s_nop 1
	v_permlane16_swap_b32_e32 v24, v25
	v_mul_f32_e32 v36, v44, v35
	v_mul_f32_e32 v36, v120, v36
	v_bfe_u32 v38, v36, 16, 1
	v_add3_u32 v36, v36, v38, s73
	s_waitcnt lgkmcnt(0)
	v_add_f32_e32 v24, v24, v25
	v_fmamk_f32 v24, v24, 0x3c000000, v190
	v_mul_f32_e32 v25, 0x4f800000, v24
	v_cmp_gt_f32_e32 vcc, s71, v24
	v_mul_f32_e32 v28, v28, v35
	global_store_short_d16_hi v[26:27], v36, off offset:128
	v_cndmask_b32_e32 v24, v24, v25, vcc
	v_sqrt_f32_e32 v25, v24
	v_mul_f32_e32 v28, v121, v28
	v_add_u32_e32 v35, -1, v25
	v_fma_f32 v36, -v35, v25, v24
	v_cmp_ge_f32_e64 s[16:17], 0, v36
	v_add_u32_e32 v36, 1, v25
	s_nop 0
	v_cndmask_b32_e64 v35, v25, v35, s[16:17]
	v_fma_f32 v25, -v36, v25, v24
	v_cmp_lt_f32_e64 s[16:17], 0, v25
	s_nop 1
	v_cndmask_b32_e64 v25, v35, v36, s[16:17]
	v_mul_f32_e32 v35, 0x37800000, v25
	v_cndmask_b32_e32 v25, v25, v35, vcc
	v_cmp_class_f32_e32 vcc, v24, v191
	v_bfe_u32 v36, v28, 16, 1
	v_add3_u32 v28, v28, v36, s73
	v_cndmask_b32_e32 v24, v25, v24, vcc
	v_div_scale_f32 v25, s[16:17], v24, v24, s72
	v_rcp_f32_e32 v35, v25
	global_store_short_d16_hi v[26:27], v28, off offset:192
	v_fma_f32 v26, -v25, v35, 1.0
	v_fmac_f32_e32 v35, v26, v35
	v_div_scale_f32 v26, vcc, s72, v24, s72
	v_mul_f32_e32 v27, v26, v35
	v_fma_f32 v28, -v25, v27, v26
	v_fmac_f32_e32 v27, v28, v35
	v_fma_f32 v25, -v25, v27, v26
	v_div_scale_f32 v26, s[16:17], v88, v88, 1.0
	v_div_fmas_f32 v25, v25, v35, v27
	v_rcp_f32_e32 v27, v26
	v_div_fixup_f32 v28, v25, v24, s72
	v_lshl_add_u64 v[24:25], s[36:37], 0, v[162:163]
	v_lshlrev_b64 v[24:25], 12, v[24:25]
	v_fma_f32 v35, -v26, v27, 1.0
	v_fmac_f32_e32 v27, v35, v27
	v_div_scale_f32 v35, vcc, 1.0, v88, 1.0
	v_mul_f32_e32 v36, v35, v27
	v_fma_f32 v38, -v26, v36, v35
	v_fmac_f32_e32 v36, v38, v27
	v_fma_f32 v26, -v26, v36, v35
	v_div_scale_f32 v35, s[16:17], v16, v16, v129
	v_rcp_f32_e32 v38, v35
	v_div_fmas_f32 v26, v26, v27, v36
	v_div_fixup_f32 v26, v26, v88, 1.0
	v_lshl_add_u64 v[24:25], s[18:19], 0, v[24:25]
	v_fma_f32 v27, -v35, v38, 1.0
	v_fmac_f32_e32 v38, v27, v38
	v_div_scale_f32 v27, vcc, v129, v16, v129
	v_mul_f32_e32 v36, v27, v38
	v_fma_f32 v39, -v35, v36, v27
	v_fmac_f32_e32 v36, v39, v38
	v_fma_f32 v27, -v35, v36, v27
	v_div_fmas_f32 v27, v27, v38, v36
	v_div_fixup_f32 v16, v27, v16, v129
	v_mul_f32_e32 v18, v16, v18
	v_fma_f32 v35, v78, v26, -v18
	v_mul_f32_e32 v18, v16, v20
	v_fma_f32 v20, v62, v26, -v18
	v_mul_f32_e32 v18, v20, v20
	v_mul_f32_e32 v22, v16, v22
	v_fmac_f32_e32 v18, v35, v35
	v_fma_f32 v22, v46, v26, -v22
	v_mul_f32_e32 v16, v16, v32
	v_fmac_f32_e32 v18, v22, v22
	v_fma_f32 v30, v30, v26, -v16
	v_fmac_f32_e32 v18, v30, v30
	s_nop 1
	v_mov_b32_dpp v16, v18 quad_perm:[1,0,3,2] row_mask:0xf bank_mask:0xf
	v_lshl_add_u64 v[24:25], v[24:25], 0, s[38:39]
	v_mul_f32_e32 v32, v34, v28
	v_lshl_add_u64 v[24:25], v[24:25], 0, v[130:131]
	v_mul_f32_e32 v32, v80, v32
	s_waitcnt lgkmcnt(0)
	v_add_f32_e32 v16, v18, v16
	s_nop 1
	v_mov_b32_dpp v18, v16 quad_perm:[2,3,0,1] row_mask:0xf bank_mask:0xf
	v_lshl_add_u64 v[26:27], v[24:25], 0, s[30:31]
	v_bfe_u32 v34, v32, 16, 1
	v_add_co_u32_e32 v24, vcc, s74, v24
	s_waitcnt lgkmcnt(0)
	v_add_f32_e32 v16, v16, v18
	s_nop 1
	v_mov_b32_dpp v18, v16 row_half_mirror row_mask:0xf bank_mask:0xf
	v_add3_u32 v32, v32, v34, s73
	v_addc_co_u32_e32 v25, vcc, 0, v25, vcc
	global_store_short_d16_hi v[24:25], v32, off offset:1024
	s_waitcnt lgkmcnt(0)
	v_add_f32_e32 v16, v16, v18
	s_nop 1
	v_mov_b32_dpp v18, v16 row_ror:8 row_mask:0xf bank_mask:0xf
	v_mul_f32_e32 v24, v37, v28
	v_mul_f32_e32 v24, v94, v24
	v_bfe_u32 v25, v24, 16, 1
	v_add3_u32 v24, v24, v25, s73
	s_waitcnt lgkmcnt(0)
	v_add_f32_e32 v16, v16, v18
	v_mov_b32_e32 v18, v16
	s_nop 1
	v_permlane16_swap_b32_e32 v16, v18
	global_store_short_d16_hi v[26:27], v24, off offset:64
	v_mul_f32_e32 v24, v40, v28
	v_mul_f32_e32 v24, v120, v24
	v_bfe_u32 v25, v24, 16, 1
	s_waitcnt lgkmcnt(0)
	v_add_f32_e32 v16, v16, v18
	v_fmamk_f32 v16, v16, 0x3c000000, v190
	v_mul_f32_e32 v18, 0x4f800000, v16
	v_cmp_gt_f32_e32 vcc, s71, v16
	v_add3_u32 v24, v24, v25, s73
	global_store_short_d16_hi v[26:27], v24, off offset:128
	v_cndmask_b32_e32 v16, v16, v18, vcc
	v_sqrt_f32_e32 v18, v16
	v_mul_f32_e32 v24, v29, v28
	v_mul_f32_e32 v24, v121, v24
	v_add_u32_e32 v25, -1, v18
	v_fma_f32 v28, -v25, v18, v16
	v_cmp_ge_f32_e64 s[16:17], 0, v28
	v_add_u32_e32 v28, 1, v18
	s_nop 0
	v_cndmask_b32_e64 v25, v18, v25, s[16:17]
	v_fma_f32 v18, -v28, v18, v16
	v_cmp_lt_f32_e64 s[16:17], 0, v18
	s_nop 1
	v_cndmask_b32_e64 v18, v25, v28, s[16:17]
	v_mul_f32_e32 v25, 0x37800000, v18
	v_cndmask_b32_e32 v18, v18, v25, vcc
	v_cmp_class_f32_e32 vcc, v16, v191
	v_bfe_u32 v28, v24, 16, 1
	v_add3_u32 v24, v24, v28, s73
	v_cndmask_b32_e32 v16, v18, v16, vcc
	v_div_scale_f32 v18, s[16:17], v16, v16, s72
	v_rcp_f32_e32 v25, v18
	global_store_short_d16_hi v[26:27], v24, off offset:192
	v_fma_f32 v24, -v18, v25, 1.0
	v_fmac_f32_e32 v25, v24, v25
	v_div_scale_f32 v24, vcc, s72, v16, s72
	v_mul_f32_e32 v26, v24, v25
	v_fma_f32 v27, -v18, v26, v24
	v_fmac_f32_e32 v26, v27, v25
	v_fma_f32 v18, -v18, v26, v24
	v_div_fmas_f32 v18, v18, v25, v26
	v_div_scale_f32 v26, s[16:17], v89, v89, 1.0
	v_rcp_f32_e32 v27, v26
	v_div_fixup_f32 v28, v18, v16, s72
	v_lshl_add_u64 v[24:25], s[36:37], 0, v[164:165]
	v_lshlrev_b64 v[24:25], 12, v[24:25]
	v_fma_f32 v16, -v26, v27, 1.0
	v_fmac_f32_e32 v27, v16, v27
	v_div_scale_f32 v16, vcc, 1.0, v89, 1.0
	v_mul_f32_e32 v18, v16, v27
	v_fma_f32 v29, -v26, v18, v16
	v_fmac_f32_e32 v18, v29, v27
	v_fma_f32 v16, -v26, v18, v16
	v_div_scale_f32 v26, s[16:17], v17, v17, v129
	v_rcp_f32_e32 v29, v26
	v_div_fmas_f32 v16, v16, v27, v18
	v_div_fixup_f32 v16, v16, v89, 1.0
	v_fma_f32 v18, -v26, v29, 1.0
	v_fmac_f32_e32 v29, v18, v29
	v_div_scale_f32 v18, vcc, v129, v17, v129
	v_mul_f32_e32 v27, v18, v29
	v_fma_f32 v32, -v26, v27, v18
	v_fmac_f32_e32 v27, v32, v29
	v_fma_f32 v18, -v26, v27, v18
	v_div_fmas_f32 v18, v18, v29, v27
	v_div_fixup_f32 v17, v18, v17, v129
	v_mul_f32_e32 v18, v17, v19
	v_fma_f32 v26, v79, v16, -v18
	v_mul_f32_e32 v18, v17, v21
	v_fma_f32 v21, v63, v16, -v18
	v_mul_f32_e32 v27, v21, v21
	v_mul_f32_e32 v18, v17, v23
	v_fmac_f32_e32 v27, v26, v26
	v_fma_f32 v23, v47, v16, -v18
	v_mul_f32_e32 v17, v17, v33
	v_fmac_f32_e32 v27, v23, v23
	v_fma_f32 v29, v31, v16, -v17
	v_fmac_f32_e32 v27, v29, v29
	s_nop 1
	v_mov_b32_dpp v31, v27 quad_perm:[1,0,3,2] row_mask:0xf bank_mask:0xf
	v_lshl_add_u64 v[16:17], s[18:19], 0, v[24:25]
	v_lshl_add_u64 v[16:17], v[16:17], 0, s[38:39]
	v_lshl_add_u64 v[16:17], v[16:17], 0, v[130:131]
	v_lshl_add_u64 v[18:19], v[16:17], 0, s[30:31]
	s_waitcnt lgkmcnt(0)
	v_add_f32_e32 v24, v27, v31
	s_nop 1
	v_mov_b32_dpp v25, v24 quad_perm:[2,3,0,1] row_mask:0xf bank_mask:0xf
	v_mul_f32_e32 v27, v35, v28
	v_mul_f32_e32 v27, v80, v27
	v_bfe_u32 v31, v27, 16, 1
	v_add_co_u32_e32 v16, vcc, s74, v16
	s_waitcnt lgkmcnt(0)
	v_add_f32_e32 v24, v24, v25
	s_nop 1
	v_mov_b32_dpp v25, v24 row_half_mirror row_mask:0xf bank_mask:0xf
	v_add3_u32 v27, v27, v31, s73
	v_addc_co_u32_e32 v17, vcc, 0, v17, vcc
	global_store_short_d16_hi v[16:17], v27, off offset:1024
	s_waitcnt lgkmcnt(0)
	v_add_f32_e32 v17, v24, v25
	v_mul_f32_e32 v16, v20, v28
	s_nop 1
	v_mov_b32_dpp v20, v17 row_ror:8 row_mask:0xf bank_mask:0xf
	v_mul_f32_e32 v16, v94, v16
	v_bfe_u32 v24, v16, 16, 1
	v_add3_u32 v16, v16, v24, s73
	global_store_short_d16_hi v[18:19], v16, off offset:64
	s_waitcnt lgkmcnt(0)
	v_add_f32_e32 v16, v17, v20
	v_mov_b32_e32 v17, v16
	s_nop 1
	v_permlane16_swap_b32_e32 v16, v17
	v_mul_f32_e32 v20, v22, v28
	v_mul_f32_e32 v20, v120, v20
	v_bfe_u32 v22, v20, 16, 1
	v_add3_u32 v20, v20, v22, s73
	s_waitcnt lgkmcnt(0)
	v_add_f32_e32 v16, v16, v17
	v_fmamk_f32 v16, v16, 0x3c000000, v190
	v_mul_f32_e32 v17, 0x4f800000, v16
	v_cmp_gt_f32_e32 vcc, s71, v16
	global_store_short_d16_hi v[18:19], v20, off offset:128
	v_mul_f32_e32 v20, v30, v28
	v_cndmask_b32_e32 v16, v16, v17, vcc
	v_sqrt_f32_e32 v17, v16
	v_mul_f32_e32 v20, v121, v20
	v_add_u32_e32 v22, -1, v17
	v_fma_f32 v24, -v22, v17, v16
	v_cmp_ge_f32_e64 s[16:17], 0, v24
	v_add_u32_e32 v24, 1, v17
	s_nop 0
	v_cndmask_b32_e64 v22, v17, v22, s[16:17]
	v_fma_f32 v17, -v24, v17, v16
	v_cmp_lt_f32_e64 s[16:17], 0, v17
	s_nop 1
	v_cndmask_b32_e64 v17, v22, v24, s[16:17]
	v_mul_f32_e32 v22, 0x37800000, v17
	v_cndmask_b32_e32 v17, v17, v22, vcc
	v_cmp_class_f32_e32 vcc, v16, v191
	v_bfe_u32 v24, v20, 16, 1
	v_add3_u32 v20, v20, v24, s73
	v_cndmask_b32_e32 v16, v17, v16, vcc
	v_div_scale_f32 v17, s[16:17], v16, v16, s72
	v_rcp_f32_e32 v22, v17
	global_store_short_d16_hi v[18:19], v20, off offset:192
	v_fma_f32 v18, -v17, v22, 1.0
	v_fmac_f32_e32 v22, v18, v22
	v_div_scale_f32 v18, vcc, s72, v16, s72
	v_mul_f32_e32 v19, v18, v22
	v_fma_f32 v20, -v17, v19, v18
	v_fmac_f32_e32 v19, v20, v22
	v_fma_f32 v17, -v17, v19, v18
	v_div_fmas_f32 v17, v17, v22, v19
	v_div_fixup_f32 v20, v17, v16, s72
	v_lshl_add_u64 v[16:17], s[36:37], 0, v[166:167]
	v_lshlrev_b64 v[16:17], 12, v[16:17]
	v_lshl_add_u64 v[16:17], s[18:19], 0, v[16:17]
	v_lshl_add_u64 v[16:17], v[16:17], 0, s[38:39]
	v_mul_f32_e32 v22, v26, v20
	v_lshl_add_u64 v[16:17], v[16:17], 0, v[130:131]
	v_mul_f32_e32 v22, v80, v22
	v_lshl_add_u64 v[18:19], v[16:17], 0, s[30:31]
	v_bfe_u32 v24, v22, 16, 1
	v_add_co_u32_e32 v16, vcc, s74, v16
	v_add3_u32 v22, v22, v24, s73
	s_nop 0
	v_addc_co_u32_e32 v17, vcc, 0, v17, vcc
	global_store_short_d16_hi v[16:17], v22, off offset:1024
	v_mul_f32_e32 v16, v21, v20
	v_mul_f32_e32 v16, v94, v16
	v_bfe_u32 v17, v16, 16, 1
	v_add3_u32 v16, v16, v17, s73
	global_store_short_d16_hi v[18:19], v16, off offset:64
	v_mul_f32_e32 v16, v23, v20
	v_mul_f32_e32 v16, v120, v16
	v_bfe_u32 v17, v16, 16, 1
	v_add3_u32 v16, v16, v17, s73
	global_store_short_d16_hi v[18:19], v16, off offset:128
	v_mul_f32_e32 v16, v29, v20
	v_mul_f32_e32 v16, v121, v16
	v_bfe_u32 v17, v16, 16, 1
	v_add3_u32 v16, v16, v17, s73
	global_store_short_d16_hi v[18:19], v16, off offset:192
	s_branch .LBB0_528

.LBB0_1907:
	s_andn2_b64 vcc, exec, s[28:29]
	s_waitcnt lgkmcnt(0)
	s_barrier
	s_cbranch_vccnz .LBB0_1886
	ds_read2_b32 v[80:81], v185 offset1:1
	ds_read2_b32 v[82:83], v185 offset0:8 offset1:9
	ds_read2_b32 v[86:87], v185 offset0:10 offset1:11
	ds_read2_b32 v[84:85], v185 offset0:16 offset1:17
	ds_read2_b32 v[94:95], v186 offset1:1
	s_waitcnt lgkmcnt(4)
	v_div_scale_f32 v88, s[16:17], v80, v80, 1.0
	v_rcp_f32_e32 v90, v88
	v_div_scale_f32 v89, vcc, 1.0, v80, 1.0
	ds_read2st64_b32 v[122:123], v187 offset1:1
	v_fma_f32 v91, -v88, v90, 1.0
	v_fmac_f32_e32 v90, v91, v90
	v_mul_f32_e32 v91, v89, v90
	v_fma_f32 v92, -v88, v91, v89
	v_fmac_f32_e32 v91, v92, v90
	v_fma_f32 v92, -v88, v91, v89
	ds_read2_b32 v[88:89], v185 offset0:26 offset1:27
	s_waitcnt lgkmcnt(2)
	v_div_scale_f32 v93, s[16:17], v94, v94, v129
	v_rcp_f32_e32 v96, v93
	v_div_fmas_f32 v90, v92, v90, v91
	v_div_fixup_f32 v80, v90, v80, 1.0
	v_lshl_add_u64 v[196:197], s[36:37], 0, v[134:135]
	v_fma_f32 v90, -v93, v96, 1.0
	v_fmac_f32_e32 v96, v90, v96
	v_div_scale_f32 v90, vcc, v129, v94, v129
	v_mul_f32_e32 v91, v90, v96
	v_fma_f32 v92, -v93, v91, v90
	v_fmac_f32_e32 v91, v92, v96
	v_fma_f32 v90, -v93, v91, v90
	v_div_fmas_f32 v90, v90, v96, v91
	ds_read2st64_b32 v[112:113], v187 offset0:2 offset1:3
	ds_read2st64_b32 v[104:105], v187 offset0:4 offset1:5
	ds_read2st64_b32 v[96:97], v187 offset0:6 offset1:7
	ds_read2st64_b32 v[124:125], v187 offset0:16 offset1:17
	ds_read2st64_b32 v[114:115], v187 offset0:18 offset1:19
	ds_read2st64_b32 v[106:107], v187 offset0:20 offset1:21
	ds_read2st64_b32 v[98:99], v187 offset0:22 offset1:23
	ds_read2st64_b32 v[126:127], v187 offset0:32 offset1:33
	v_div_fixup_f32 v90, v90, v94, v129
	ds_read2st64_b32 v[116:117], v187 offset0:34 offset1:35
	ds_read2st64_b32 v[108:109], v187 offset0:36 offset1:37
	ds_read2st64_b32 v[100:101], v187 offset0:38 offset1:39
	ds_read2st64_b32 v[194:195], v187 offset0:48 offset1:49
	s_waitcnt lgkmcnt(13)
	v_mul_f32_e32 v91, v90, v122
	v_fma_f32 v64, v64, v80, -v91
	s_waitcnt lgkmcnt(8)
	v_mul_f32_e32 v91, v90, v124
	v_fma_f32 v48, v48, v80, -v91
	v_mul_f32_e32 v91, v48, v48
	s_waitcnt lgkmcnt(4)
	v_mul_f32_e32 v92, v90, v126
	v_fmac_f32_e32 v91, v64, v64
	v_fma_f32 v122, v32, v80, -v92
	s_waitcnt lgkmcnt(0)
	v_mul_f32_e32 v32, v90, v194
	v_fmac_f32_e32 v91, v122, v122
	v_fma_f32 v124, v16, v80, -v32
	v_fmac_f32_e32 v91, v124, v124
	s_nop 1
	v_mov_b32_dpp v16, v91 quad_perm:[1,0,3,2] row_mask:0xf bank_mask:0xf
	ds_read2st64_b32 v[118:119], v187 offset0:50 offset1:51
	ds_read2st64_b32 v[110:111], v187 offset0:52 offset1:53
	ds_read2st64_b32 v[102:103], v187 offset0:54 offset1:55
	global_load_dword v80, v[136:137], off offset:512
	global_load_dword v94, v[136:137], off offset:640
	v_lshlrev_b64 v[196:197], 12, v[196:197]
	s_waitcnt lgkmcnt(3)
	v_add_f32_e32 v16, v91, v16
	s_nop 1
	v_mov_b32_dpp v32, v16 quad_perm:[2,3,0,1] row_mask:0xf bank_mask:0xf
	v_lshl_add_u64 v[196:197], s[18:19], 0, v[196:197]
	s_waitcnt lgkmcnt(0)
	v_add_f32_e32 v16, v16, v32
	s_nop 1
	v_mov_b32_dpp v32, v16 row_half_mirror row_mask:0xf bank_mask:0xf
	s_waitcnt lgkmcnt(0)
	v_add_f32_e32 v16, v16, v32
	s_nop 1
	v_mov_b32_dpp v32, v16 row_ror:8 row_mask:0xf bank_mask:0xf
	s_waitcnt lgkmcnt(0)
	v_add_f32_e32 v16, v16, v32
	v_mov_b32_e32 v32, v16
	s_nop 1
	v_permlane16_swap_b32_e32 v16, v32
	s_waitcnt lgkmcnt(0)
	v_add_f32_e32 v16, v16, v32
	v_fmamk_f32 v16, v16, 0x3c000000, v190
	v_mul_f32_e32 v32, 0x4f800000, v16
	v_cmp_gt_f32_e32 vcc, s71, v16
	s_nop 1
	v_cndmask_b32_e32 v16, v16, v32, vcc
	v_sqrt_f32_e32 v32, v16
	s_nop 0
	v_add_u32_e32 v90, -1, v32
	v_fma_f32 v91, -v90, v32, v16
	v_cmp_ge_f32_e64 s[16:17], 0, v91
	v_add_u32_e32 v91, 1, v32
	s_nop 0
	v_cndmask_b32_e64 v90, v32, v90, s[16:17]
	v_fma_f32 v32, -v91, v32, v16
	v_cmp_lt_f32_e64 s[16:17], 0, v32
	s_nop 1
	v_cndmask_b32_e64 v32, v90, v91, s[16:17]
	v_mul_f32_e32 v90, 0x37800000, v32
	v_cndmask_b32_e32 v32, v32, v90, vcc
	v_cmp_class_f32_e32 vcc, v16, v191
	ds_read2_b32 v[92:93], v185 offset0:18 offset1:19
	ds_read2_b32 v[90:91], v185 offset0:24 offset1:25
	v_cndmask_b32_e32 v16, v32, v16, vcc
	v_div_scale_f32 v32, s[16:17], v16, v16, s72
	v_rcp_f32_e32 v121, v32
	v_div_scale_f32 v126, vcc, s72, v16, s72
	v_fma_f32 v120, -v32, v121, 1.0
	v_fmac_f32_e32 v121, v120, v121
	global_load_dword v120, v[136:137], off offset:768
	v_mul_f32_e32 v130, v126, v121
	v_fma_f32 v193, -v32, v130, v126
	v_fmac_f32_e32 v130, v193, v121
	v_fma_f32 v32, -v32, v130, v126
	v_div_fmas_f32 v32, v32, v121, v130
	global_load_dword v121, v[136:137], off offset:896
	v_div_fixup_f32 v126, v32, v16, s72
	v_div_scale_f32 v16, s[16:17], v81, v81, 1.0
	v_rcp_f32_e32 v32, v16
	v_mul_f32_e32 v64, v64, v126
	v_fma_f32 v130, -v16, v32, 1.0
	v_fmac_f32_e32 v32, v130, v32
	v_div_scale_f32 v130, vcc, 1.0, v81, 1.0
	v_mul_f32_e32 v193, v130, v32
	v_fma_f32 v194, -v16, v193, v130
	v_fmac_f32_e32 v193, v194, v32
	v_fma_f32 v16, -v16, v193, v130
	v_div_scale_f32 v130, s[16:17], v95, v95, v129
	v_rcp_f32_e32 v194, v130
	v_div_fmas_f32 v16, v16, v32, v193
	v_div_fixup_f32 v16, v16, v81, 1.0
	s_waitcnt vmcnt(3)
	v_mul_f32_e32 v64, v80, v64
	v_fma_f32 v32, -v130, v194, 1.0
	v_fmac_f32_e32 v194, v32, v194
	v_div_scale_f32 v32, vcc, v129, v95, v129
	v_mul_f32_e32 v81, v32, v194
	v_fma_f32 v193, -v130, v81, v32
	v_fmac_f32_e32 v81, v193, v194
	v_fma_f32 v32, -v130, v81, v32
	v_div_fmas_f32 v32, v32, v194, v81
	v_div_fixup_f32 v32, v32, v95, v129
	v_mul_f32_e32 v81, v32, v123
	v_fma_f32 v81, v65, v16, -v81
	v_mul_f32_e32 v65, v32, v125
	v_fma_f32 v95, v49, v16, -v65
	v_mul_f32_e32 v49, v95, v95
	v_mul_f32_e32 v65, v32, v127
	v_fmac_f32_e32 v49, v81, v81
	v_fma_f32 v123, v33, v16, -v65
	v_mul_f32_e32 v32, v32, v195
	v_fmac_f32_e32 v49, v123, v123
	v_fma_f32 v125, v17, v16, -v32
	v_fmac_f32_e32 v49, v125, v125
	s_nop 1
	v_mov_b32_dpp v65, v49 quad_perm:[1,0,3,2] row_mask:0xf bank_mask:0xf
	v_lshl_add_u64 v[16:17], v[196:197], 0, s[38:39]
	v_lshlrev_b32_e32 v130, 1, v128
	v_lshl_add_u64 v[16:17], v[16:17], 0, v[130:131]
	v_lshl_add_u64 v[32:33], v[16:17], 0, s[30:31]
	s_waitcnt lgkmcnt(0)
	v_add_f32_e32 v49, v49, v65
	s_nop 1
	v_mov_b32_dpp v65, v49 quad_perm:[2,3,0,1] row_mask:0xf bank_mask:0xf
	v_bfe_u32 v127, v64, 16, 1
	v_add_co_u32_e32 v16, vcc, s74, v16
	v_add3_u32 v64, v64, v127, s73
	s_waitcnt lgkmcnt(0)
	v_add_f32_e32 v49, v49, v65
	s_nop 1
	v_mov_b32_dpp v65, v49 row_half_mirror row_mask:0xf bank_mask:0xf
	v_addc_co_u32_e32 v17, vcc, 0, v17, vcc
	global_store_short_d16_hi v[16:17], v64, off offset:1024
	v_mul_f32_e32 v16, v48, v126
	s_waitcnt lgkmcnt(0)
	v_add_f32_e32 v17, v49, v65
	s_nop 1
	v_mov_b32_dpp v48, v17 row_ror:8 row_mask:0xf bank_mask:0xf
	s_waitcnt vmcnt(3)
	v_mul_f32_e32 v16, v94, v16
	v_bfe_u32 v49, v16, 16, 1
	v_add3_u32 v16, v16, v49, s73
	global_store_short_d16_hi v[32:33], v16, off offset:64
	s_waitcnt lgkmcnt(0)
	v_add_f32_e32 v16, v17, v48
	v_mov_b32_e32 v17, v16
	s_nop 1
	v_permlane16_swap_b32_e32 v16, v17
	v_mul_f32_e32 v48, v122, v126
	s_waitcnt lgkmcnt(0)
	v_add_f32_e32 v16, v16, v17
	v_fmamk_f32 v16, v16, 0x3c000000, v190
	v_mul_f32_e32 v17, 0x4f800000, v16
	v_cmp_gt_f32_e32 vcc, s71, v16
	s_waitcnt vmcnt(3)
	v_mul_f32_e32 v48, v120, v48
	v_bfe_u32 v49, v48, 16, 1
	v_cndmask_b32_e32 v16, v16, v17, vcc
	v_sqrt_f32_e32 v17, v16
	v_add3_u32 v48, v48, v49, s73
	global_store_short_d16_hi v[32:33], v48, off offset:128
	v_mul_f32_e32 v48, v124, v126
	v_add_u32_e32 v49, -1, v17
	v_fma_f32 v64, -v49, v17, v16
	v_cmp_ge_f32_e64 s[16:17], 0, v64
	v_add_u32_e32 v64, 1, v17
	s_waitcnt vmcnt(3)
	v_mul_f32_e32 v48, v121, v48
	v_cndmask_b32_e64 v49, v17, v49, s[16:17]
	v_fma_f32 v17, -v64, v17, v16
	v_cmp_lt_f32_e64 s[16:17], 0, v17
	s_nop 1
	v_cndmask_b32_e64 v17, v49, v64, s[16:17]
	v_mul_f32_e32 v49, 0x37800000, v17
	v_cndmask_b32_e32 v17, v17, v49, vcc
	v_cmp_class_f32_e32 vcc, v16, v191
	s_nop 1
	v_cndmask_b32_e32 v49, v17, v16, vcc
	v_div_scale_f32 v16, s[16:17], v49, v49, s72
	v_rcp_f32_e32 v64, v16
	v_bfe_u32 v17, v48, 16, 1
	v_add3_u32 v17, v48, v17, s73
	global_store_short_d16_hi v[32:33], v17, off offset:192
	v_fma_f32 v17, -v16, v64, 1.0
	v_fmac_f32_e32 v64, v17, v64
	v_div_scale_f32 v17, vcc, s72, v49, s72
	v_mul_f32_e32 v32, v17, v64
	v_fma_f32 v33, -v16, v32, v17
	v_fmac_f32_e32 v32, v33, v64
	v_fma_f32 v33, -v16, v32, v17
	ds_read2_b32 v[16:17], v188 offset1:1
	v_div_fmas_f32 v48, v33, v64, v32
	ds_read2_b32 v[32:33], v189 offset1:1
	v_div_fixup_f32 v122, v48, v49, s72
	v_lshl_add_u64 v[48:49], s[36:37], 0, v[138:139]
	s_waitcnt lgkmcnt(1)
	v_div_scale_f32 v64, s[16:17], v16, v16, 1.0
	v_rcp_f32_e32 v65, v64
	v_lshlrev_b64 v[48:49], 12, v[48:49]
	v_lshl_add_u64 v[48:49], s[18:19], 0, v[48:49]
	v_lshl_add_u64 v[48:49], v[48:49], 0, s[38:39]
	v_fma_f32 v124, -v64, v65, 1.0
	v_fmac_f32_e32 v65, v124, v65
	v_div_scale_f32 v124, vcc, 1.0, v16, 1.0
	v_mul_f32_e32 v126, v124, v65
	v_fma_f32 v127, -v64, v126, v124
	v_fmac_f32_e32 v126, v127, v65
	v_fma_f32 v64, -v64, v126, v124
	s_waitcnt lgkmcnt(0)
	v_div_scale_f32 v124, s[16:17], v32, v32, v129
	v_rcp_f32_e32 v127, v124
	v_div_fmas_f32 v64, v64, v65, v126
	v_div_fixup_f32 v16, v64, v16, 1.0
	v_mul_f32_e32 v81, v81, v122
	v_fma_f32 v64, -v124, v127, 1.0
	v_fmac_f32_e32 v127, v64, v127
	v_div_scale_f32 v64, vcc, v129, v32, v129
	v_mul_f32_e32 v65, v64, v127
	v_fma_f32 v126, -v124, v65, v64
	v_fmac_f32_e32 v65, v126, v127
	v_fma_f32 v64, -v124, v65, v64
	v_div_fmas_f32 v64, v64, v127, v65
	v_div_fixup_f32 v32, v64, v32, v129
	v_mul_f32_e32 v64, v32, v112
	v_fma_f32 v66, v66, v16, -v64
	v_mul_f32_e32 v64, v32, v114
	v_fma_f32 v50, v50, v16, -v64
	v_mul_f32_e32 v112, v50, v50
	v_mul_f32_e32 v64, v32, v116
	v_fmac_f32_e32 v112, v66, v66
	v_fma_f32 v34, v34, v16, -v64
	v_mul_f32_e32 v32, v32, v118
	v_fmac_f32_e32 v112, v34, v34
	v_fma_f32 v32, v18, v16, -v32
	v_fmac_f32_e32 v112, v32, v32
	s_nop 1
	v_mov_b32_dpp v16, v112 quad_perm:[1,0,3,2] row_mask:0xf bank_mask:0xf
	v_lshl_add_u64 v[48:49], v[48:49], 0, v[130:131]
	v_mul_f32_e32 v81, v80, v81
	v_lshl_add_u64 v[64:65], v[48:49], 0, s[30:31]
	v_add_co_u32_e32 v48, vcc, s74, v48
	s_waitcnt lgkmcnt(0)
	v_add_f32_e32 v16, v112, v16
	s_nop 1
	v_mov_b32_dpp v18, v16 quad_perm:[2,3,0,1] row_mask:0xf bank_mask:0xf
	v_bfe_u32 v112, v81, 16, 1
	v_add3_u32 v81, v81, v112, s73
	v_addc_co_u32_e32 v49, vcc, 0, v49, vcc
	s_waitcnt lgkmcnt(0)
	v_add_f32_e32 v16, v16, v18
	s_nop 1
	v_mov_b32_dpp v18, v16 row_half_mirror row_mask:0xf bank_mask:0xf
	global_store_short_d16_hi v[48:49], v81, off offset:1024
	v_mul_f32_e32 v48, v95, v122
	v_mul_f32_e32 v48, v94, v48
	v_bfe_u32 v49, v48, 16, 1
	s_waitcnt lgkmcnt(0)
	v_add_f32_e32 v16, v16, v18
	s_nop 1
	v_mov_b32_dpp v18, v16 row_ror:8 row_mask:0xf bank_mask:0xf
	v_add3_u32 v48, v48, v49, s73
	global_store_short_d16_hi v[64:65], v48, off offset:64
	v_mul_f32_e32 v48, v123, v122
	v_mul_f32_e32 v48, v120, v48
	s_waitcnt lgkmcnt(0)
	v_add_f32_e32 v16, v16, v18
	v_mov_b32_e32 v18, v16
	s_nop 1
	v_permlane16_swap_b32_e32 v16, v18
	v_bfe_u32 v49, v48, 16, 1
	v_add3_u32 v48, v48, v49, s73
	global_store_short_d16_hi v[64:65], v48, off offset:128
	v_mul_f32_e32 v48, v125, v122
	s_waitcnt lgkmcnt(0)
	v_add_f32_e32 v16, v16, v18
	v_fmamk_f32 v16, v16, 0x3c000000, v190
	v_mul_f32_e32 v18, 0x4f800000, v16
	v_cmp_gt_f32_e32 vcc, s71, v16
	v_mul_f32_e32 v48, v121, v48
	s_nop 0
	v_cndmask_b32_e32 v16, v16, v18, vcc
	v_sqrt_f32_e32 v18, v16
	s_nop 0
	v_add_u32_e32 v49, -1, v18
	v_fma_f32 v81, -v49, v18, v16
	v_cmp_ge_f32_e64 s[16:17], 0, v81
	v_add_u32_e32 v81, 1, v18
	s_nop 0
	v_cndmask_b32_e64 v49, v18, v49, s[16:17]
	v_fma_f32 v18, -v81, v18, v16
	v_cmp_lt_f32_e64 s[16:17], 0, v18
	s_nop 1
	v_cndmask_b32_e64 v18, v49, v81, s[16:17]
	v_mul_f32_e32 v49, 0x37800000, v18
	v_cndmask_b32_e32 v18, v18, v49, vcc
	v_cmp_class_f32_e32 vcc, v16, v191
	v_bfe_u32 v81, v48, 16, 1
	v_add3_u32 v48, v48, v81, s73
	v_cndmask_b32_e32 v16, v18, v16, vcc
	v_div_scale_f32 v18, s[16:17], v16, v16, s72
	v_rcp_f32_e32 v49, v18
	global_store_short_d16_hi v[64:65], v48, off offset:192
	v_fma_f32 v48, -v18, v49, 1.0
	v_fmac_f32_e32 v49, v48, v49
	v_div_scale_f32 v48, vcc, s72, v16, s72
	v_mul_f32_e32 v64, v48, v49
	v_fma_f32 v65, -v18, v64, v48
	v_fmac_f32_e32 v64, v65, v49
	v_fma_f32 v18, -v18, v64, v48
	v_div_fmas_f32 v18, v18, v49, v64
	v_div_scale_f32 v64, s[16:17], v17, v17, 1.0
	v_rcp_f32_e32 v65, v64
	v_div_fixup_f32 v81, v18, v16, s72
	v_lshl_add_u64 v[48:49], s[36:37], 0, v[140:141]
	v_lshlrev_b64 v[48:49], 12, v[48:49]
	v_fma_f32 v16, -v64, v65, 1.0
	v_fmac_f32_e32 v65, v16, v65
	v_div_scale_f32 v16, vcc, 1.0, v17, 1.0
	v_mul_f32_e32 v18, v16, v65
	v_fma_f32 v95, -v64, v18, v16
	v_fmac_f32_e32 v18, v95, v65
	v_fma_f32 v16, -v64, v18, v16
	v_div_scale_f32 v64, s[16:17], v33, v33, v129
	v_rcp_f32_e32 v95, v64
	v_div_fmas_f32 v16, v16, v65, v18
	v_div_fixup_f32 v16, v16, v17, 1.0
	v_mul_f32_e32 v32, v32, v81
	v_fma_f32 v17, -v64, v95, 1.0
	v_fmac_f32_e32 v95, v17, v95
	v_div_scale_f32 v17, vcc, v129, v33, v129
	v_mul_f32_e32 v18, v17, v95
	v_fma_f32 v65, -v64, v18, v17
	v_fmac_f32_e32 v18, v65, v95
	v_fma_f32 v17, -v64, v18, v17
	v_div_fmas_f32 v17, v17, v95, v18
	v_div_fixup_f32 v17, v17, v33, v129
	v_mul_f32_e32 v18, v17, v113
	v_fma_f32 v64, v67, v16, -v18
	v_mul_f32_e32 v18, v17, v115
	v_fma_f32 v65, v51, v16, -v18
	v_mul_f32_e32 v33, v65, v65
	v_mul_f32_e32 v18, v17, v117
	v_fmac_f32_e32 v33, v64, v64
	v_fma_f32 v67, v35, v16, -v18
	v_mul_f32_e32 v17, v17, v119
	v_fmac_f32_e32 v33, v67, v67
	v_fma_f32 v95, v19, v16, -v17
	v_fmac_f32_e32 v33, v95, v95
	s_nop 1
	v_mov_b32_dpp v35, v33 quad_perm:[1,0,3,2] row_mask:0xf bank_mask:0xf
	v_lshl_add_u64 v[16:17], s[18:19], 0, v[48:49]
	v_lshl_add_u64 v[16:17], v[16:17], 0, s[38:39]
	v_mul_f32_e32 v48, v66, v81
	v_lshl_add_u64 v[16:17], v[16:17], 0, v[130:131]
	s_waitcnt lgkmcnt(0)
	v_add_f32_e32 v33, v33, v35
	s_nop 1
	v_mov_b32_dpp v35, v33 quad_perm:[2,3,0,1] row_mask:0xf bank_mask:0xf
	v_mul_f32_e32 v48, v80, v48
	v_lshl_add_u64 v[18:19], v[16:17], 0, s[30:31]
	v_bfe_u32 v49, v48, 16, 1
	v_add_co_u32_e32 v16, vcc, s74, v16
	s_waitcnt lgkmcnt(0)
	v_add_f32_e32 v33, v33, v35
	s_nop 1
	v_mov_b32_dpp v35, v33 row_half_mirror row_mask:0xf bank_mask:0xf
	v_add3_u32 v48, v48, v49, s73
	v_addc_co_u32_e32 v17, vcc, 0, v17, vcc
	global_store_short_d16_hi v[16:17], v48, off offset:1024
	s_waitcnt lgkmcnt(0)
	v_add_f32_e32 v17, v33, v35
	s_nop 1
	v_mov_b32_dpp v33, v17 row_ror:8 row_mask:0xf bank_mask:0xf
	v_mul_f32_e32 v16, v50, v81
	v_mul_f32_e32 v16, v94, v16
	v_bfe_u32 v35, v16, 16, 1
	v_add3_u32 v16, v16, v35, s73
	global_store_short_d16_hi v[18:19], v16, off offset:64
	s_waitcnt lgkmcnt(0)
	v_add_f32_e32 v16, v17, v33
	v_mov_b32_e32 v17, v16
	s_nop 1
	v_permlane16_swap_b32_e32 v16, v17
	v_mul_f32_e32 v33, v34, v81
	v_mul_f32_e32 v33, v120, v33
	v_bfe_u32 v34, v33, 16, 1
	v_add3_u32 v33, v33, v34, s73
	s_waitcnt lgkmcnt(0)
	v_add_f32_e32 v16, v16, v17
	v_fmamk_f32 v16, v16, 0x3c000000, v190
	v_mul_f32_e32 v17, 0x4f800000, v16
	v_cmp_gt_f32_e32 vcc, s71, v16
	global_store_short_d16_hi v[18:19], v33, off offset:128
	v_mul_f32_e32 v32, v121, v32
	v_cndmask_b32_e32 v16, v16, v17, vcc
	v_sqrt_f32_e32 v17, v16
	s_nop 0
	v_add_u32_e32 v33, -1, v17
	v_fma_f32 v34, -v33, v17, v16
	v_cmp_ge_f32_e64 s[16:17], 0, v34
	v_add_u32_e32 v34, 1, v17
	s_nop 0
	v_cndmask_b32_e64 v33, v17, v33, s[16:17]
	v_fma_f32 v17, -v34, v17, v16
	v_cmp_lt_f32_e64 s[16:17], 0, v17
	s_nop 1
	v_cndmask_b32_e64 v17, v33, v34, s[16:17]
	v_mul_f32_e32 v33, 0x37800000, v17
	v_cndmask_b32_e32 v17, v17, v33, vcc
	v_cmp_class_f32_e32 vcc, v16, v191
	v_bfe_u32 v34, v32, 16, 1
	v_add3_u32 v32, v32, v34, s73
	v_cndmask_b32_e32 v16, v17, v16, vcc
	v_div_scale_f32 v17, s[16:17], v16, v16, s72
	v_rcp_f32_e32 v33, v17
	global_store_short_d16_hi v[18:19], v32, off offset:192
	v_fma_f32 v18, -v17, v33, 1.0
	v_fmac_f32_e32 v33, v18, v33
	v_div_scale_f32 v18, vcc, s72, v16, s72
	v_mul_f32_e32 v19, v18, v33
	v_fma_f32 v32, -v17, v19, v18
	v_fmac_f32_e32 v19, v32, v33
	v_fma_f32 v17, -v17, v19, v18
	v_div_scale_f32 v18, s[16:17], v82, v82, 1.0
	v_rcp_f32_e32 v50, v18
	v_div_fmas_f32 v17, v17, v33, v19
	v_div_fixup_f32 v66, v17, v16, s72
	v_lshl_add_u64 v[16:17], s[36:37], 0, v[142:143]
	v_lshlrev_b64 v[32:33], 12, v[16:17]
	v_fma_f32 v16, -v18, v50, 1.0
	v_fmac_f32_e32 v50, v16, v50
	v_div_scale_f32 v16, vcc, 1.0, v82, 1.0
	v_mul_f32_e32 v51, v16, v50
	v_fma_f32 v17, -v18, v51, v16
	v_fmac_f32_e32 v51, v17, v50
	v_fma_f32 v81, -v18, v51, v16
	ds_read2_b32 v[48:49], v186 offset0:8 offset1:9
	ds_read2_b32 v[18:19], v186 offset0:10 offset1:11
	ds_read2_b32 v[34:35], v186 offset0:16 offset1:17
	ds_read2_b32 v[16:17], v186 offset0:18 offset1:19
	v_div_fmas_f32 v50, v81, v50, v51
	s_waitcnt lgkmcnt(3)
	v_div_scale_f32 v112, s[16:17], v48, v48, v129
	v_rcp_f32_e32 v113, v112
	v_div_fixup_f32 v50, v50, v82, 1.0
	v_lshl_add_u64 v[32:33], s[18:19], 0, v[32:33]
	v_lshl_add_u64 v[32:33], v[32:33], 0, s[38:39]
	v_fma_f32 v51, -v112, v113, 1.0
	v_fmac_f32_e32 v113, v51, v113
	v_div_scale_f32 v51, vcc, v129, v48, v129
	v_mul_f32_e32 v81, v51, v113
	v_fma_f32 v82, -v112, v81, v51
	v_fmac_f32_e32 v81, v82, v113
	v_fma_f32 v51, -v112, v81, v51
	v_div_fmas_f32 v51, v51, v113, v81
	v_div_fixup_f32 v48, v51, v48, v129
	v_mul_f32_e32 v51, v48, v104
	v_fma_f32 v68, v68, v50, -v51
	v_mul_f32_e32 v51, v48, v106
	v_fma_f32 v52, v52, v50, -v51
	v_mul_f32_e32 v81, v52, v52
	v_mul_f32_e32 v51, v48, v108
	v_fmac_f32_e32 v81, v68, v68
	v_fma_f32 v36, v36, v50, -v51
	v_mul_f32_e32 v48, v48, v110
	v_fmac_f32_e32 v81, v36, v36
	v_fma_f32 v48, v20, v50, -v48
	v_fmac_f32_e32 v81, v48, v48
	s_nop 1
	v_mov_b32_dpp v20, v81 quad_perm:[1,0,3,2] row_mask:0xf bank_mask:0xf
	v_mul_f32_e32 v64, v64, v66
	v_lshl_add_u64 v[32:33], v[32:33], 0, v[130:131]
	v_mul_f32_e32 v64, v80, v64
	v_lshl_add_u64 v[50:51], v[32:33], 0, s[30:31]
	s_waitcnt lgkmcnt(0)
	v_add_f32_e32 v20, v81, v20
	s_nop 1
	v_mov_b32_dpp v81, v20 quad_perm:[2,3,0,1] row_mask:0xf bank_mask:0xf
	v_bfe_u32 v82, v64, 16, 1
	v_add_co_u32_e32 v32, vcc, s74, v32
	v_add3_u32 v64, v64, v82, s73
	s_waitcnt lgkmcnt(0)
	v_add_f32_e32 v20, v20, v81
	s_nop 1
	v_mov_b32_dpp v81, v20 row_half_mirror row_mask:0xf bank_mask:0xf
	v_addc_co_u32_e32 v33, vcc, 0, v33, vcc
	global_store_short_d16_hi v[32:33], v64, off offset:1024
	v_mul_f32_e32 v32, v65, v66
	s_waitcnt lgkmcnt(0)
	v_add_f32_e32 v20, v20, v81
	s_nop 1
	v_mov_b32_dpp v33, v20 row_ror:8 row_mask:0xf bank_mask:0xf
	v_mul_f32_e32 v32, v94, v32
	v_bfe_u32 v64, v32, 16, 1
	v_add3_u32 v32, v32, v64, s73
	global_store_short_d16_hi v[50:51], v32, off offset:64
	s_waitcnt lgkmcnt(0)
	v_add_f32_e32 v20, v20, v33
	v_mov_b32_e32 v32, v20
	s_nop 1
	v_permlane16_swap_b32_e32 v20, v32
	v_mul_f32_e32 v33, v67, v66
	v_mul_f32_e32 v33, v120, v33
	v_bfe_u32 v64, v33, 16, 1
	v_add3_u32 v33, v33, v64, s73
	s_waitcnt lgkmcnt(0)
	v_add_f32_e32 v20, v20, v32
	v_fmamk_f32 v20, v20, 0x3c000000, v190
	v_mul_f32_e32 v32, 0x4f800000, v20
	v_cmp_gt_f32_e32 vcc, s71, v20
	global_store_short_d16_hi v[50:51], v33, off offset:128
	v_mul_f32_e32 v33, v95, v66
	v_cndmask_b32_e32 v20, v20, v32, vcc
	v_sqrt_f32_e32 v32, v20
	v_mul_f32_e32 v33, v121, v33
	v_add_u32_e32 v64, -1, v32
	v_fma_f32 v65, -v64, v32, v20
	v_cmp_ge_f32_e64 s[16:17], 0, v65
	v_add_u32_e32 v65, 1, v32
	s_nop 0
	v_cndmask_b32_e64 v64, v32, v64, s[16:17]
	v_fma_f32 v32, -v65, v32, v20
	v_cmp_lt_f32_e64 s[16:17], 0, v32
	s_nop 1
	v_cndmask_b32_e64 v32, v64, v65, s[16:17]
	v_mul_f32_e32 v64, 0x37800000, v32
	v_cndmask_b32_e32 v32, v32, v64, vcc
	v_cmp_class_f32_e32 vcc, v20, v191
	v_bfe_u32 v65, v33, 16, 1
	v_add3_u32 v33, v33, v65, s73
	v_cndmask_b32_e32 v20, v32, v20, vcc
	v_div_scale_f32 v32, s[16:17], v20, v20, s72
	v_rcp_f32_e32 v64, v32
	global_store_short_d16_hi v[50:51], v33, off offset:192
	v_fma_f32 v33, -v32, v64, 1.0
	v_fmac_f32_e32 v64, v33, v64
	v_div_scale_f32 v33, vcc, s72, v20, s72
	v_mul_f32_e32 v50, v33, v64
	v_fma_f32 v51, -v32, v50, v33
	v_fmac_f32_e32 v50, v51, v64
	v_fma_f32 v32, -v32, v50, v33
	v_div_fmas_f32 v32, v32, v64, v50
	v_div_scale_f32 v50, s[16:17], v83, v83, 1.0
	v_rcp_f32_e32 v51, v50
	v_div_fixup_f32 v64, v32, v20, s72
	v_lshl_add_u64 v[32:33], s[36:37], 0, v[144:145]
	v_lshlrev_b64 v[32:33], 12, v[32:33]
	v_fma_f32 v20, -v50, v51, 1.0
	v_fmac_f32_e32 v51, v20, v51
	v_div_scale_f32 v20, vcc, 1.0, v83, 1.0
	v_mul_f32_e32 v65, v20, v51
	v_fma_f32 v66, -v50, v65, v20
	v_fmac_f32_e32 v65, v66, v51
	v_fma_f32 v20, -v50, v65, v20
	v_div_scale_f32 v50, s[16:17], v49, v49, v129
	v_rcp_f32_e32 v66, v50
	v_div_fmas_f32 v20, v20, v51, v65
	v_div_fixup_f32 v20, v20, v83, 1.0
	v_mul_f32_e32 v36, v36, v64
	v_fma_f32 v51, -v50, v66, 1.0
	v_fmac_f32_e32 v66, v51, v66
	v_div_scale_f32 v51, vcc, v129, v49, v129
	v_mul_f32_e32 v65, v51, v66
	v_fma_f32 v67, -v50, v65, v51
	v_fmac_f32_e32 v65, v67, v66
	v_fma_f32 v50, -v50, v65, v51
	v_div_fmas_f32 v50, v50, v66, v65
	v_div_fixup_f32 v49, v50, v49, v129
	v_mul_f32_e32 v51, v49, v107
	v_mul_f32_e32 v50, v49, v105
	v_fma_f32 v51, v53, v20, -v51
	v_fma_f32 v50, v69, v20, -v50
	v_mul_f32_e32 v53, v51, v51
	v_mul_f32_e32 v65, v49, v109
	v_fmac_f32_e32 v53, v50, v50
	v_fma_f32 v37, v37, v20, -v65
	v_mul_f32_e32 v49, v49, v111
	v_fmac_f32_e32 v53, v37, v37
	v_fma_f32 v49, v21, v20, -v49
	v_fmac_f32_e32 v53, v49, v49
	s_nop 1
	v_mov_b32_dpp v65, v53 quad_perm:[1,0,3,2] row_mask:0xf bank_mask:0xf
	v_lshl_add_u64 v[20:21], s[18:19], 0, v[32:33]
	v_lshl_add_u64 v[20:21], v[20:21], 0, s[38:39]
	v_mul_f32_e32 v66, v68, v64
	v_lshl_add_u64 v[20:21], v[20:21], 0, v[130:131]
	s_waitcnt lgkmcnt(0)
	v_add_f32_e32 v53, v53, v65
	s_nop 1
	v_mov_b32_dpp v65, v53 quad_perm:[2,3,0,1] row_mask:0xf bank_mask:0xf
	v_mul_f32_e32 v66, v80, v66
	v_lshl_add_u64 v[32:33], v[20:21], 0, s[30:31]
	v_bfe_u32 v67, v66, 16, 1
	v_add_co_u32_e32 v20, vcc, s74, v20
	s_waitcnt lgkmcnt(0)
	v_add_f32_e32 v53, v53, v65
	s_nop 1
	v_mov_b32_dpp v65, v53 row_half_mirror row_mask:0xf bank_mask:0xf
	v_add3_u32 v66, v66, v67, s73
	v_addc_co_u32_e32 v21, vcc, 0, v21, vcc
	global_store_short_d16_hi v[20:21], v66, off offset:1024
	s_waitcnt lgkmcnt(0)
	v_add_f32_e32 v21, v53, v65
	v_mul_f32_e32 v20, v52, v64
	s_nop 1
	v_mov_b32_dpp v52, v21 row_ror:8 row_mask:0xf bank_mask:0xf
	v_mul_f32_e32 v20, v94, v20
	v_bfe_u32 v53, v20, 16, 1
	v_add3_u32 v20, v20, v53, s73
	global_store_short_d16_hi v[32:33], v20, off offset:64
	s_waitcnt lgkmcnt(0)
	v_add_f32_e32 v20, v21, v52
	v_mov_b32_e32 v21, v20
	s_nop 1
	v_permlane16_swap_b32_e32 v20, v21
	v_mul_f32_e32 v36, v120, v36
	v_bfe_u32 v52, v36, 16, 1
	v_add3_u32 v36, v36, v52, s73
	global_store_short_d16_hi v[32:33], v36, off offset:128
	s_waitcnt lgkmcnt(0)
	v_add_f32_e32 v20, v20, v21
	v_fmamk_f32 v20, v20, 0x3c000000, v190
	v_mul_f32_e32 v21, 0x4f800000, v20
	v_cmp_gt_f32_e32 vcc, s71, v20
	v_mul_f32_e32 v36, v48, v64
	v_mul_f32_e32 v36, v121, v36
	v_cndmask_b32_e32 v20, v20, v21, vcc
	v_sqrt_f32_e32 v21, v20
	s_nop 0
	v_add_u32_e32 v48, -1, v21
	v_fma_f32 v52, -v48, v21, v20
	v_cmp_ge_f32_e64 s[16:17], 0, v52
	v_add_u32_e32 v52, 1, v21
	s_nop 0
	v_cndmask_b32_e64 v48, v21, v48, s[16:17]
	v_fma_f32 v21, -v52, v21, v20
	v_cmp_lt_f32_e64 s[16:17], 0, v21
	s_nop 1
	v_cndmask_b32_e64 v21, v48, v52, s[16:17]
	v_mul_f32_e32 v48, 0x37800000, v21
	v_cndmask_b32_e32 v21, v21, v48, vcc
	v_cmp_class_f32_e32 vcc, v20, v191
	v_bfe_u32 v52, v36, 16, 1
	v_add3_u32 v36, v36, v52, s73
	v_cndmask_b32_e32 v20, v21, v20, vcc
	v_div_scale_f32 v21, s[16:17], v20, v20, s72
	v_rcp_f32_e32 v48, v21
	global_store_short_d16_hi v[32:33], v36, off offset:192
	v_fma_f32 v32, -v21, v48, 1.0
	v_fmac_f32_e32 v48, v32, v48
	v_div_scale_f32 v32, vcc, s72, v20, s72
	v_mul_f32_e32 v33, v32, v48
	v_fma_f32 v36, -v21, v33, v32
	v_fmac_f32_e32 v33, v36, v48
	v_fma_f32 v21, -v21, v33, v32
	v_div_scale_f32 v32, s[16:17], v86, v86, 1.0
	v_div_fmas_f32 v21, v21, v48, v33
	v_rcp_f32_e32 v33, v32
	v_div_fixup_f32 v36, v21, v20, s72
	v_lshl_add_u64 v[20:21], s[36:37], 0, v[146:147]
	v_lshlrev_b64 v[20:21], 12, v[20:21]
	v_fma_f32 v48, -v32, v33, 1.0
	v_fmac_f32_e32 v33, v48, v33
	v_div_scale_f32 v48, vcc, 1.0, v86, 1.0
	v_mul_f32_e32 v52, v48, v33
	v_fma_f32 v53, -v32, v52, v48
	v_fmac_f32_e32 v52, v53, v33
	v_fma_f32 v32, -v32, v52, v48
	v_div_scale_f32 v48, s[16:17], v18, v18, v129
	v_rcp_f32_e32 v53, v48
	v_div_fmas_f32 v32, v32, v33, v52
	v_div_fixup_f32 v32, v32, v86, 1.0
	v_lshl_add_u64 v[20:21], s[18:19], 0, v[20:21]
	v_fma_f32 v33, -v48, v53, 1.0
	v_fmac_f32_e32 v53, v33, v53
	v_div_scale_f32 v33, vcc, v129, v18, v129
	v_mul_f32_e32 v52, v33, v53
	v_fma_f32 v64, -v48, v52, v33
	v_fmac_f32_e32 v52, v64, v53
	v_fma_f32 v33, -v48, v52, v33
	v_div_fmas_f32 v33, v33, v53, v52
	v_div_fixup_f32 v18, v33, v18, v129
	v_mul_f32_e32 v33, v18, v96
	v_fma_f32 v48, v70, v32, -v33
	v_mul_f32_e32 v33, v18, v98
	v_fma_f32 v52, v54, v32, -v33
	v_mul_f32_e32 v53, v52, v52
	v_mul_f32_e32 v33, v18, v100
	v_fmac_f32_e32 v53, v48, v48
	v_fma_f32 v38, v38, v32, -v33
	v_mul_f32_e32 v18, v18, v102
	v_fmac_f32_e32 v53, v38, v38
	v_fma_f32 v22, v22, v32, -v18
	v_fmac_f32_e32 v53, v22, v22
	s_nop 1
	v_mov_b32_dpp v18, v53 quad_perm:[1,0,3,2] row_mask:0xf bank_mask:0xf
	v_lshl_add_u64 v[20:21], v[20:21], 0, s[38:39]
	v_mul_f32_e32 v50, v50, v36
	v_lshl_add_u64 v[20:21], v[20:21], 0, v[130:131]
	v_mul_f32_e32 v50, v80, v50
	s_waitcnt lgkmcnt(0)
	v_add_f32_e32 v18, v53, v18
	s_nop 1
	v_mov_b32_dpp v53, v18 quad_perm:[2,3,0,1] row_mask:0xf bank_mask:0xf
	v_lshl_add_u64 v[32:33], v[20:21], 0, s[30:31]
	v_bfe_u32 v54, v50, 16, 1
	v_add_co_u32_e32 v20, vcc, s74, v20
	s_waitcnt lgkmcnt(0)
	v_add_f32_e32 v18, v18, v53
	s_nop 1
	v_mov_b32_dpp v53, v18 row_half_mirror row_mask:0xf bank_mask:0xf
	v_add3_u32 v50, v50, v54, s73
	v_addc_co_u32_e32 v21, vcc, 0, v21, vcc
	global_store_short_d16_hi v[20:21], v50, off offset:1024
	s_waitcnt lgkmcnt(0)
	v_add_f32_e32 v18, v18, v53
	s_nop 1
	v_mov_b32_dpp v21, v18 row_ror:8 row_mask:0xf bank_mask:0xf
	v_mul_f32_e32 v20, v51, v36
	v_mul_f32_e32 v20, v94, v20
	v_bfe_u32 v50, v20, 16, 1
	v_add3_u32 v20, v20, v50, s73
	s_waitcnt lgkmcnt(0)
	v_add_f32_e32 v18, v18, v21
	global_store_short_d16_hi v[32:33], v20, off offset:64
	v_mov_b32_e32 v20, v18
	s_nop 1
	v_permlane16_swap_b32_e32 v18, v20
	v_mul_f32_e32 v21, v37, v36
	v_mul_f32_e32 v21, v120, v21
	v_bfe_u32 v37, v21, 16, 1
	v_add3_u32 v21, v21, v37, s73
	s_waitcnt lgkmcnt(0)
	v_add_f32_e32 v18, v18, v20
	v_fmamk_f32 v18, v18, 0x3c000000, v190
	v_mul_f32_e32 v20, 0x4f800000, v18
	v_cmp_gt_f32_e32 vcc, s71, v18
	global_store_short_d16_hi v[32:33], v21, off offset:128
	v_mul_f32_e32 v21, v49, v36
	v_cndmask_b32_e32 v18, v18, v20, vcc
	v_sqrt_f32_e32 v20, v18
	v_mul_f32_e32 v21, v121, v21
	v_add_u32_e32 v36, -1, v20
	v_fma_f32 v37, -v36, v20, v18
	v_cmp_ge_f32_e64 s[16:17], 0, v37
	v_add_u32_e32 v37, 1, v20
	s_nop 0
	v_cndmask_b32_e64 v36, v20, v36, s[16:17]
	v_fma_f32 v20, -v37, v20, v18
	v_cmp_lt_f32_e64 s[16:17], 0, v20
	s_nop 1
	v_cndmask_b32_e64 v20, v36, v37, s[16:17]
	v_mul_f32_e32 v36, 0x37800000, v20
	v_cndmask_b32_e32 v20, v20, v36, vcc
	v_cmp_class_f32_e32 vcc, v18, v191
	v_bfe_u32 v37, v21, 16, 1
	v_add3_u32 v21, v21, v37, s73
	v_cndmask_b32_e32 v18, v20, v18, vcc
	v_div_scale_f32 v20, s[16:17], v18, v18, s72
	v_rcp_f32_e32 v36, v20
	global_store_short_d16_hi v[32:33], v21, off offset:192
	v_fma_f32 v21, -v20, v36, 1.0
	v_fmac_f32_e32 v36, v21, v36
	v_div_scale_f32 v21, vcc, s72, v18, s72
	v_mul_f32_e32 v32, v21, v36
	v_fma_f32 v33, -v20, v32, v21
	v_fmac_f32_e32 v32, v33, v36
	v_fma_f32 v20, -v20, v32, v21
	v_div_fmas_f32 v20, v20, v36, v32
	v_div_scale_f32 v32, s[16:17], v87, v87, 1.0
	v_rcp_f32_e32 v33, v32
	v_div_fixup_f32 v36, v20, v18, s72
	v_lshl_add_u64 v[20:21], s[36:37], 0, v[148:149]
	v_lshlrev_b64 v[20:21], 12, v[20:21]
	v_fma_f32 v18, -v32, v33, 1.0
	v_fmac_f32_e32 v33, v18, v33
	v_div_scale_f32 v18, vcc, 1.0, v87, 1.0
	v_mul_f32_e32 v37, v18, v33
	v_fma_f32 v49, -v32, v37, v18
	v_fmac_f32_e32 v37, v49, v33
	v_fma_f32 v18, -v32, v37, v18
	v_div_scale_f32 v32, s[16:17], v19, v19, v129
	v_rcp_f32_e32 v49, v32
	v_div_fmas_f32 v18, v18, v33, v37
	v_div_fixup_f32 v18, v18, v87, 1.0
	v_mul_f32_e32 v22, v22, v36
	v_fma_f32 v33, -v32, v49, 1.0
	v_fmac_f32_e32 v49, v33, v49
	v_div_scale_f32 v33, vcc, v129, v19, v129
	v_mul_f32_e32 v37, v33, v49
	v_fma_f32 v50, -v32, v37, v33
	v_fmac_f32_e32 v37, v50, v49
	v_fma_f32 v32, -v32, v37, v33
	v_div_fmas_f32 v32, v32, v49, v37
	v_div_fixup_f32 v19, v32, v19, v129
	v_mul_f32_e32 v32, v19, v97
	v_fma_f32 v81, v71, v18, -v32
	v_mul_f32_e32 v32, v19, v99
	v_fma_f32 v95, v55, v18, -v32
	v_mul_f32_e32 v32, v95, v95
	v_mul_f32_e32 v33, v19, v101
	v_fmac_f32_e32 v32, v81, v81
	v_fma_f32 v100, v39, v18, -v33
	v_mul_f32_e32 v19, v19, v103
	v_fmac_f32_e32 v32, v100, v100
	v_fma_f32 v101, v23, v18, -v19
	v_fmac_f32_e32 v32, v101, v101
	s_nop 1
	v_mov_b32_dpp v23, v32 quad_perm:[1,0,3,2] row_mask:0xf bank_mask:0xf
	v_lshl_add_u64 v[18:19], s[18:19], 0, v[20:21]
	v_lshl_add_u64 v[18:19], v[18:19], 0, s[38:39]
	v_mul_f32_e32 v33, v48, v36
	v_lshl_add_u64 v[18:19], v[18:19], 0, v[130:131]
	s_waitcnt lgkmcnt(0)
	v_add_f32_e32 v23, v32, v23
	s_nop 1
	v_mov_b32_dpp v32, v23 quad_perm:[2,3,0,1] row_mask:0xf bank_mask:0xf
	v_mul_f32_e32 v33, v80, v33
	v_lshl_add_u64 v[20:21], v[18:19], 0, s[30:31]
	v_bfe_u32 v37, v33, 16, 1
	v_add_co_u32_e32 v18, vcc, s74, v18
	s_waitcnt lgkmcnt(0)
	v_add_f32_e32 v23, v23, v32
	s_nop 1
	v_mov_b32_dpp v32, v23 row_half_mirror row_mask:0xf bank_mask:0xf
	v_add3_u32 v33, v33, v37, s73
	v_addc_co_u32_e32 v19, vcc, 0, v19, vcc
	global_store_short_d16_hi v[18:19], v33, off offset:1024
	s_waitcnt lgkmcnt(0)
	v_add_f32_e32 v19, v23, v32
	s_nop 1
	v_mov_b32_dpp v23, v19 row_ror:8 row_mask:0xf bank_mask:0xf
	v_mul_f32_e32 v18, v52, v36
	v_mul_f32_e32 v18, v94, v18
	v_bfe_u32 v32, v18, 16, 1
	v_add3_u32 v18, v18, v32, s73
	global_store_short_d16_hi v[20:21], v18, off offset:64
	s_waitcnt lgkmcnt(0)
	v_add_f32_e32 v18, v19, v23
	v_mov_b32_e32 v19, v18
	s_nop 1
	v_permlane16_swap_b32_e32 v18, v19
	v_mul_f32_e32 v23, v38, v36
	v_mul_f32_e32 v23, v120, v23
	v_bfe_u32 v32, v23, 16, 1
	v_add3_u32 v23, v23, v32, s73
	s_waitcnt lgkmcnt(0)
	v_add_f32_e32 v18, v18, v19
	v_fmamk_f32 v18, v18, 0x3c000000, v190
	v_mul_f32_e32 v19, 0x4f800000, v18
	v_cmp_gt_f32_e32 vcc, s71, v18
	global_store_short_d16_hi v[20:21], v23, off offset:128
	v_mul_f32_e32 v22, v121, v22
	v_cndmask_b32_e32 v18, v18, v19, vcc
	v_sqrt_f32_e32 v19, v18
	ds_read2st64_b32 v[70:71], v187 offset0:8 offset1:9
	v_add_u32_e32 v23, -1, v19
	v_fma_f32 v32, -v23, v19, v18
	v_cmp_ge_f32_e64 s[16:17], 0, v32
	v_add_u32_e32 v32, 1, v19
	s_nop 0
	v_cndmask_b32_e64 v23, v19, v23, s[16:17]
	v_fma_f32 v19, -v32, v19, v18
	v_cmp_lt_f32_e64 s[16:17], 0, v19
	s_nop 1
	v_cndmask_b32_e64 v19, v23, v32, s[16:17]
	v_mul_f32_e32 v23, 0x37800000, v19
	v_cndmask_b32_e32 v19, v19, v23, vcc
	v_cmp_class_f32_e32 vcc, v18, v191
	v_bfe_u32 v32, v22, 16, 1
	v_add3_u32 v22, v22, v32, s73
	v_cndmask_b32_e32 v18, v19, v18, vcc
	v_div_scale_f32 v19, s[16:17], v18, v18, s72
	v_rcp_f32_e32 v23, v19
	global_store_short_d16_hi v[20:21], v22, off offset:192
	v_fma_f32 v20, -v19, v23, 1.0
	v_fmac_f32_e32 v23, v20, v23
	v_div_scale_f32 v20, vcc, s72, v18, s72
	v_mul_f32_e32 v21, v20, v23
	v_fma_f32 v22, -v19, v21, v20
	v_fmac_f32_e32 v21, v22, v23
	v_fma_f32 v19, -v19, v21, v20
	v_div_scale_f32 v20, s[16:17], v84, v84, 1.0
	v_div_fmas_f32 v19, v19, v23, v21
	v_rcp_f32_e32 v21, v20
	v_div_fixup_f32 v102, v19, v18, s72
	v_lshl_add_u64 v[18:19], s[36:37], 0, v[150:151]
	v_lshlrev_b64 v[68:69], 12, v[18:19]
	v_fma_f32 v18, -v20, v21, 1.0
	v_fmac_f32_e32 v21, v18, v21
	v_div_scale_f32 v18, vcc, 1.0, v84, 1.0
	v_mul_f32_e32 v19, v18, v21
	v_fma_f32 v22, -v20, v19, v18
	v_fmac_f32_e32 v19, v22, v21
	v_fma_f32 v18, -v20, v19, v18
	v_div_scale_f32 v20, s[16:17], v34, v34, v129
	v_rcp_f32_e32 v22, v20
	v_div_fmas_f32 v18, v18, v21, v19
	v_div_fixup_f32 v84, v18, v84, 1.0
	v_lshl_add_u64 v[68:69], s[18:19], 0, v[68:69]
	v_fma_f32 v18, -v20, v22, 1.0
	v_fmac_f32_e32 v22, v18, v22
	v_div_scale_f32 v18, vcc, v129, v34, v129
	v_mul_f32_e32 v19, v18, v22
	v_fma_f32 v21, -v20, v19, v18
	v_fmac_f32_e32 v19, v21, v22
	v_fma_f32 v18, -v20, v19, v18
	v_div_fmas_f32 v18, v18, v22, v19
	v_div_fixup_f32 v34, v18, v34, v129
	ds_read2st64_b32 v[52:53], v187 offset0:10 offset1:11
	ds_read2st64_b32 v[36:37], v187 offset0:12 offset1:13
	ds_read2st64_b32 v[18:19], v187 offset0:14 offset1:15
	ds_read2st64_b32 v[82:83], v187 offset0:24 offset1:25
	s_waitcnt lgkmcnt(4)
	v_mul_f32_e32 v20, v34, v70
	v_fma_f32 v70, v72, v84, -v20
	ds_read2st64_b32 v[54:55], v187 offset0:26 offset1:27
	ds_read2st64_b32 v[38:39], v187 offset0:28 offset1:29
	ds_read2st64_b32 v[20:21], v187 offset0:30 offset1:31
	ds_read2st64_b32 v[86:87], v187 offset0:40 offset1:41
	s_waitcnt lgkmcnt(4)
	v_mul_f32_e32 v22, v34, v82
	v_fma_f32 v56, v56, v84, -v22
	ds_read2st64_b32 v[64:65], v187 offset0:42 offset1:43
	ds_read2st64_b32 v[48:49], v187 offset0:44 offset1:45
	ds_read2st64_b32 v[22:23], v187 offset0:46 offset1:47
	ds_read2st64_b32 v[96:97], v187 offset0:56 offset1:57
	v_mul_f32_e32 v72, v56, v56
	s_waitcnt lgkmcnt(4)
	v_mul_f32_e32 v32, v34, v86
	v_fmac_f32_e32 v72, v70, v70
	v_fma_f32 v40, v40, v84, -v32
	s_waitcnt lgkmcnt(0)
	v_mul_f32_e32 v34, v34, v96
	v_fmac_f32_e32 v72, v40, v40
	v_fma_f32 v82, v24, v84, -v34
	v_fmac_f32_e32 v72, v82, v82
	s_nop 1
	v_mov_b32_dpp v24, v72 quad_perm:[1,0,3,2] row_mask:0xf bank_mask:0xf
	v_lshl_add_u64 v[68:69], v[68:69], 0, s[38:39]
	v_lshl_add_u64 v[68:69], v[68:69], 0, v[130:131]
	v_lshl_add_u64 v[98:99], v[68:69], 0, s[30:31]
	v_add_co_u32_e32 v68, vcc, s74, v68
	s_waitcnt lgkmcnt(0)
	v_add_f32_e32 v24, v72, v24
	s_nop 1
	v_mov_b32_dpp v34, v24 quad_perm:[2,3,0,1] row_mask:0xf bank_mask:0xf
	v_mul_f32_e32 v72, v81, v102
	v_mul_f32_e32 v72, v80, v72
	v_bfe_u32 v81, v72, 16, 1
	v_add3_u32 v72, v72, v81, s73
	s_waitcnt lgkmcnt(0)
	v_add_f32_e32 v24, v24, v34
	s_nop 1
	v_mov_b32_dpp v34, v24 row_half_mirror row_mask:0xf bank_mask:0xf
	v_addc_co_u32_e32 v69, vcc, 0, v69, vcc
	ds_read2st64_b32 v[66:67], v187 offset0:58 offset1:59
	ds_read2st64_b32 v[50:51], v187 offset0:60 offset1:61
	ds_read2st64_b32 v[32:33], v187 offset0:62 offset1:63
	global_store_short_d16_hi v[68:69], v72, off offset:1024
	s_waitcnt lgkmcnt(3)
	v_add_f32_e32 v24, v24, v34
	s_nop 1
	v_mov_b32_dpp v34, v24 row_ror:8 row_mask:0xf bank_mask:0xf
	v_mul_f32_e32 v68, v95, v102
	v_mul_f32_e32 v68, v94, v68
	v_bfe_u32 v69, v68, 16, 1
	v_add3_u32 v68, v68, v69, s73
	s_waitcnt lgkmcnt(0)
	v_add_f32_e32 v24, v24, v34
	v_mov_b32_e32 v34, v24
	s_nop 1
	v_permlane16_swap_b32_e32 v24, v34
	global_store_short_d16_hi v[98:99], v68, off offset:64
	v_mul_f32_e32 v68, v100, v102
	v_mul_f32_e32 v68, v120, v68
	v_bfe_u32 v69, v68, 16, 1
	s_waitcnt lgkmcnt(0)
	v_add_f32_e32 v24, v24, v34
	v_fmamk_f32 v24, v24, 0x3c000000, v190
	v_mul_f32_e32 v34, 0x4f800000, v24
	v_cmp_gt_f32_e32 vcc, s71, v24
	v_add3_u32 v68, v68, v69, s73
	global_store_short_d16_hi v[98:99], v68, off offset:128
	v_cndmask_b32_e32 v24, v24, v34, vcc
	v_sqrt_f32_e32 v34, v24
	v_mul_f32_e32 v68, v101, v102
	v_mul_f32_e32 v68, v121, v68
	v_add_u32_e32 v69, -1, v34
	v_fma_f32 v72, -v69, v34, v24
	v_cmp_ge_f32_e64 s[16:17], 0, v72
	v_add_u32_e32 v72, 1, v34
	s_nop 0
	v_cndmask_b32_e64 v69, v34, v69, s[16:17]
	v_fma_f32 v34, -v72, v34, v24
	v_cmp_lt_f32_e64 s[16:17], 0, v34
	s_nop 1
	v_cndmask_b32_e64 v34, v69, v72, s[16:17]
	v_mul_f32_e32 v69, 0x37800000, v34
	v_cndmask_b32_e32 v34, v34, v69, vcc
	v_cmp_class_f32_e32 vcc, v24, v191
	v_bfe_u32 v72, v68, 16, 1
	v_add3_u32 v68, v68, v72, s73
	v_cndmask_b32_e32 v24, v34, v24, vcc
	v_div_scale_f32 v34, s[16:17], v24, v24, s72
	v_rcp_f32_e32 v69, v34
	global_store_short_d16_hi v[98:99], v68, off offset:192
	v_fma_f32 v68, -v34, v69, 1.0
	v_fmac_f32_e32 v69, v68, v69
	v_div_scale_f32 v68, vcc, s72, v24, s72
	v_mul_f32_e32 v72, v68, v69
	v_fma_f32 v81, -v34, v72, v68
	v_fmac_f32_e32 v72, v81, v69
	v_fma_f32 v34, -v34, v72, v68
	v_div_fmas_f32 v34, v34, v69, v72
	v_div_scale_f32 v72, s[16:17], v85, v85, 1.0
	v_rcp_f32_e32 v81, v72
	v_div_fixup_f32 v84, v34, v24, s72
	v_lshl_add_u64 v[68:69], s[36:37], 0, v[152:153]
	v_lshlrev_b64 v[68:69], 12, v[68:69]
	v_fma_f32 v24, -v72, v81, 1.0
	v_fmac_f32_e32 v81, v24, v81
	v_div_scale_f32 v24, vcc, 1.0, v85, 1.0
	v_mul_f32_e32 v34, v24, v81
	v_fma_f32 v86, -v72, v34, v24
	v_fmac_f32_e32 v34, v86, v81
	v_fma_f32 v24, -v72, v34, v24
	v_div_scale_f32 v72, s[16:17], v35, v35, v129
	v_rcp_f32_e32 v86, v72
	v_div_fmas_f32 v24, v24, v81, v34
	v_div_fixup_f32 v24, v24, v85, 1.0
	v_mul_f32_e32 v70, v70, v84
	v_fma_f32 v34, -v72, v86, 1.0
	v_fmac_f32_e32 v86, v34, v86
	v_div_scale_f32 v34, vcc, v129, v35, v129
	v_mul_f32_e32 v81, v34, v86
	v_fma_f32 v85, -v72, v81, v34
	v_fmac_f32_e32 v81, v85, v86
	v_fma_f32 v34, -v72, v81, v34
	v_div_fmas_f32 v34, v34, v86, v81
	v_div_fixup_f32 v34, v34, v35, v129
	v_mul_f32_e32 v35, v34, v71
	v_fma_f32 v71, v73, v24, -v35
	v_mul_f32_e32 v35, v34, v83
	v_fma_f32 v57, v57, v24, -v35
	v_mul_f32_e32 v72, v57, v57
	v_mul_f32_e32 v35, v34, v87
	v_fmac_f32_e32 v72, v71, v71
	v_fma_f32 v41, v41, v24, -v35
	v_mul_f32_e32 v34, v34, v97
	v_fmac_f32_e32 v72, v41, v41
	v_fma_f32 v73, v25, v24, -v34
	v_fmac_f32_e32 v72, v73, v73
	s_nop 1
	v_mov_b32_dpp v81, v72 quad_perm:[1,0,3,2] row_mask:0xf bank_mask:0xf
	v_lshl_add_u64 v[24:25], s[18:19], 0, v[68:69]
	v_lshl_add_u64 v[24:25], v[24:25], 0, s[38:39]
	v_lshl_add_u64 v[24:25], v[24:25], 0, v[130:131]
	v_mul_f32_e32 v70, v80, v70
	s_waitcnt lgkmcnt(0)
	v_add_f32_e32 v68, v72, v81
	s_nop 1
	v_mov_b32_dpp v69, v68 quad_perm:[2,3,0,1] row_mask:0xf bank_mask:0xf
	v_lshl_add_u64 v[34:35], v[24:25], 0, s[30:31]
	v_bfe_u32 v72, v70, 16, 1
	v_add_co_u32_e32 v24, vcc, s74, v24
	s_waitcnt lgkmcnt(0)
	v_add_f32_e32 v68, v68, v69
	s_nop 1
	v_mov_b32_dpp v69, v68 row_half_mirror row_mask:0xf bank_mask:0xf
	v_add3_u32 v70, v70, v72, s73
	v_addc_co_u32_e32 v25, vcc, 0, v25, vcc
	global_store_short_d16_hi v[24:25], v70, off offset:1024
	s_waitcnt lgkmcnt(0)
	v_add_f32_e32 v25, v68, v69
	v_mul_f32_e32 v24, v56, v84
	s_nop 1
	v_mov_b32_dpp v56, v25 row_ror:8 row_mask:0xf bank_mask:0xf
	v_mul_f32_e32 v24, v94, v24
	v_bfe_u32 v68, v24, 16, 1
	v_add3_u32 v24, v24, v68, s73
	global_store_short_d16_hi v[34:35], v24, off offset:64
	s_waitcnt lgkmcnt(0)
	v_add_f32_e32 v24, v25, v56
	v_mov_b32_e32 v25, v24
	s_nop 1
	v_permlane16_swap_b32_e32 v24, v25
	v_mul_f32_e32 v40, v40, v84
	v_mul_f32_e32 v40, v120, v40
	v_bfe_u32 v56, v40, 16, 1
	v_add3_u32 v40, v40, v56, s73
	s_waitcnt lgkmcnt(0)
	v_add_f32_e32 v24, v24, v25
	v_fmamk_f32 v24, v24, 0x3c000000, v190
	v_mul_f32_e32 v25, 0x4f800000, v24
	v_cmp_gt_f32_e32 vcc, s71, v24
	global_store_short_d16_hi v[34:35], v40, off offset:128
	v_mul_f32_e32 v40, v82, v84
	v_cndmask_b32_e32 v24, v24, v25, vcc
	v_sqrt_f32_e32 v25, v24
	v_mul_f32_e32 v40, v121, v40
	v_add_u32_e32 v56, -1, v25
	v_fma_f32 v68, -v56, v25, v24
	v_cmp_ge_f32_e64 s[16:17], 0, v68
	v_add_u32_e32 v68, 1, v25
	s_nop 0
	v_cndmask_b32_e64 v56, v25, v56, s[16:17]
	v_fma_f32 v25, -v68, v25, v24
	v_cmp_lt_f32_e64 s[16:17], 0, v25
	s_nop 1
	v_cndmask_b32_e64 v25, v56, v68, s[16:17]
	v_mul_f32_e32 v56, 0x37800000, v25
	v_cndmask_b32_e32 v25, v25, v56, vcc
	v_cmp_class_f32_e32 vcc, v24, v191
	v_bfe_u32 v68, v40, 16, 1
	v_add3_u32 v40, v40, v68, s73
	v_cndmask_b32_e32 v24, v25, v24, vcc
	v_div_scale_f32 v25, s[16:17], v24, v24, s72
	v_rcp_f32_e32 v56, v25
	global_store_short_d16_hi v[34:35], v40, off offset:192
	v_fma_f32 v34, -v25, v56, 1.0
	v_fmac_f32_e32 v56, v34, v56
	v_div_scale_f32 v34, vcc, s72, v24, s72
	v_mul_f32_e32 v35, v34, v56
	v_fma_f32 v40, -v25, v35, v34
	v_fmac_f32_e32 v35, v40, v56
	v_fma_f32 v25, -v25, v35, v34
	v_div_scale_f32 v34, s[16:17], v92, v92, 1.0
	v_div_fmas_f32 v25, v25, v56, v35
	v_rcp_f32_e32 v35, v34
	v_div_fixup_f32 v40, v25, v24, s72
	v_lshl_add_u64 v[24:25], s[36:37], 0, v[154:155]
	v_lshlrev_b64 v[24:25], 12, v[24:25]
	v_fma_f32 v56, -v34, v35, 1.0
	v_fmac_f32_e32 v35, v56, v35
	v_div_scale_f32 v56, vcc, 1.0, v92, 1.0
	v_mul_f32_e32 v68, v56, v35
	v_fma_f32 v69, -v34, v68, v56
	v_fmac_f32_e32 v68, v69, v35
	v_fma_f32 v34, -v34, v68, v56
	v_div_scale_f32 v56, s[16:17], v16, v16, v129
	v_rcp_f32_e32 v69, v56
	v_div_fmas_f32 v34, v34, v35, v68
	v_div_fixup_f32 v34, v34, v92, 1.0
	v_lshl_add_u64 v[24:25], s[18:19], 0, v[24:25]
	v_fma_f32 v35, -v56, v69, 1.0
	v_fmac_f32_e32 v69, v35, v69
	v_div_scale_f32 v35, vcc, v129, v16, v129
	v_mul_f32_e32 v68, v35, v69
	v_fma_f32 v70, -v56, v68, v35
	v_fmac_f32_e32 v68, v70, v69
	v_fma_f32 v35, -v56, v68, v35
	v_div_fmas_f32 v35, v35, v69, v68
	v_div_fixup_f32 v16, v35, v16, v129
	v_mul_f32_e32 v35, v16, v52
	v_fma_f32 v52, v74, v34, -v35
	v_mul_f32_e32 v35, v16, v54
	v_fma_f32 v54, v58, v34, -v35
	v_mul_f32_e32 v56, v54, v54
	v_mul_f32_e32 v35, v16, v64
	v_fmac_f32_e32 v56, v52, v52
	v_fma_f32 v42, v42, v34, -v35
	v_mul_f32_e32 v16, v16, v66
	v_fmac_f32_e32 v56, v42, v42
	v_fma_f32 v26, v26, v34, -v16
	v_fmac_f32_e32 v56, v26, v26
	s_nop 1
	v_mov_b32_dpp v16, v56 quad_perm:[1,0,3,2] row_mask:0xf bank_mask:0xf
	v_lshl_add_u64 v[24:25], v[24:25], 0, s[38:39]
	v_mul_f32_e32 v58, v71, v40
	v_lshl_add_u64 v[24:25], v[24:25], 0, v[130:131]
	v_mul_f32_e32 v58, v80, v58
	s_waitcnt lgkmcnt(0)
	v_add_f32_e32 v16, v56, v16
	s_nop 1
	v_mov_b32_dpp v56, v16 quad_perm:[2,3,0,1] row_mask:0xf bank_mask:0xf
	v_lshl_add_u64 v[34:35], v[24:25], 0, s[30:31]
	v_bfe_u32 v64, v58, 16, 1
	v_add_co_u32_e32 v24, vcc, s74, v24
	s_waitcnt lgkmcnt(0)
	v_add_f32_e32 v16, v16, v56
	s_nop 1
	v_mov_b32_dpp v56, v16 row_half_mirror row_mask:0xf bank_mask:0xf
	v_add3_u32 v58, v58, v64, s73
	v_addc_co_u32_e32 v25, vcc, 0, v25, vcc
	global_store_short_d16_hi v[24:25], v58, off offset:1024
	s_waitcnt lgkmcnt(0)
	v_add_f32_e32 v16, v16, v56
	s_nop 1
	v_mov_b32_dpp v25, v16 row_ror:8 row_mask:0xf bank_mask:0xf
	v_mul_f32_e32 v24, v57, v40
	v_mul_f32_e32 v24, v94, v24
	v_bfe_u32 v56, v24, 16, 1
	v_add3_u32 v24, v24, v56, s73
	s_waitcnt lgkmcnt(0)
	v_add_f32_e32 v16, v16, v25
	global_store_short_d16_hi v[34:35], v24, off offset:64
	v_mov_b32_e32 v24, v16
	s_nop 1
	v_permlane16_swap_b32_e32 v16, v24
	v_mul_f32_e32 v25, v41, v40
	v_mul_f32_e32 v25, v120, v25
	v_bfe_u32 v41, v25, 16, 1
	v_add3_u32 v25, v25, v41, s73
	s_waitcnt lgkmcnt(0)
	v_add_f32_e32 v16, v16, v24
	v_fmamk_f32 v16, v16, 0x3c000000, v190
	v_mul_f32_e32 v24, 0x4f800000, v16
	v_cmp_gt_f32_e32 vcc, s71, v16
	global_store_short_d16_hi v[34:35], v25, off offset:128
	v_mul_f32_e32 v25, v73, v40
	v_cndmask_b32_e32 v16, v16, v24, vcc
	v_sqrt_f32_e32 v24, v16
	v_mul_f32_e32 v25, v121, v25
	v_add_u32_e32 v40, -1, v24
	v_fma_f32 v41, -v40, v24, v16
	v_cmp_ge_f32_e64 s[16:17], 0, v41
	v_add_u32_e32 v41, 1, v24
	s_nop 0
	v_cndmask_b32_e64 v40, v24, v40, s[16:17]
	v_fma_f32 v24, -v41, v24, v16
	v_cmp_lt_f32_e64 s[16:17], 0, v24
	s_nop 1
	v_cndmask_b32_e64 v24, v40, v41, s[16:17]
	v_mul_f32_e32 v40, 0x37800000, v24
	v_cndmask_b32_e32 v24, v24, v40, vcc
	v_cmp_class_f32_e32 vcc, v16, v191
	v_bfe_u32 v41, v25, 16, 1
	v_add3_u32 v25, v25, v41, s73
	v_cndmask_b32_e32 v16, v24, v16, vcc
	v_div_scale_f32 v24, s[16:17], v16, v16, s72
	v_rcp_f32_e32 v40, v24
	global_store_short_d16_hi v[34:35], v25, off offset:192
	v_fma_f32 v25, -v24, v40, 1.0
	v_fmac_f32_e32 v40, v25, v40
	v_div_scale_f32 v25, vcc, s72, v16, s72
	v_mul_f32_e32 v34, v25, v40
	v_fma_f32 v35, -v24, v34, v25
	v_fmac_f32_e32 v34, v35, v40
	v_fma_f32 v24, -v24, v34, v25
	v_div_fmas_f32 v24, v24, v40, v34
	v_div_scale_f32 v34, s[16:17], v93, v93, 1.0
	v_rcp_f32_e32 v35, v34
	v_div_fixup_f32 v40, v24, v16, s72
	v_lshl_add_u64 v[24:25], s[36:37], 0, v[156:157]
	v_lshlrev_b64 v[24:25], 12, v[24:25]
	v_fma_f32 v16, -v34, v35, 1.0
	v_fmac_f32_e32 v35, v16, v35
	v_div_scale_f32 v16, vcc, 1.0, v93, 1.0
	v_mul_f32_e32 v41, v16, v35
	v_fma_f32 v56, -v34, v41, v16
	v_fmac_f32_e32 v41, v56, v35
	v_fma_f32 v16, -v34, v41, v16
	v_div_scale_f32 v34, s[16:17], v17, v17, v129
	v_rcp_f32_e32 v56, v34
	v_div_fmas_f32 v16, v16, v35, v41
	v_div_fixup_f32 v16, v16, v93, 1.0
	v_mul_f32_e32 v26, v26, v40
	v_fma_f32 v35, -v34, v56, 1.0
	v_fmac_f32_e32 v56, v35, v56
	v_div_scale_f32 v35, vcc, v129, v17, v129
	v_mul_f32_e32 v41, v35, v56
	v_fma_f32 v57, -v34, v41, v35
	v_fmac_f32_e32 v41, v57, v56
	v_fma_f32 v34, -v34, v41, v35
	v_div_fmas_f32 v34, v34, v56, v41
	v_div_fixup_f32 v17, v34, v17, v129
	v_mul_f32_e32 v34, v17, v53
	v_fma_f32 v41, v75, v16, -v34
	v_mul_f32_e32 v34, v17, v55
	v_fma_f32 v53, v59, v16, -v34
	v_mul_f32_e32 v34, v53, v53
	v_mul_f32_e32 v35, v17, v65
	v_fmac_f32_e32 v34, v41, v41
	v_fma_f32 v43, v43, v16, -v35
	v_mul_f32_e32 v17, v17, v67
	v_fmac_f32_e32 v34, v43, v43
	v_fma_f32 v55, v27, v16, -v17
	v_fmac_f32_e32 v34, v55, v55
	s_nop 1
	v_mov_b32_dpp v27, v34 quad_perm:[1,0,3,2] row_mask:0xf bank_mask:0xf
	v_lshl_add_u64 v[16:17], s[18:19], 0, v[24:25]
	v_lshl_add_u64 v[16:17], v[16:17], 0, s[38:39]
	v_mul_f32_e32 v35, v52, v40
	v_lshl_add_u64 v[16:17], v[16:17], 0, v[130:131]
	s_waitcnt lgkmcnt(0)
	v_add_f32_e32 v27, v34, v27
	s_nop 1
	v_mov_b32_dpp v34, v27 quad_perm:[2,3,0,1] row_mask:0xf bank_mask:0xf
	v_mul_f32_e32 v35, v80, v35
	v_lshl_add_u64 v[24:25], v[16:17], 0, s[30:31]
	v_bfe_u32 v52, v35, 16, 1
	v_add_co_u32_e32 v16, vcc, s74, v16
	s_waitcnt lgkmcnt(0)
	v_add_f32_e32 v27, v27, v34
	s_nop 1
	v_mov_b32_dpp v34, v27 row_half_mirror row_mask:0xf bank_mask:0xf
	v_add3_u32 v35, v35, v52, s73
	v_addc_co_u32_e32 v17, vcc, 0, v17, vcc
	global_store_short_d16_hi v[16:17], v35, off offset:1024
	s_waitcnt lgkmcnt(0)
	v_add_f32_e32 v17, v27, v34
	s_nop 1
	v_mov_b32_dpp v27, v17 row_ror:8 row_mask:0xf bank_mask:0xf
	v_mul_f32_e32 v16, v54, v40
	v_mul_f32_e32 v16, v94, v16
	v_bfe_u32 v34, v16, 16, 1
	v_add3_u32 v16, v16, v34, s73
	global_store_short_d16_hi v[24:25], v16, off offset:64
	s_waitcnt lgkmcnt(0)
	v_add_f32_e32 v16, v17, v27
	v_mov_b32_e32 v17, v16
	s_nop 1
	v_permlane16_swap_b32_e32 v16, v17
	v_mul_f32_e32 v27, v42, v40
	v_mul_f32_e32 v27, v120, v27
	v_bfe_u32 v34, v27, 16, 1
	v_add3_u32 v27, v27, v34, s73
	s_waitcnt lgkmcnt(0)
	v_add_f32_e32 v16, v16, v17
	v_fmamk_f32 v16, v16, 0x3c000000, v190
	v_mul_f32_e32 v17, 0x4f800000, v16
	v_cmp_gt_f32_e32 vcc, s71, v16
	global_store_short_d16_hi v[24:25], v27, off offset:128
	v_mul_f32_e32 v26, v121, v26
	v_cndmask_b32_e32 v16, v16, v17, vcc
	v_sqrt_f32_e32 v17, v16
	s_nop 0
	v_add_u32_e32 v27, -1, v17
	v_fma_f32 v34, -v27, v17, v16
	v_cmp_ge_f32_e64 s[16:17], 0, v34
	v_add_u32_e32 v34, 1, v17
	s_nop 0
	v_cndmask_b32_e64 v27, v17, v27, s[16:17]
	v_fma_f32 v17, -v34, v17, v16
	v_cmp_lt_f32_e64 s[16:17], 0, v17
	s_nop 1
	v_cndmask_b32_e64 v17, v27, v34, s[16:17]
	v_mul_f32_e32 v27, 0x37800000, v17
	v_cndmask_b32_e32 v17, v17, v27, vcc
	v_cmp_class_f32_e32 vcc, v16, v191
	v_bfe_u32 v34, v26, 16, 1
	v_add3_u32 v26, v26, v34, s73
	v_cndmask_b32_e32 v16, v17, v16, vcc
	v_div_scale_f32 v17, s[16:17], v16, v16, s72
	v_rcp_f32_e32 v27, v17
	global_store_short_d16_hi v[24:25], v26, off offset:192
	v_div_scale_f32 v34, s[16:17], v90, v90, 1.0
	v_fma_f32 v24, -v17, v27, 1.0
	v_fmac_f32_e32 v27, v24, v27
	v_div_scale_f32 v24, vcc, s72, v16, s72
	v_mul_f32_e32 v25, v24, v27
	v_fma_f32 v26, -v17, v25, v24
	v_fmac_f32_e32 v25, v26, v27
	v_rcp_f32_e32 v35, v34
	v_fma_f32 v17, -v17, v25, v24
	v_div_fmas_f32 v17, v17, v27, v25
	v_div_fixup_f32 v40, v17, v16, s72
	v_lshl_add_u64 v[16:17], s[36:37], 0, v[158:159]
	v_lshlrev_b64 v[24:25], 12, v[16:17]
	v_fma_f32 v16, -v34, v35, 1.0
	ds_read2_b32 v[26:27], v186 offset0:24 offset1:25
	v_fmac_f32_e32 v35, v16, v35
	v_div_scale_f32 v16, vcc, 1.0, v90, 1.0
	v_mul_f32_e32 v42, v16, v35
	v_fma_f32 v17, -v34, v42, v16
	v_fmac_f32_e32 v42, v17, v35
	v_fma_f32 v34, -v34, v42, v16
	ds_read2_b32 v[16:17], v186 offset0:26 offset1:27
	s_waitcnt lgkmcnt(1)
	v_div_scale_f32 v52, s[16:17], v26, v26, v129
	v_rcp_f32_e32 v54, v52
	v_div_fmas_f32 v34, v34, v35, v42
	v_div_fixup_f32 v34, v34, v90, 1.0
	v_lshl_add_u64 v[24:25], s[18:19], 0, v[24:25]
	v_fma_f32 v35, -v52, v54, 1.0
	v_fmac_f32_e32 v54, v35, v54
	v_div_scale_f32 v35, vcc, v129, v26, v129
	v_mul_f32_e32 v42, v35, v54
	v_fma_f32 v56, -v52, v42, v35
	v_fmac_f32_e32 v42, v56, v54
	v_fma_f32 v35, -v52, v42, v35
	v_div_fmas_f32 v35, v35, v54, v42
	v_div_fixup_f32 v26, v35, v26, v129
	v_mul_f32_e32 v35, v26, v36
	v_fma_f32 v36, v76, v34, -v35
	v_mul_f32_e32 v35, v26, v38
	v_fma_f32 v38, v60, v34, -v35
	v_mul_f32_e32 v42, v38, v38
	v_mul_f32_e32 v35, v26, v48
	v_fmac_f32_e32 v42, v36, v36
	v_fma_f32 v44, v44, v34, -v35
	v_mul_f32_e32 v26, v26, v50
	v_fmac_f32_e32 v42, v44, v44
	v_fma_f32 v28, v28, v34, -v26
	v_fmac_f32_e32 v42, v28, v28
	s_nop 1
	v_mov_b32_dpp v26, v42 quad_perm:[1,0,3,2] row_mask:0xf bank_mask:0xf
	v_lshl_add_u64 v[24:25], v[24:25], 0, s[38:39]
	v_mul_f32_e32 v41, v41, v40
	v_lshl_add_u64 v[24:25], v[24:25], 0, v[130:131]
	v_mul_f32_e32 v41, v80, v41
	s_waitcnt lgkmcnt(0)
	v_add_f32_e32 v26, v42, v26
	s_nop 1
	v_mov_b32_dpp v42, v26 quad_perm:[2,3,0,1] row_mask:0xf bank_mask:0xf
	v_lshl_add_u64 v[34:35], v[24:25], 0, s[30:31]
	v_bfe_u32 v48, v41, 16, 1
	v_add_co_u32_e32 v24, vcc, s74, v24
	s_waitcnt lgkmcnt(0)
	v_add_f32_e32 v26, v26, v42
	s_nop 1
	v_mov_b32_dpp v42, v26 row_half_mirror row_mask:0xf bank_mask:0xf
	v_add3_u32 v41, v41, v48, s73
	v_addc_co_u32_e32 v25, vcc, 0, v25, vcc
	global_store_short_d16_hi v[24:25], v41, off offset:1024
	s_waitcnt lgkmcnt(0)
	v_add_f32_e32 v25, v26, v42
	s_nop 1
	v_mov_b32_dpp v26, v25 row_ror:8 row_mask:0xf bank_mask:0xf
	v_mul_f32_e32 v24, v53, v40
	v_mul_f32_e32 v24, v94, v24
	v_bfe_u32 v41, v24, 16, 1
	v_add3_u32 v24, v24, v41, s73
	global_store_short_d16_hi v[34:35], v24, off offset:64
	s_waitcnt lgkmcnt(0)
	v_add_f32_e32 v24, v25, v26
	v_mov_b32_e32 v25, v24
	s_nop 1
	v_permlane16_swap_b32_e32 v24, v25
	v_mul_f32_e32 v26, v43, v40
	v_mul_f32_e32 v26, v120, v26
	v_bfe_u32 v41, v26, 16, 1
	v_add3_u32 v26, v26, v41, s73
	s_waitcnt lgkmcnt(0)
	v_add_f32_e32 v24, v24, v25
	v_fmamk_f32 v24, v24, 0x3c000000, v190
	v_mul_f32_e32 v25, 0x4f800000, v24
	v_cmp_gt_f32_e32 vcc, s71, v24
	global_store_short_d16_hi v[34:35], v26, off offset:128
	v_mul_f32_e32 v26, v55, v40
	v_cndmask_b32_e32 v24, v24, v25, vcc
	v_sqrt_f32_e32 v25, v24
	v_mul_f32_e32 v26, v121, v26
	v_add_u32_e32 v40, -1, v25
	v_fma_f32 v41, -v40, v25, v24
	v_cmp_ge_f32_e64 s[16:17], 0, v41
	v_add_u32_e32 v41, 1, v25
	s_nop 0
	v_cndmask_b32_e64 v40, v25, v40, s[16:17]
	v_fma_f32 v25, -v41, v25, v24
	v_cmp_lt_f32_e64 s[16:17], 0, v25
	s_nop 1
	v_cndmask_b32_e64 v25, v40, v41, s[16:17]
	v_mul_f32_e32 v40, 0x37800000, v25
	v_cndmask_b32_e32 v25, v25, v40, vcc
	v_cmp_class_f32_e32 vcc, v24, v191
	v_bfe_u32 v41, v26, 16, 1
	v_add3_u32 v26, v26, v41, s73
	v_cndmask_b32_e32 v24, v25, v24, vcc
	v_div_scale_f32 v25, s[16:17], v24, v24, s72
	v_rcp_f32_e32 v40, v25
	global_store_short_d16_hi v[34:35], v26, off offset:192
	v_fma_f32 v26, -v25, v40, 1.0
	v_fmac_f32_e32 v40, v26, v40
	v_div_scale_f32 v26, vcc, s72, v24, s72
	v_mul_f32_e32 v34, v26, v40
	v_fma_f32 v35, -v25, v34, v26
	v_fmac_f32_e32 v34, v35, v40
	v_fma_f32 v25, -v25, v34, v26
	v_div_scale_f32 v26, s[16:17], v91, v91, 1.0
	v_div_fmas_f32 v25, v25, v40, v34
	v_rcp_f32_e32 v34, v26
	v_div_fixup_f32 v35, v25, v24, s72
	v_lshl_add_u64 v[24:25], s[36:37], 0, v[160:161]
	v_lshlrev_b64 v[24:25], 12, v[24:25]
	v_fma_f32 v40, -v26, v34, 1.0
	v_fmac_f32_e32 v34, v40, v34
	v_div_scale_f32 v40, vcc, 1.0, v91, 1.0
	v_mul_f32_e32 v41, v40, v34
	v_fma_f32 v42, -v26, v41, v40
	v_fmac_f32_e32 v41, v42, v34
	v_fma_f32 v26, -v26, v41, v40
	v_div_scale_f32 v40, s[16:17], v27, v27, v129
	v_rcp_f32_e32 v42, v40
	v_div_fmas_f32 v26, v26, v34, v41
	v_div_fixup_f32 v26, v26, v91, 1.0
	v_lshl_add_u64 v[24:25], s[18:19], 0, v[24:25]
	v_fma_f32 v34, -v40, v42, 1.0
	v_fmac_f32_e32 v42, v34, v42
	v_div_scale_f32 v34, vcc, v129, v27, v129
	v_mul_f32_e32 v41, v34, v42
	v_fma_f32 v43, -v40, v41, v34
	v_fmac_f32_e32 v41, v43, v42
	v_fma_f32 v34, -v40, v41, v34
	v_div_fmas_f32 v34, v34, v42, v41
	v_div_fixup_f32 v27, v34, v27, v129
	v_mul_f32_e32 v34, v27, v37
	v_mul_f32_e32 v37, v27, v39
	v_fma_f32 v37, v61, v26, -v37
	v_fma_f32 v34, v77, v26, -v34
	v_mul_f32_e32 v39, v37, v37
	v_mul_f32_e32 v40, v27, v49
	v_fmac_f32_e32 v39, v34, v34
	v_fma_f32 v40, v45, v26, -v40
	v_mul_f32_e32 v27, v27, v51
	v_fmac_f32_e32 v39, v40, v40
	v_fma_f32 v29, v29, v26, -v27
	v_fmac_f32_e32 v39, v29, v29
	s_nop 1
	v_mov_b32_dpp v41, v39 quad_perm:[1,0,3,2] row_mask:0xf bank_mask:0xf
	v_lshl_add_u64 v[24:25], v[24:25], 0, s[38:39]
	v_mul_f32_e32 v36, v36, v35
	v_lshl_add_u64 v[24:25], v[24:25], 0, v[130:131]
	v_mul_f32_e32 v36, v80, v36
	s_waitcnt lgkmcnt(0)
	v_add_f32_e32 v39, v39, v41
	s_nop 1
	v_mov_b32_dpp v41, v39 quad_perm:[2,3,0,1] row_mask:0xf bank_mask:0xf
	v_lshl_add_u64 v[26:27], v[24:25], 0, s[30:31]
	v_bfe_u32 v42, v36, 16, 1
	v_add_co_u32_e32 v24, vcc, s74, v24
	s_waitcnt lgkmcnt(0)
	v_add_f32_e32 v39, v39, v41
	s_nop 1
	v_mov_b32_dpp v41, v39 row_half_mirror row_mask:0xf bank_mask:0xf
	v_add3_u32 v36, v36, v42, s73
	v_addc_co_u32_e32 v25, vcc, 0, v25, vcc
	global_store_short_d16_hi v[24:25], v36, off offset:1024
	s_waitcnt lgkmcnt(0)
	v_add_f32_e32 v25, v39, v41
	s_nop 1
	v_mov_b32_dpp v36, v25 row_ror:8 row_mask:0xf bank_mask:0xf
	v_mul_f32_e32 v24, v38, v35
	v_mul_f32_e32 v24, v94, v24
	v_bfe_u32 v38, v24, 16, 1
	v_add3_u32 v24, v24, v38, s73
	global_store_short_d16_hi v[26:27], v24, off offset:64
	s_waitcnt lgkmcnt(0)
	v_add_f32_e32 v24, v25, v36
	v_mov_b32_e32 v25, v24
	s_nop 1
	v_permlane16_swap_b32_e32 v24, v25
	v_mul_f32_e32 v36, v44, v35
	v_mul_f32_e32 v36, v120, v36
	v_bfe_u32 v38, v36, 16, 1
	v_add3_u32 v36, v36, v38, s73
	s_waitcnt lgkmcnt(0)
	v_add_f32_e32 v24, v24, v25
	v_fmamk_f32 v24, v24, 0x3c000000, v190
	v_mul_f32_e32 v25, 0x4f800000, v24
	v_cmp_gt_f32_e32 vcc, s71, v24
	v_mul_f32_e32 v28, v28, v35
	global_store_short_d16_hi v[26:27], v36, off offset:128
	v_cndmask_b32_e32 v24, v24, v25, vcc
	v_sqrt_f32_e32 v25, v24
	v_mul_f32_e32 v28, v121, v28
	v_add_u32_e32 v35, -1, v25
	v_fma_f32 v36, -v35, v25, v24
	v_cmp_ge_f32_e64 s[16:17], 0, v36
	v_add_u32_e32 v36, 1, v25
	s_nop 0
	v_cndmask_b32_e64 v35, v25, v35, s[16:17]
	v_fma_f32 v25, -v36, v25, v24
	v_cmp_lt_f32_e64 s[16:17], 0, v25
	s_nop 1
	v_cndmask_b32_e64 v25, v35, v36, s[16:17]
	v_mul_f32_e32 v35, 0x37800000, v25
	v_cndmask_b32_e32 v25, v25, v35, vcc
	v_cmp_class_f32_e32 vcc, v24, v191
	v_bfe_u32 v36, v28, 16, 1
	v_add3_u32 v28, v28, v36, s73
	v_cndmask_b32_e32 v24, v25, v24, vcc
	v_div_scale_f32 v25, s[16:17], v24, v24, s72
	v_rcp_f32_e32 v35, v25
	global_store_short_d16_hi v[26:27], v28, off offset:192
	v_fma_f32 v26, -v25, v35, 1.0
	v_fmac_f32_e32 v35, v26, v35
	v_div_scale_f32 v26, vcc, s72, v24, s72
	v_mul_f32_e32 v27, v26, v35
	v_fma_f32 v28, -v25, v27, v26
	v_fmac_f32_e32 v27, v28, v35
	v_fma_f32 v25, -v25, v27, v26
	v_div_scale_f32 v26, s[16:17], v88, v88, 1.0
	v_div_fmas_f32 v25, v25, v35, v27
	v_rcp_f32_e32 v27, v26
	v_div_fixup_f32 v28, v25, v24, s72
	v_lshl_add_u64 v[24:25], s[36:37], 0, v[162:163]
	v_lshlrev_b64 v[24:25], 12, v[24:25]
	v_fma_f32 v35, -v26, v27, 1.0
	v_fmac_f32_e32 v27, v35, v27
	v_div_scale_f32 v35, vcc, 1.0, v88, 1.0
	v_mul_f32_e32 v36, v35, v27
	v_fma_f32 v38, -v26, v36, v35
	v_fmac_f32_e32 v36, v38, v27
	v_fma_f32 v26, -v26, v36, v35
	v_div_scale_f32 v35, s[16:17], v16, v16, v129
	v_rcp_f32_e32 v38, v35
	v_div_fmas_f32 v26, v26, v27, v36
	v_div_fixup_f32 v26, v26, v88, 1.0
	v_lshl_add_u64 v[24:25], s[18:19], 0, v[24:25]
	v_fma_f32 v27, -v35, v38, 1.0
	v_fmac_f32_e32 v38, v27, v38
	v_div_scale_f32 v27, vcc, v129, v16, v129
	v_mul_f32_e32 v36, v27, v38
	v_fma_f32 v39, -v35, v36, v27
	v_fmac_f32_e32 v36, v39, v38
	v_fma_f32 v27, -v35, v36, v27
	v_div_fmas_f32 v27, v27, v38, v36
	v_div_fixup_f32 v16, v27, v16, v129
	v_mul_f32_e32 v18, v16, v18
	v_fma_f32 v35, v78, v26, -v18
	v_mul_f32_e32 v18, v16, v20
	v_fma_f32 v20, v62, v26, -v18
	v_mul_f32_e32 v18, v20, v20
	v_mul_f32_e32 v22, v16, v22
	v_fmac_f32_e32 v18, v35, v35
	v_fma_f32 v22, v46, v26, -v22
	v_mul_f32_e32 v16, v16, v32
	v_fmac_f32_e32 v18, v22, v22
	v_fma_f32 v30, v30, v26, -v16
	v_fmac_f32_e32 v18, v30, v30
	s_nop 1
	v_mov_b32_dpp v16, v18 quad_perm:[1,0,3,2] row_mask:0xf bank_mask:0xf
	v_lshl_add_u64 v[24:25], v[24:25], 0, s[38:39]
	v_mul_f32_e32 v32, v34, v28
	v_lshl_add_u64 v[24:25], v[24:25], 0, v[130:131]
	v_mul_f32_e32 v32, v80, v32
	s_waitcnt lgkmcnt(0)
	v_add_f32_e32 v16, v18, v16
	s_nop 1
	v_mov_b32_dpp v18, v16 quad_perm:[2,3,0,1] row_mask:0xf bank_mask:0xf
	v_lshl_add_u64 v[26:27], v[24:25], 0, s[30:31]
	v_bfe_u32 v34, v32, 16, 1
	v_add_co_u32_e32 v24, vcc, s74, v24
	s_waitcnt lgkmcnt(0)
	v_add_f32_e32 v16, v16, v18
	s_nop 1
	v_mov_b32_dpp v18, v16 row_half_mirror row_mask:0xf bank_mask:0xf
	v_add3_u32 v32, v32, v34, s73
	v_addc_co_u32_e32 v25, vcc, 0, v25, vcc
	global_store_short_d16_hi v[24:25], v32, off offset:1024
	s_waitcnt lgkmcnt(0)
	v_add_f32_e32 v16, v16, v18
	s_nop 1
	v_mov_b32_dpp v18, v16 row_ror:8 row_mask:0xf bank_mask:0xf
	v_mul_f32_e32 v24, v37, v28
	v_mul_f32_e32 v24, v94, v24
	v_bfe_u32 v25, v24, 16, 1
	v_add3_u32 v24, v24, v25, s73
	s_waitcnt lgkmcnt(0)
	v_add_f32_e32 v16, v16, v18
	v_mov_b32_e32 v18, v16
	s_nop 1
	v_permlane16_swap_b32_e32 v16, v18
	global_store_short_d16_hi v[26:27], v24, off offset:64
	v_mul_f32_e32 v24, v40, v28
	v_mul_f32_e32 v24, v120, v24
	v_bfe_u32 v25, v24, 16, 1
	s_waitcnt lgkmcnt(0)
	v_add_f32_e32 v16, v16, v18
	v_fmamk_f32 v16, v16, 0x3c000000, v190
	v_mul_f32_e32 v18, 0x4f800000, v16
	v_cmp_gt_f32_e32 vcc, s71, v16
	v_add3_u32 v24, v24, v25, s73
	global_store_short_d16_hi v[26:27], v24, off offset:128
	v_cndmask_b32_e32 v16, v16, v18, vcc
	v_sqrt_f32_e32 v18, v16
	v_mul_f32_e32 v24, v29, v28
	v_mul_f32_e32 v24, v121, v24
	v_add_u32_e32 v25, -1, v18
	v_fma_f32 v28, -v25, v18, v16
	v_cmp_ge_f32_e64 s[16:17], 0, v28
	v_add_u32_e32 v28, 1, v18
	s_nop 0
	v_cndmask_b32_e64 v25, v18, v25, s[16:17]
	v_fma_f32 v18, -v28, v18, v16
	v_cmp_lt_f32_e64 s[16:17], 0, v18
	s_nop 1
	v_cndmask_b32_e64 v18, v25, v28, s[16:17]
	v_mul_f32_e32 v25, 0x37800000, v18
	v_cndmask_b32_e32 v18, v18, v25, vcc
	v_cmp_class_f32_e32 vcc, v16, v191
	v_bfe_u32 v28, v24, 16, 1
	v_add3_u32 v24, v24, v28, s73
	v_cndmask_b32_e32 v16, v18, v16, vcc
	v_div_scale_f32 v18, s[16:17], v16, v16, s72
	v_rcp_f32_e32 v25, v18
	global_store_short_d16_hi v[26:27], v24, off offset:192
	v_fma_f32 v24, -v18, v25, 1.0
	v_fmac_f32_e32 v25, v24, v25
	v_div_scale_f32 v24, vcc, s72, v16, s72
	v_mul_f32_e32 v26, v24, v25
	v_fma_f32 v27, -v18, v26, v24
	v_fmac_f32_e32 v26, v27, v25
	v_fma_f32 v18, -v18, v26, v24
	v_div_fmas_f32 v18, v18, v25, v26
	v_div_scale_f32 v26, s[16:17], v89, v89, 1.0
	v_rcp_f32_e32 v27, v26
	v_div_fixup_f32 v28, v18, v16, s72
	v_lshl_add_u64 v[24:25], s[36:37], 0, v[164:165]
	v_lshlrev_b64 v[24:25], 12, v[24:25]
	v_fma_f32 v16, -v26, v27, 1.0
	v_fmac_f32_e32 v27, v16, v27
	v_div_scale_f32 v16, vcc, 1.0, v89, 1.0
	v_mul_f32_e32 v18, v16, v27
	v_fma_f32 v29, -v26, v18, v16
	v_fmac_f32_e32 v18, v29, v27
	v_fma_f32 v16, -v26, v18, v16
	v_div_scale_f32 v26, s[16:17], v17, v17, v129
	v_rcp_f32_e32 v29, v26
	v_div_fmas_f32 v16, v16, v27, v18
	v_div_fixup_f32 v16, v16, v89, 1.0
	v_fma_f32 v18, -v26, v29, 1.0
	v_fmac_f32_e32 v29, v18, v29
	v_div_scale_f32 v18, vcc, v129, v17, v129
	v_mul_f32_e32 v27, v18, v29
	v_fma_f32 v32, -v26, v27, v18
	v_fmac_f32_e32 v27, v32, v29
	v_fma_f32 v18, -v26, v27, v18
	v_div_fmas_f32 v18, v18, v29, v27
	v_div_fixup_f32 v17, v18, v17, v129
	v_mul_f32_e32 v18, v17, v19
	v_fma_f32 v26, v79, v16, -v18
	v_mul_f32_e32 v18, v17, v21
	v_fma_f32 v21, v63, v16, -v18
	v_mul_f32_e32 v27, v21, v21
	v_mul_f32_e32 v18, v17, v23
	v_fmac_f32_e32 v27, v26, v26
	v_fma_f32 v23, v47, v16, -v18
	v_mul_f32_e32 v17, v17, v33
	v_fmac_f32_e32 v27, v23, v23
	v_fma_f32 v29, v31, v16, -v17
	v_fmac_f32_e32 v27, v29, v29
	s_nop 1
	v_mov_b32_dpp v31, v27 quad_perm:[1,0,3,2] row_mask:0xf bank_mask:0xf
	v_lshl_add_u64 v[16:17], s[18:19], 0, v[24:25]
	v_lshl_add_u64 v[16:17], v[16:17], 0, s[38:39]
	v_lshl_add_u64 v[16:17], v[16:17], 0, v[130:131]
	v_lshl_add_u64 v[18:19], v[16:17], 0, s[30:31]
	s_waitcnt lgkmcnt(0)
	v_add_f32_e32 v24, v27, v31
	s_nop 1
	v_mov_b32_dpp v25, v24 quad_perm:[2,3,0,1] row_mask:0xf bank_mask:0xf
	v_mul_f32_e32 v27, v35, v28
	v_mul_f32_e32 v27, v80, v27
	v_bfe_u32 v31, v27, 16, 1
	v_add_co_u32_e32 v16, vcc, s74, v16
	s_waitcnt lgkmcnt(0)
	v_add_f32_e32 v24, v24, v25
	s_nop 1
	v_mov_b32_dpp v25, v24 row_half_mirror row_mask:0xf bank_mask:0xf
	v_add3_u32 v27, v27, v31, s73
	v_addc_co_u32_e32 v17, vcc, 0, v17, vcc
	global_store_short_d16_hi v[16:17], v27, off offset:1024
	s_waitcnt lgkmcnt(0)
	v_add_f32_e32 v17, v24, v25
	v_mul_f32_e32 v16, v20, v28
	s_nop 1
	v_mov_b32_dpp v20, v17 row_ror:8 row_mask:0xf bank_mask:0xf
	v_mul_f32_e32 v16, v94, v16
	v_bfe_u32 v24, v16, 16, 1
	v_add3_u32 v16, v16, v24, s73
	global_store_short_d16_hi v[18:19], v16, off offset:64
	s_waitcnt lgkmcnt(0)
	v_add_f32_e32 v16, v17, v20
	v_mov_b32_e32 v17, v16
	s_nop 1
	v_permlane16_swap_b32_e32 v16, v17
	v_mul_f32_e32 v20, v22, v28
	v_mul_f32_e32 v20, v120, v20
	v_bfe_u32 v22, v20, 16, 1
	v_add3_u32 v20, v20, v22, s73
	s_waitcnt lgkmcnt(0)
	v_add_f32_e32 v16, v16, v17
	v_fmamk_f32 v16, v16, 0x3c000000, v190
	v_mul_f32_e32 v17, 0x4f800000, v16
	v_cmp_gt_f32_e32 vcc, s71, v16
	global_store_short_d16_hi v[18:19], v20, off offset:128
	v_mul_f32_e32 v20, v30, v28
	v_cndmask_b32_e32 v16, v16, v17, vcc
	v_sqrt_f32_e32 v17, v16
	v_mul_f32_e32 v20, v121, v20
	v_add_u32_e32 v22, -1, v17
	v_fma_f32 v24, -v22, v17, v16
	v_cmp_ge_f32_e64 s[16:17], 0, v24
	v_add_u32_e32 v24, 1, v17
	s_nop 0
	v_cndmask_b32_e64 v22, v17, v22, s[16:17]
	v_fma_f32 v17, -v24, v17, v16
	v_cmp_lt_f32_e64 s[16:17], 0, v17
	s_nop 1
	v_cndmask_b32_e64 v17, v22, v24, s[16:17]
	v_mul_f32_e32 v22, 0x37800000, v17
	v_cndmask_b32_e32 v17, v17, v22, vcc
	v_cmp_class_f32_e32 vcc, v16, v191
	v_bfe_u32 v24, v20, 16, 1
	v_add3_u32 v20, v20, v24, s73
	v_cndmask_b32_e32 v16, v17, v16, vcc
	v_div_scale_f32 v17, s[16:17], v16, v16, s72
	v_rcp_f32_e32 v22, v17
	global_store_short_d16_hi v[18:19], v20, off offset:192
	v_fma_f32 v18, -v17, v22, 1.0
	v_fmac_f32_e32 v22, v18, v22
	v_div_scale_f32 v18, vcc, s72, v16, s72
	v_mul_f32_e32 v19, v18, v22
	v_fma_f32 v20, -v17, v19, v18
	v_fmac_f32_e32 v19, v20, v22
	v_fma_f32 v17, -v17, v19, v18
	v_div_fmas_f32 v17, v17, v22, v19
	v_div_fixup_f32 v20, v17, v16, s72
	v_lshl_add_u64 v[16:17], s[36:37], 0, v[166:167]
	v_lshlrev_b64 v[16:17], 12, v[16:17]
	v_lshl_add_u64 v[16:17], s[18:19], 0, v[16:17]
	v_lshl_add_u64 v[16:17], v[16:17], 0, s[38:39]
	v_mul_f32_e32 v22, v26, v20
	v_lshl_add_u64 v[16:17], v[16:17], 0, v[130:131]
	v_mul_f32_e32 v22, v80, v22
	v_lshl_add_u64 v[18:19], v[16:17], 0, s[30:31]
	v_bfe_u32 v24, v22, 16, 1
	v_add_co_u32_e32 v16, vcc, s74, v16
	v_add3_u32 v22, v22, v24, s73
	s_nop 0
	v_addc_co_u32_e32 v17, vcc, 0, v17, vcc
	global_store_short_d16_hi v[16:17], v22, off offset:1024
	v_mul_f32_e32 v16, v21, v20
	v_mul_f32_e32 v16, v94, v16
	v_bfe_u32 v17, v16, 16, 1
	v_add3_u32 v16, v16, v17, s73
	global_store_short_d16_hi v[18:19], v16, off offset:64
	v_mul_f32_e32 v16, v23, v20
	v_mul_f32_e32 v16, v120, v16
	v_bfe_u32 v17, v16, 16, 1
	v_add3_u32 v16, v16, v17, s73
	global_store_short_d16_hi v[18:19], v16, off offset:128
	v_mul_f32_e32 v16, v29, v20
	v_mul_f32_e32 v16, v121, v16
	v_bfe_u32 v17, v16, 16, 1
	v_add3_u32 v16, v16, v17, s73
	global_store_short_d16_hi v[18:19], v16, off offset:192
	s_branch .LBB0_1886
